# v2 + nt policy on P0 streaming loads and small weight transposer loads
# baseline (speedup 1.0000x reference)
.LBB0_9:
	s_lshl_b32 s6, s2, 6
	s_ashr_i32 s7, s6, 31
	s_lshl_b64 s[6:7], s[6:7], 2
	s_add_u32 s42, s52, s6
	s_addc_u32 s43, s53, s7
	s_add_u32 s6, s54, s6
	s_addc_u32 s7, s55, s7
	s_ashr_i32 s3, s2, 31
	s_lshl_b64 s[44:45], s[2:3], 2
	s_add_u32 s44, s56, s44
	s_addc_u32 s45, s57, s45
	global_load_dword v4, v7, s[44:45] nt
	global_load_dword v5, v49, s[42:43] nt
	global_load_dword v6, v49, s[6:7] nt
	s_mov_b64 s[6:7], 0
	s_waitcnt vmcnt(2)
	v_mul_f32_e32 v2, 0x3fb8aa3b, v4
	v_fma_f32 v3, v4, s71, -v2
	v_rndne_f32_e32 v24, v2
	v_fmac_f32_e32 v3, 0x32a5705f, v4
	v_sub_f32_e32 v2, v2, v24
	v_add_f32_e32 v2, v2, v3
	v_cvt_i32_f32_e32 v24, v24
	v_exp_f32_e32 v25, v2
	v_cmp_ngt_f32_e32 vcc, s72, v4
	v_mov_b32_e32 v2, v39
	v_mov_b32_e32 v3, v38
	v_ldexp_f32 v24, v25, v24
	v_cndmask_b32_e32 v24, 0, v24, vcc
	v_cmp_nlt_f32_e32 vcc, s73, v4
	v_mov_b32_e32 v25, v11
	s_nop 0
	v_cndmask_b32_e32 v24, v48, v24, vcc
	s_waitcnt vmcnt(1)
	v_mul_f32_e32 v4, v24, v5
	s_waitcnt vmcnt(0)
	v_mul_f32_e32 v5, v24, v6
	s_branch .LBB0_11

.LBB0_20:
	s_or_b64 exec, exec, s[42:43]
	s_waitcnt vmcnt(0)
	v_mul_f32_e32 v34, v24, v28
	v_mul_f32_e32 v55, 0x3fb8aa3b, v34
	v_fma_f32 v56, v34, s71, -v55
	v_rndne_f32_e32 v57, v55
	v_fmac_f32_e32 v56, 0x32a5705f, v34
	v_sub_f32_e32 v55, v55, v57
	v_add_f32_e32 v55, v55, v56
	v_cvt_i32_f32_e32 v56, v57
	v_exp_f32_e32 v55, v55
	v_cmp_ngt_f32_e32 vcc, s72, v34
	s_movk_i32 s3, 0x200
	v_lshl_add_u64 v[2:3], v[2:3], 0, s[96:97]
	v_ldexp_f32 v55, v55, v56
	v_lshl_add_u64 v[56:57], s[58:59], 0, v[8:9]
	global_load_dword v58, v[56:57], off nt
	v_lshl_add_u64 v[56:57], s[60:61], 0, v[8:9]
	global_load_dword v59, v[56:57], off nt
	v_lshl_add_u64 v[56:57], s[62:63], 0, v[8:9]
	global_load_dword v60, v[56:57], off nt
	v_lshl_add_u64 v[56:57], s[6:7], 0, v[8:9]
	global_load_dword v56, v[56:57], off nt
	v_cndmask_b32_e32 v55, 0, v55, vcc
	v_cmp_nlt_f32_e32 vcc, s73, v34
	v_lshl_add_u64 v[4:5], v[4:5], 0, s[96:97]
	s_nop 0
	v_cndmask_b32_e32 v34, v48, v55, vcc
	v_mul_f32_e32 v55, v33, v33
	v_fmamk_f32 v57, v55, 0xb94c1982, v50
	v_fmaak_f32 v57, v55, v57, 0xbe2aaa9d
	v_mul_f32_e32 v57, v55, v57
	v_fmac_f32_e32 v33, v33, v57
	v_fmamk_f32 v57, v55, 0x37d75334, v51
	v_fmaak_f32 v57, v55, v57, 0x3d2aabf7
	v_fmaak_f32 v57, v55, v57, 0xbf000004
	v_fma_f32 v55, v55, v57, 1.0
	v_and_b32_e32 v57, 1, v32
	v_cmp_eq_u32_e32 vcc, 0, v57
	v_lshlrev_b32_e32 v32, 30, v32
	s_nop 0
	v_cndmask_b32_e64 v33, -v33, v55, vcc
	v_bitop3_b32 v32, v32, v33, s10 bitop3:0x6c
	v_mul_f32_e32 v33, v35, v35
	v_fmamk_f32 v55, v33, 0xb94c1982, v50
	v_fmaak_f32 v55, v33, v55, 0xbe2aaa9d
	v_mul_f32_e32 v55, v33, v55
	v_fmac_f32_e32 v35, v35, v55
	v_fmamk_f32 v55, v33, 0x37d75334, v51
	v_fmaak_f32 v55, v33, v55, 0x3d2aabf7
	v_fmaak_f32 v55, v33, v55, 0xbf000004
	v_fma_f32 v33, v33, v55, 1.0
	v_and_b32_e32 v55, 1, v6
	v_lshlrev_b32_e32 v6, 30, v6
	v_cmp_class_f32_e64 vcc, v30, s11
	v_cmp_eq_u32_e64 s[42:43], 0, v55
	v_and_b32_e32 v6, 0x80000000, v6
	v_xor_b32_e32 v30, v31, v30
	v_cndmask_b32_e64 v33, v33, v35, s[42:43]
	v_xor_b32_e32 v6, v30, v6
	v_xor_b32_e32 v6, v6, v33
	v_cndmask_b32_e32 v6, v54, v6, vcc
	v_cndmask_b32_e32 v32, v54, v32, vcc
	v_mul_f32_e32 v6, v34, v6
	v_mul_f32_e32 v30, v29, v29
	v_fma_f32 v31, v34, v32, -1.0
	v_mul_f32_e32 v32, v29, v6
	v_fmac_f32_e32 v30, v28, v28
	v_fmac_f32_e32 v32, v28, v31
	v_div_scale_f32 v33, s[42:43], v30, v30, v32
	v_rcp_f32_e32 v34, v33
	v_mul_f32_e32 v29, v29, v31
	v_fma_f32 v6, v28, v6, -v29
	v_div_scale_f32 v28, s[42:43], v30, v30, v6
	v_fma_f32 v35, -v33, v34, 1.0
	v_fmac_f32_e32 v34, v35, v34
	v_div_scale_f32 v35, vcc, v32, v30, v32
	v_mul_f32_e32 v55, v35, v34
	v_fma_f32 v57, -v33, v55, v35
	v_rcp_f32_e32 v29, v28
	v_fmac_f32_e32 v55, v57, v34
	v_fma_f32 v33, -v33, v55, v35
	v_div_fmas_f32 v31, v33, v34, v55
	v_div_fixup_f32 v31, v31, v30, v32
	v_fma_f32 v32, -v28, v29, 1.0
	v_fmac_f32_e32 v29, v32, v29
	v_div_scale_f32 v32, vcc, v6, v30, v6
	v_mul_f32_e32 v33, v32, v29
	v_fma_f32 v34, -v28, v33, v32
	v_fmac_f32_e32 v33, v34, v29
	v_fma_f32 v28, -v28, v33, v32
	v_div_fmas_f32 v28, v28, v29, v33
	v_add_co_u32_e32 v26, vcc, s3, v26
	s_xor_b64 s[42:43], vcc, -1
	s_add_u32 s6, s6, 0x800
	s_addc_u32 s7, s7, 0
	s_add_u32 s62, s62, 0x800
	s_addc_u32 s63, s63, 0
	s_add_u32 s60, s60, 0x800
	v_div_fixup_f32 v6, v28, v30, v6
	s_addc_u32 s61, s61, 0
	s_waitcnt vmcnt(2)
	v_mul_f32_e32 v28, v59, v6
	v_mul_f32_e32 v6, v58, v6
	s_add_u32 s58, s58, 0x800
	v_fma_f32 v28, v58, v31, -v28
	v_fmac_f32_e32 v6, v59, v31
	s_addc_u32 s59, s59, 0
	ds_write2st64_b32 v27, v28, v6 offset1:16
	s_waitcnt vmcnt(0)
	ds_write2st64_b32 v27, v60, v56 offset0:32 offset1:48
	v_add_u32_e32 v6, 0xfffff000, v25
	s_and_b64 s[42:43], exec, s[42:43]
	ds_write_b32 v6, v60
	ds_write_b32 v25, v56
	v_add_u32_e32 v27, 0x800, v27
	v_add_u32_e32 v25, 32, v25
	s_or_b64 s[48:49], s[42:43], s[48:49]
	s_andn2_b64 exec, exec, s[48:49]
	s_cbranch_execz .LBB0_29
.LBB0_21:
	global_load_dword v29, v[2:3], off nt
	global_load_dword v28, v[4:5], off nt
	s_waitcnt vmcnt(1)
	v_mul_f32_e32 v30, v24, v29
	v_and_b32_e32 v31, 0x7fffffff, v30
	v_lshrrev_b32_e32 v6, 23, v31
	v_and_b32_e32 v32, 0x7fffff, v31
	v_cmp_nlt_f32_e64 s[76:77], |v30|, s74
	v_add_u32_e32 v55, 0xffffff88, v6
	v_or_b32_e32 v34, 0x800000, v32
	s_and_saveexec_b64 s[42:43], s[76:77]
	s_xor_b64 s[78:79], exec, s[42:43]
	s_cbranch_execz .LBB0_23
	v_cmp_lt_u32_e32 vcc, 63, v55
	s_nop 1
	v_cndmask_b32_e32 v6, 0, v52, vcc
	v_add_u32_e32 v6, v6, v55
	v_cmp_lt_u32_e64 s[42:43], 31, v6
	s_nop 1
	v_cndmask_b32_e64 v32, 0, v53, s[42:43]
	v_add_u32_e32 v6, v32, v6
	v_cmp_lt_u32_e64 s[44:45], 31, v6
	s_nop 1
	v_cndmask_b32_e64 v32, 0, v53, s[44:45]
	v_add_u32_e32 v35, v32, v6
	v_mad_u64_u32 v[32:33], s[46:47], v34, s75, 0
	v_mov_b32_e32 v6, v33
	v_mad_u64_u32 v[56:57], s[46:47], v34, s69, v[6:7]
	v_mov_b32_e32 v6, v57
	v_mad_u64_u32 v[58:59], s[46:47], v34, s0, v[6:7]
	v_mov_b32_e32 v6, v59
	v_mad_u64_u32 v[60:61], s[46:47], v34, s1, v[6:7]
	v_mov_b32_e32 v6, v61
	v_mad_u64_u32 v[62:63], s[46:47], v34, s33, v[6:7]
	v_mov_b32_e32 v6, v63
	v_mad_u64_u32 v[64:65], s[46:47], v34, s68, v[6:7]
	v_mov_b32_e32 v6, v65
	v_mad_u64_u32 v[66:67], s[46:47], v34, s88, v[6:7]
	v_cndmask_b32_e32 v33, v64, v60, vcc
	v_cndmask_b32_e32 v6, v66, v62, vcc
	v_cndmask_b32_e32 v59, v67, v64, vcc
	v_cndmask_b32_e64 v57, v6, v33, s[42:43]
	v_cndmask_b32_e64 v6, v59, v6, s[42:43]
	v_cndmask_b32_e32 v59, v62, v58, vcc
	v_cndmask_b32_e64 v33, v33, v59, s[42:43]
	v_sub_u32_e32 v61, 32, v35
	v_cmp_eq_u32_e64 s[46:47], 0, v35
	v_cndmask_b32_e32 v35, v60, v56, vcc
	v_cndmask_b32_e64 v6, v6, v57, s[44:45]
	v_cndmask_b32_e64 v57, v57, v33, s[44:45]
	v_cndmask_b32_e64 v56, v59, v35, s[42:43]
	v_alignbit_b32 v62, v6, v57, v61
	v_cndmask_b32_e64 v33, v33, v56, s[44:45]
	v_cndmask_b32_e64 v6, v62, v6, s[46:47]
	v_alignbit_b32 v59, v57, v33, v61
	v_cndmask_b32_e32 v32, v58, v32, vcc
	v_cndmask_b32_e64 v57, v59, v57, s[46:47]
	v_bfe_u32 v62, v6, 29, 1
	v_cndmask_b32_e64 v32, v35, v32, s[42:43]
	v_alignbit_b32 v59, v6, v57, 30
	v_sub_u32_e32 v63, 0, v62
	v_cndmask_b32_e64 v32, v56, v32, s[44:45]
	v_xor_b32_e32 v59, v59, v63
	v_alignbit_b32 v35, v33, v32, v61
	v_cndmask_b32_e64 v33, v35, v33, s[46:47]
	v_ffbh_u32_e32 v56, v59
	v_alignbit_b32 v35, v57, v33, 30
	v_min_u32_e32 v56, 32, v56
	v_alignbit_b32 v32, v33, v32, 30
	v_xor_b32_e32 v35, v35, v63
	v_sub_u32_e32 v57, 31, v56
	v_xor_b32_e32 v32, v32, v63
	v_alignbit_b32 v58, v59, v35, v57
	v_alignbit_b32 v32, v35, v32, v57
	v_alignbit_b32 v33, v58, v32, 9
	v_ffbh_u32_e32 v35, v33
	v_min_u32_e32 v35, 32, v35
	v_lshrrev_b32_e32 v60, 29, v6
	v_not_b32_e32 v57, v35
	v_alignbit_b32 v32, v33, v32, v57
	v_lshlrev_b32_e32 v33, 31, v60
	v_or_b32_e32 v57, 0x33000000, v33
	v_add_lshl_u32 v35, v35, v56, 23
	v_lshrrev_b32_e32 v32, 9, v32
	v_sub_u32_e32 v35, v57, v35
	v_or_b32_e32 v33, 0.5, v33
	v_lshlrev_b32_e32 v56, 23, v56
	v_or_b32_e32 v32, v35, v32
	v_lshrrev_b32_e32 v35, 9, v58
	v_sub_u32_e32 v33, v33, v56
	v_or_b32_e32 v33, v35, v33
	v_mul_f32_e32 v35, 0x3fc90fda, v33
	v_fma_f32 v56, v33, s89, -v35
	v_fmac_f32_e32 v56, 0x33a22168, v33
	v_fmac_f32_e32 v56, 0x3fc90fda, v32
	v_lshrrev_b32_e32 v6, 30, v6
	v_add_f32_e32 v33, v35, v56
	v_add_u32_e32 v32, v62, v6

.LBB0_29:
	s_or_b64 exec, exec, s[48:49]
	v_lshl_or_b32 v2, s2, 4, v1
	v_ashrrev_i32_e32 v3, 31, v2
	v_lshl_add_u64 v[2:3], v[2:3], 2, s[66:67]
	s_waitcnt lgkmcnt(0)
	s_barrier
	global_load_dword v6, v[2:3], off nt
	v_mov_b32_e32 v4, 0
	s_movk_i32 s3, 0xf000
	v_mov_b32_e32 v55, v43
	v_mov_b32_e32 v5, v4
	v_mov_b32_e32 v2, v4
	v_mov_b32_e32 v3, v4
	v_mov_b32_e32 v34, v4
	v_mov_b32_e32 v35, v4
	v_mov_b32_e32 v32, v4
	v_mov_b32_e32 v33, v4
	v_mov_b32_e32 v30, v4
	v_mov_b32_e32 v31, v4
	v_mov_b32_e32 v28, v4
	v_mov_b32_e32 v29, v4
	v_mov_b32_e32 v26, v4
	v_mov_b32_e32 v27, v4
	v_mov_b32_e32 v24, v4
	v_mov_b32_e32 v25, v4

.LBB0_41:
	v_readlane_b32 s0, v252, 41
	v_readlane_b32 s1, v252, 42
	v_readlane_b32 s38, v252, 19
	s_andn2_b64 vcc, exec, s[0:1]
	s_mov_b32 s80, s14
	v_readlane_b32 s90, v252, 43
	s_mov_b32 s85, s15
	v_readlane_b32 s39, v252, 20
	v_readlane_b32 s75, v252, 17
	v_readlane_b32 s91, v252, 44
	s_cbranch_vccnz .LBB0_152
	v_readlane_b32 s1, v252, 39
	s_sub_i32 s18, s90, s1
	s_lshl_b32 s9, s18, 3
	v_readlane_b32 s0, v252, 13
	s_add_i32 s9, s9, s0
	s_sub_i32 s36, s80, s1
	s_mulk_i32 s0, 0x4100
	s_lshl_b32 s8, s36, 3
	s_add_i32 s10, s0, 0
	s_cmpk_gt_u32 s9, 0x9ff
	s_cbranch_scc1 .LBB0_47
	s_and_b32 s0, s9, 0xffff
	s_mul_i32 s0, s0, 0xcccd
	s_lshr_b32 s1, s0, 22
	s_lshr_b32 s0, s0, 16
	s_and_b32 s2, s0, 0xffc0
	s_mul_i32 s2, s2, 0x9000
	v_readlane_b32 s4, v252, 29
	v_readlane_b32 s5, v252, 30
	s_add_u32 s2, s4, s2
	s_mulk_i32 s1, 0x50
	s_addc_u32 s3, s5, 0
	s_sub_i32 s1, s9, s1
	s_lshl_b32 s1, s1, 8
	s_and_b32 s1, s1, 0x3ff00
	s_add_u32 s2, s2, s1
	s_addc_u32 s3, s3, 0
	v_mov_b32_e32 v3, 0
	v_lshlrev_b32_e32 v2, 2, v198
	s_mov_b32 s0, 0x9000
	v_lshl_add_u64 v[4:5], s[2:3], 0, v[2:3]
	v_add_co_u32_e32 v6, vcc, s0, v4
	s_mov_b32 s1, 0x12000
	s_nop 0
	v_addc_co_u32_e32 v7, vcc, 0, v5, vcc
	v_add_co_u32_e32 v8, vcc, s1, v4
	s_mov_b32 s4, 0x1b000
	s_nop 0
	v_addc_co_u32_e32 v9, vcc, 0, v5, vcc
	v_add_co_u32_e32 v10, vcc, s4, v4
	s_mov_b32 s5, 0x24000
	s_nop 0
	v_addc_co_u32_e32 v11, vcc, 0, v5, vcc
	v_add_co_u32_e32 v12, vcc, s5, v4
	s_mov_b32 s6, 0x2d000
	s_nop 0
	v_addc_co_u32_e32 v13, vcc, 0, v5, vcc
	v_add_co_u32_e32 v14, vcc, s6, v4
	s_mov_b32 s7, 0x36000
	s_nop 0
	v_addc_co_u32_e32 v15, vcc, 0, v5, vcc
	v_add_co_u32_e32 v16, vcc, s7, v4
	s_mov_b32 s11, 0x3f000
	s_nop 0
	v_addc_co_u32_e32 v17, vcc, 0, v5, vcc
	v_add_co_u32_e32 v18, vcc, s11, v4
	s_mov_b32 s12, 0x48000
	s_nop 0
	v_addc_co_u32_e32 v19, vcc, 0, v5, vcc
	v_add_co_u32_e32 v20, vcc, s12, v4
	s_mov_b32 s13, 0x51000
	s_nop 0
	v_addc_co_u32_e32 v21, vcc, 0, v5, vcc
	global_load_dword v1, v[6:7], off nt
	s_nop 0
	global_load_dword v8, v[8:9], off nt
	s_nop 0
	global_load_dword v9, v[10:11], off nt
	s_nop 0
	global_load_dword v10, v[12:13], off nt
	global_load_dword v11, v[14:15], off nt
	s_nop 0
	global_load_dword v12, v[16:17], off nt
	global_load_dword v13, v[18:19], off nt
	global_load_dword v14, v[20:21], off nt
	v_add_co_u32_e32 v6, vcc, s13, v4
	s_mov_b32 s14, 0x5a000
	s_nop 0
	v_addc_co_u32_e32 v7, vcc, 0, v5, vcc
	v_add_co_u32_e32 v16, vcc, s14, v4
	s_mov_b32 s15, 0x63000
	s_nop 0
	v_addc_co_u32_e32 v17, vcc, 0, v5, vcc
	v_add_co_u32_e32 v18, vcc, s15, v4
	s_mov_b32 s16, 0x6c000
	s_nop 0
	v_addc_co_u32_e32 v19, vcc, 0, v5, vcc
	v_add_co_u32_e32 v20, vcc, s16, v4
	s_mov_b32 s17, 0x75000
	s_nop 0
	v_addc_co_u32_e32 v21, vcc, 0, v5, vcc
	v_add_co_u32_e32 v22, vcc, s17, v4
	s_mov_b32 s19, 0x7e000
	s_nop 0
	v_addc_co_u32_e32 v23, vcc, 0, v5, vcc
	v_add_co_u32_e32 v24, vcc, s19, v4
	s_mov_b32 s20, 0x87000
	s_nop 0
	v_addc_co_u32_e32 v25, vcc, 0, v5, vcc
	v_add_co_u32_e32 v26, vcc, s20, v4
	s_mov_b32 s21, 0x90000
	s_nop 0
	v_addc_co_u32_e32 v27, vcc, 0, v5, vcc
	v_add_co_u32_e32 v28, vcc, s21, v4
	s_mov_b32 s22, 0x99000
	s_nop 0
	v_addc_co_u32_e32 v29, vcc, 0, v5, vcc
	global_load_dword v15, v[6:7], off nt
	s_nop 0
	global_load_dword v16, v[16:17], off nt
	s_nop 0
	global_load_dword v17, v[18:19], off nt
	s_nop 0
	global_load_dword v18, v[20:21], off nt
	global_load_dword v19, v[22:23], off nt
	s_nop 0
	global_load_dword v20, v[24:25], off nt
	global_load_dword v21, v[26:27], off nt
	global_load_dword v22, v[28:29], off nt
	v_add_co_u32_e32 v6, vcc, s22, v4
	s_mov_b32 s23, 0xa2000
	s_nop 0
	v_addc_co_u32_e32 v7, vcc, 0, v5, vcc
	v_add_co_u32_e32 v24, vcc, s23, v4
	s_mov_b32 s24, 0xab000
	s_nop 0
	v_addc_co_u32_e32 v25, vcc, 0, v5, vcc
	v_add_co_u32_e32 v26, vcc, s24, v4
	s_mov_b32 s25, 0xb4000
	s_nop 0
	v_addc_co_u32_e32 v27, vcc, 0, v5, vcc
	v_add_co_u32_e32 v28, vcc, s25, v4
	s_mov_b32 s26, 0xbd000
	s_nop 0
	v_addc_co_u32_e32 v29, vcc, 0, v5, vcc
	v_add_co_u32_e32 v30, vcc, s26, v4
	s_mov_b32 s27, 0xc6000
	s_nop 0
	v_addc_co_u32_e32 v31, vcc, 0, v5, vcc
	v_add_co_u32_e32 v32, vcc, s27, v4
	s_mov_b32 s28, 0xcf000
	s_nop 0
	v_addc_co_u32_e32 v33, vcc, 0, v5, vcc
	v_add_co_u32_e32 v34, vcc, s28, v4
	s_mov_b32 s29, 0xd8000
	s_nop 0
	v_addc_co_u32_e32 v35, vcc, 0, v5, vcc
	v_add_co_u32_e32 v36, vcc, s29, v4
	s_mov_b32 s30, 0xe1000
	s_nop 0
	v_addc_co_u32_e32 v37, vcc, 0, v5, vcc
	global_load_dword v23, v[6:7], off nt
	s_nop 0
	global_load_dword v24, v[24:25], off nt
	s_nop 0
	global_load_dword v25, v[26:27], off nt
	s_nop 0
	global_load_dword v26, v[28:29], off nt
	global_load_dword v27, v[30:31], off nt
	s_nop 0
	global_load_dword v28, v[32:33], off nt
	global_load_dword v29, v[34:35], off nt
	global_load_dword v30, v[36:37], off nt
	v_add_co_u32_e32 v6, vcc, s30, v4
	s_mov_b32 s31, 0xea000
	s_nop 0
	v_addc_co_u32_e32 v7, vcc, 0, v5, vcc
	v_add_co_u32_e32 v32, vcc, s31, v4
	s_mov_b32 s33, 0xf3000
	s_nop 0
	v_addc_co_u32_e32 v33, vcc, 0, v5, vcc
	v_add_co_u32_e32 v34, vcc, s33, v4
	s_mov_b32 s34, 0xfc000
	s_nop 0
	v_addc_co_u32_e32 v35, vcc, 0, v5, vcc
	v_add_co_u32_e32 v36, vcc, s34, v4
	s_mov_b32 s35, 0x105000
	s_nop 0
	v_addc_co_u32_e32 v37, vcc, 0, v5, vcc
	v_add_co_u32_e32 v38, vcc, s35, v4
	s_mov_b32 s37, 0x10e000
	s_nop 0
	v_addc_co_u32_e32 v39, vcc, 0, v5, vcc
	v_add_co_u32_e32 v40, vcc, s37, v4
	s_mov_b32 s38, 0x117000
	s_nop 0
	v_addc_co_u32_e32 v41, vcc, 0, v5, vcc
	v_add_co_u32_e32 v42, vcc, s38, v4
	s_mov_b32 s39, 0x120000
	s_nop 0
	v_addc_co_u32_e32 v43, vcc, 0, v5, vcc
	v_add_co_u32_e32 v44, vcc, s39, v4
	s_mov_b32 s40, 0x129000
	s_nop 0
	v_addc_co_u32_e32 v45, vcc, 0, v5, vcc
	global_load_dword v31, v[6:7], off nt
	s_nop 0
	global_load_dword v32, v[32:33], off nt
	s_nop 0
	global_load_dword v33, v[34:35], off nt
	s_nop 0
	global_load_dword v34, v[36:37], off nt
	global_load_dword v35, v[38:39], off nt
	s_nop 0
	global_load_dword v36, v[40:41], off nt
	global_load_dword v39, v[42:43], off nt
	s_nop 0
	global_load_dword v40, v[44:45], off nt
	v_add_co_u32_e32 v6, vcc, s40, v4
	s_mov_b32 s41, 0x132000
	s_nop 0
	v_addc_co_u32_e32 v7, vcc, 0, v5, vcc
	v_add_co_u32_e32 v42, vcc, s41, v4
	s_mov_b32 s42, 0x13b000
	s_nop 0
	v_addc_co_u32_e32 v43, vcc, 0, v5, vcc
	v_add_co_u32_e32 v44, vcc, s42, v4
	s_mov_b32 s43, 0x144000
	s_nop 0
	v_addc_co_u32_e32 v45, vcc, 0, v5, vcc
	v_add_co_u32_e32 v46, vcc, s43, v4
	s_mov_b32 s44, 0x14d000
	s_nop 0
	v_addc_co_u32_e32 v47, vcc, 0, v5, vcc
	v_add_co_u32_e32 v48, vcc, s44, v4
	s_mov_b32 s45, 0x156000
	s_nop 0
	v_addc_co_u32_e32 v49, vcc, 0, v5, vcc
	v_add_co_u32_e32 v50, vcc, s45, v4
	s_mov_b32 s46, 0x15f000
	s_nop 0
	v_addc_co_u32_e32 v51, vcc, 0, v5, vcc
	v_add_co_u32_e32 v52, vcc, s46, v4
	s_mov_b32 s47, 0x168000
	s_nop 0
	v_addc_co_u32_e32 v53, vcc, 0, v5, vcc
	v_add_co_u32_e32 v54, vcc, s47, v4
	s_mov_b32 s48, 0x171000
	s_nop 0
	v_addc_co_u32_e32 v55, vcc, 0, v5, vcc
	global_load_dword v57, v[6:7], off nt
	global_load_dword v58, v[42:43], off nt
	global_load_dword v59, v[44:45], off nt
	global_load_dword v60, v[46:47], off nt
	global_load_dword v61, v[48:49], off nt
	global_load_dword v62, v[50:51], off nt
	global_load_dword v63, v[52:53], off nt
	global_load_dword v64, v[54:55], off nt
	v_add_co_u32_e32 v6, vcc, s48, v4
	s_mov_b32 s49, 0x17a000
	s_nop 0
	v_addc_co_u32_e32 v7, vcc, 0, v5, vcc
	v_add_co_u32_e32 v42, vcc, s49, v4
	s_mov_b32 s50, 0x183000
	s_nop 0
	v_addc_co_u32_e32 v43, vcc, 0, v5, vcc
	v_add_co_u32_e32 v44, vcc, s50, v4
	s_mov_b32 s51, 0x18c000
	s_nop 0
	v_addc_co_u32_e32 v45, vcc, 0, v5, vcc
	v_add_co_u32_e32 v46, vcc, s51, v4
	s_mov_b32 s52, 0x195000
	s_nop 0
	v_addc_co_u32_e32 v47, vcc, 0, v5, vcc
	v_add_co_u32_e32 v48, vcc, s52, v4
	s_mov_b32 s53, 0x19e000
	s_nop 0
	v_addc_co_u32_e32 v49, vcc, 0, v5, vcc
	v_add_co_u32_e32 v50, vcc, s53, v4
	s_mov_b32 s54, 0x1a7000
	s_nop 0
	v_addc_co_u32_e32 v51, vcc, 0, v5, vcc
	v_add_co_u32_e32 v52, vcc, s54, v4
	s_mov_b32 s55, 0x1b0000
	s_nop 0
	v_addc_co_u32_e32 v53, vcc, 0, v5, vcc
	v_add_co_u32_e32 v54, vcc, s55, v4
	s_mov_b32 s56, 0x1b9000
	s_nop 0
	v_addc_co_u32_e32 v55, vcc, 0, v5, vcc
	global_load_dword v65, v[6:7], off nt
	global_load_dword v66, v[42:43], off nt
	global_load_dword v67, v[44:45], off nt
	global_load_dword v68, v[46:47], off nt
	global_load_dword v69, v[48:49], off nt
	global_load_dword v70, v[50:51], off nt
	global_load_dword v71, v[52:53], off nt
	global_load_dword v72, v[54:55], off nt
	v_add_co_u32_e32 v6, vcc, s56, v4
	s_mov_b32 s57, 0x1c2000
	s_nop 0
	v_addc_co_u32_e32 v7, vcc, 0, v5, vcc
	v_add_co_u32_e32 v42, vcc, s57, v4
	s_mov_b32 s58, 0x1cb000
	s_nop 0
	v_addc_co_u32_e32 v43, vcc, 0, v5, vcc
	v_add_co_u32_e32 v44, vcc, s58, v4
	s_mov_b32 s59, 0x1d4000
	s_nop 0
	v_addc_co_u32_e32 v45, vcc, 0, v5, vcc
	v_add_co_u32_e32 v46, vcc, s59, v4
	s_mov_b32 s60, 0x1dd000
	s_nop 0
	v_addc_co_u32_e32 v47, vcc, 0, v5, vcc
	v_add_co_u32_e32 v48, vcc, s60, v4
	s_mov_b32 s61, 0x1e6000
	s_nop 0
	v_addc_co_u32_e32 v49, vcc, 0, v5, vcc
	v_add_co_u32_e32 v50, vcc, s61, v4
	s_mov_b32 s62, 0x1ef000
	s_nop 0
	v_addc_co_u32_e32 v51, vcc, 0, v5, vcc
	v_add_co_u32_e32 v52, vcc, s62, v4
	s_mov_b32 s63, 0x1f8000
	s_nop 0
	v_addc_co_u32_e32 v53, vcc, 0, v5, vcc
	v_add_co_u32_e32 v54, vcc, s63, v4
	s_mov_b32 s64, 0x201000
	s_nop 0
	v_addc_co_u32_e32 v55, vcc, 0, v5, vcc
	global_load_dword v73, v[6:7], off nt
	global_load_dword v74, v[42:43], off nt
	global_load_dword v75, v[44:45], off nt
	global_load_dword v76, v[46:47], off nt
	global_load_dword v77, v[48:49], off nt
	global_load_dword v78, v[50:51], off nt
	global_load_dword v79, v[52:53], off nt
	global_load_dword v80, v[54:55], off nt
	v_add_co_u32_e32 v6, vcc, s64, v4
	s_mov_b32 s65, 0x20a000
	s_nop 0
	v_addc_co_u32_e32 v7, vcc, 0, v5, vcc
	v_add_co_u32_e32 v42, vcc, s65, v4
	s_mov_b32 s66, 0x213000
	s_nop 0
	v_addc_co_u32_e32 v43, vcc, 0, v5, vcc
	v_add_co_u32_e32 v44, vcc, s66, v4
	s_mov_b32 s67, 0x21c000
	s_nop 0
	v_addc_co_u32_e32 v45, vcc, 0, v5, vcc
	v_add_co_u32_e32 v46, vcc, s67, v4
	s_mov_b32 s67, 0x225000
	s_nop 0
	v_addc_co_u32_e32 v47, vcc, 0, v5, vcc
	v_add_co_u32_e32 v48, vcc, s67, v4
	s_mov_b32 s67, 0x22e000
	s_nop 0
	v_addc_co_u32_e32 v49, vcc, 0, v5, vcc
	v_add_co_u32_e32 v50, vcc, s67, v4
	s_mov_b32 s67, 0x237000
	s_nop 0
	v_addc_co_u32_e32 v51, vcc, 0, v5, vcc
	v_add_co_u32_e32 v4, vcc, s67, v4
	v_add_u32_e32 v37, s10, v2
	s_nop 0
	v_addc_co_u32_e32 v5, vcc, 0, v5, vcc
	global_load_dword v81, v2, s[2:3] nt
	global_load_dword v82, v[6:7], off nt
	global_load_dword v83, v[42:43], off nt
	global_load_dword v84, v[44:45], off nt
	global_load_dword v85, v[46:47], off nt
	global_load_dword v86, v[48:49], off nt
	global_load_dword v87, v[50:51], off nt
	global_load_dword v88, v[4:5], off nt
	v_lshlrev_b32_e32 v2, 3, v0
	v_and_b32_e32 v2, 56, v2
	v_mul_u32_u24_e32 v6, 0x104, v2
	v_lshlrev_b32_e32 v2, 1, v2
	v_lshl_add_u64 v[4:5], s[82:83], 0, v[2:3]
	s_mov_b64 s[2:3], 0x100000
	v_lshl_add_u64 v[4:5], v[4:5], 0, s[2:3]
	v_readlane_b32 s3, v252, 39
	v_lshrrev_b32_e32 v38, 3, v198
	s_lshl_b32 s2, s3, 4
	v_lshlrev_b32_e32 v2, 2, v38
	s_sub_i32 s67, s85, s2
	s_lshl_b32 s2, s3, 3
	v_add3_u32 v41, s10, v6, v2
	v_or_b32_e32 v42, 8, v38
	v_or_b32_e32 v43, 16, v38
	v_or_b32_e32 v44, 24, v38
	v_or_b32_e32 v45, 32, v38
	v_or_b32_e32 v46, 40, v38
	v_or_b32_e32 v47, 48, v38
	v_or_b32_e32 v48, 56, v38
	s_sub_i32 s68, 0, s2
	v_lshlrev_b32_e32 v2, 2, v198
	s_movk_i32 s69, 0x7fff
	s_mov_b32 s70, 0xffff0000
	v_mov_b32_e32 v49, 0xf07
	v_mov_b32_e32 v50, 0xf0f
	v_mov_b32_e32 v51, 0xf17
	v_mov_b32_e32 v52, 0xf1f
	v_mov_b32_e32 v53, 0xf27
	v_mov_b32_e32 v54, 0xf2f
	v_mov_b32_e32 v55, 0xf37
	v_mov_b32_e32 v56, 0xf3f
	v_readlane_b32 s71, v252, 14
	s_branch .LBB0_45

.LBB0_45:
	v_add_u32_e32 v6, 0x400, v37
	s_waitcnt vmcnt(7)
	ds_write2_b32 v37, v81, v1 offset1:65
	ds_write2_b32 v37, v8, v9 offset0:130 offset1:195
	ds_write2_b32 v6, v10, v11 offset0:4 offset1:69
	ds_write2_b32 v6, v12, v13 offset0:134 offset1:199
	v_add_u32_e32 v6, 0x800, v37
	ds_write2_b32 v6, v14, v15 offset0:8 offset1:73
	ds_write2_b32 v6, v16, v17 offset0:138 offset1:203
	v_add_u32_e32 v6, 0xc00, v37
	ds_write2_b32 v6, v18, v19 offset0:12 offset1:77
	ds_write2_b32 v6, v20, v21 offset0:142 offset1:207
	v_add_u32_e32 v6, 0x1000, v37
	ds_write2_b32 v6, v22, v23 offset0:16 offset1:81
	ds_write2_b32 v6, v24, v25 offset0:146 offset1:211
	v_add_u32_e32 v6, 0x1400, v37
	ds_write2_b32 v6, v26, v27 offset0:20 offset1:85
	ds_write2_b32 v6, v28, v29 offset0:150 offset1:215
	v_add_u32_e32 v6, 0x1800, v37
	ds_write2_b32 v6, v30, v31 offset0:24 offset1:89
	ds_write2_b32 v6, v32, v33 offset0:154 offset1:219
	v_add_u32_e32 v6, 0x1c00, v37
	ds_write2_b32 v6, v34, v35 offset0:28 offset1:93
	ds_write2_b32 v6, v36, v39 offset0:158 offset1:223
	v_add_u32_e32 v6, 0x2000, v37
	ds_write2_b32 v6, v40, v57 offset0:32 offset1:97
	ds_write2_b32 v6, v58, v59 offset0:162 offset1:227
	v_add_u32_e32 v6, 0x2400, v37
	ds_write2_b32 v6, v60, v61 offset0:36 offset1:101
	ds_write2_b32 v6, v62, v63 offset0:166 offset1:231
	v_add_u32_e32 v6, 0x2800, v37
	ds_write2_b32 v6, v64, v65 offset0:40 offset1:105
	ds_write2_b32 v6, v66, v67 offset0:170 offset1:235
	v_add_u32_e32 v6, 0x2c00, v37
	ds_write2_b32 v6, v68, v69 offset0:44 offset1:109
	ds_write2_b32 v6, v70, v71 offset0:174 offset1:239
	v_add_u32_e32 v6, 0x3000, v37
	ds_write2_b32 v6, v72, v73 offset0:48 offset1:113
	ds_write2_b32 v6, v74, v75 offset0:178 offset1:243
	v_add_u32_e32 v6, 0x3400, v37
	ds_write2_b32 v6, v76, v77 offset0:52 offset1:117
	ds_write2_b32 v6, v78, v79 offset0:182 offset1:247
	v_add_u32_e32 v6, 0x3800, v37
	s_waitcnt vmcnt(6)
	ds_write2_b32 v6, v80, v82 offset0:56 offset1:121
	s_waitcnt vmcnt(4)
	ds_write2_b32 v6, v83, v84 offset0:186 offset1:251
	v_add_u32_e32 v6, 0x3c00, v37
	s_waitcnt vmcnt(2)
	ds_write2_b32 v6, v85, v86 offset0:60 offset1:125
	s_waitcnt vmcnt(0)
	ds_write2_b32 v6, v87, v88 offset0:190 offset1:255
	s_waitcnt lgkmcnt(0)
	s_add_i32 s2, s67, s71
	s_cmpk_gt_i32 s2, 0x9ff
	s_cbranch_scc1 .LBB0_44
	s_mul_hi_i32 s3, s2, 0x66666667
	s_lshr_b32 s72, s3, 31
	s_ashr_i32 s3, s3, 10
	s_add_i32 s3, s3, s72
	s_mulk_i32 s3, 0xa00
	s_sub_i32 s2, s2, s3
	s_sext_i32_i16 s3, s2
	s_mulk_i32 s3, 0x6667
	s_lshr_b32 s72, s3, 31
	s_ashr_i32 s3, s3, 21
	s_add_i32 s3, s3, s72
	s_mul_i32 s73, s3, 0x240000
	v_readlane_b32 s76, v252, 29
	s_mul_hi_i32 s72, s3, 0x240000
	v_readlane_b32 s77, v252, 30
	s_add_u32 s73, s76, s73
	s_mulk_i32 s3, 0x50
	s_addc_u32 s72, s77, s72
	s_sub_i32 s2, s2, s3
	s_sext_i32_i16 s2, s2
	s_lshl_b32 s2, s2, 6
	s_ashr_i32 s3, s2, 31
	s_lshl_b64 s[2:3], s[2:3], 2
	s_add_u32 s2, s73, s2
	s_addc_u32 s3, s72, s3
	v_lshl_add_u64 v[6:7], s[2:3], 0, v[2:3]
	v_add_co_u32_e32 v8, vcc, s0, v6
	s_nop 1
	v_addc_co_u32_e32 v9, vcc, 0, v7, vcc
	v_add_co_u32_e32 v10, vcc, s1, v6
	s_nop 1
	v_addc_co_u32_e32 v11, vcc, 0, v7, vcc
	v_add_co_u32_e32 v12, vcc, s4, v6
	s_nop 1
	v_addc_co_u32_e32 v13, vcc, 0, v7, vcc
	v_add_co_u32_e32 v14, vcc, s5, v6
	s_nop 1
	v_addc_co_u32_e32 v15, vcc, 0, v7, vcc
	v_add_co_u32_e32 v16, vcc, s6, v6
	s_nop 1
	v_addc_co_u32_e32 v17, vcc, 0, v7, vcc
	v_add_co_u32_e32 v18, vcc, s7, v6
	s_nop 1
	v_addc_co_u32_e32 v19, vcc, 0, v7, vcc
	v_add_co_u32_e32 v20, vcc, s11, v6
	s_nop 1
	v_addc_co_u32_e32 v21, vcc, 0, v7, vcc
	v_add_co_u32_e32 v22, vcc, s12, v6
	s_nop 1
	v_addc_co_u32_e32 v23, vcc, 0, v7, vcc
	global_load_dword v1, v[8:9], off nt
	s_nop 0
	global_load_dword v8, v[10:11], off nt
	global_load_dword v9, v[12:13], off nt
	s_nop 0
	global_load_dword v10, v[14:15], off nt
	global_load_dword v11, v[16:17], off nt
	global_load_dword v12, v[18:19], off nt
	global_load_dword v13, v[20:21], off nt
	s_nop 0
	global_load_dword v14, v[22:23], off nt
	v_add_co_u32_e32 v16, vcc, s13, v6
	s_nop 1
	v_addc_co_u32_e32 v17, vcc, 0, v7, vcc
	v_add_co_u32_e32 v18, vcc, s14, v6
	s_nop 1
	v_addc_co_u32_e32 v19, vcc, 0, v7, vcc
	v_add_co_u32_e32 v20, vcc, s15, v6
	s_nop 1
	v_addc_co_u32_e32 v21, vcc, 0, v7, vcc
	v_add_co_u32_e32 v22, vcc, s16, v6
	s_nop 1
	v_addc_co_u32_e32 v23, vcc, 0, v7, vcc
	v_add_co_u32_e32 v24, vcc, s17, v6
	s_nop 1
	v_addc_co_u32_e32 v25, vcc, 0, v7, vcc
	v_add_co_u32_e32 v26, vcc, s19, v6
	s_nop 1
	v_addc_co_u32_e32 v27, vcc, 0, v7, vcc
	v_add_co_u32_e32 v28, vcc, s20, v6
	s_nop 1
	v_addc_co_u32_e32 v29, vcc, 0, v7, vcc
	v_add_co_u32_e32 v30, vcc, s21, v6
	s_nop 1
	v_addc_co_u32_e32 v31, vcc, 0, v7, vcc
	global_load_dword v15, v[16:17], off nt
	s_nop 0
	global_load_dword v16, v[18:19], off nt
	global_load_dword v17, v[20:21], off nt
	s_nop 0
	global_load_dword v18, v[22:23], off nt
	global_load_dword v19, v[24:25], off nt
	global_load_dword v20, v[26:27], off nt
	global_load_dword v21, v[28:29], off nt
	s_nop 0
	global_load_dword v22, v[30:31], off nt
	v_add_co_u32_e32 v24, vcc, s22, v6
	s_nop 1
	v_addc_co_u32_e32 v25, vcc, 0, v7, vcc
	v_add_co_u32_e32 v26, vcc, s23, v6
	s_nop 1
	v_addc_co_u32_e32 v27, vcc, 0, v7, vcc
	v_add_co_u32_e32 v28, vcc, s24, v6
	s_nop 1
	v_addc_co_u32_e32 v29, vcc, 0, v7, vcc
	v_add_co_u32_e32 v30, vcc, s25, v6
	s_nop 1
	v_addc_co_u32_e32 v31, vcc, 0, v7, vcc
	v_add_co_u32_e32 v32, vcc, s26, v6
	s_nop 1
	v_addc_co_u32_e32 v33, vcc, 0, v7, vcc
	v_add_co_u32_e32 v34, vcc, s27, v6
	s_nop 1
	v_addc_co_u32_e32 v35, vcc, 0, v7, vcc
	v_add_co_u32_e32 v58, vcc, s28, v6
	s_nop 1
	v_addc_co_u32_e32 v59, vcc, 0, v7, vcc
	v_add_co_u32_e32 v60, vcc, s29, v6
	s_nop 1
	v_addc_co_u32_e32 v61, vcc, 0, v7, vcc
	global_load_dword v23, v[24:25], off nt
	s_nop 0
	global_load_dword v24, v[26:27], off nt
	global_load_dword v25, v[28:29], off nt
	s_nop 0
	global_load_dword v26, v[30:31], off nt
	global_load_dword v27, v[32:33], off nt
	global_load_dword v28, v[34:35], off nt
	global_load_dword v29, v[58:59], off nt
	s_nop 0
	global_load_dword v30, v[60:61], off nt
	v_add_co_u32_e32 v32, vcc, s30, v6
	s_nop 1
	v_addc_co_u32_e32 v33, vcc, 0, v7, vcc
	v_add_co_u32_e32 v34, vcc, s31, v6
	s_nop 1
	v_addc_co_u32_e32 v35, vcc, 0, v7, vcc
	v_add_co_u32_e32 v58, vcc, s33, v6
	s_nop 1
	v_addc_co_u32_e32 v59, vcc, 0, v7, vcc
	v_add_co_u32_e32 v60, vcc, s34, v6
	s_nop 1
	v_addc_co_u32_e32 v61, vcc, 0, v7, vcc
	v_add_co_u32_e32 v62, vcc, s35, v6
	s_nop 1
	v_addc_co_u32_e32 v63, vcc, 0, v7, vcc
	v_add_co_u32_e32 v64, vcc, s37, v6
	s_nop 1
	v_addc_co_u32_e32 v65, vcc, 0, v7, vcc
	v_add_co_u32_e32 v66, vcc, s38, v6
	s_nop 1
	v_addc_co_u32_e32 v67, vcc, 0, v7, vcc
	v_add_co_u32_e32 v68, vcc, s39, v6
	s_nop 1
	v_addc_co_u32_e32 v69, vcc, 0, v7, vcc
	global_load_dword v31, v[32:33], off nt
	s_nop 0
	global_load_dword v32, v[34:35], off nt
	global_load_dword v33, v[58:59], off nt
	s_nop 0
	global_load_dword v34, v[60:61], off nt
	global_load_dword v35, v[62:63], off nt
	global_load_dword v36, v[64:65], off nt
	global_load_dword v39, v[66:67], off nt
	global_load_dword v40, v[68:69], off nt
	v_add_co_u32_e32 v58, vcc, s40, v6
	s_nop 1
	v_addc_co_u32_e32 v59, vcc, 0, v7, vcc
	v_add_co_u32_e32 v60, vcc, s41, v6
	s_nop 1
	v_addc_co_u32_e32 v61, vcc, 0, v7, vcc
	v_add_co_u32_e32 v62, vcc, s42, v6
	s_nop 1
	v_addc_co_u32_e32 v63, vcc, 0, v7, vcc
	v_add_co_u32_e32 v64, vcc, s43, v6
	s_nop 1
	v_addc_co_u32_e32 v65, vcc, 0, v7, vcc
	v_add_co_u32_e32 v66, vcc, s44, v6
	s_nop 1
	v_addc_co_u32_e32 v67, vcc, 0, v7, vcc
	v_add_co_u32_e32 v68, vcc, s45, v6
	s_nop 1
	v_addc_co_u32_e32 v69, vcc, 0, v7, vcc
	v_add_co_u32_e32 v70, vcc, s46, v6
	s_nop 1
	v_addc_co_u32_e32 v71, vcc, 0, v7, vcc
	v_add_co_u32_e32 v72, vcc, s47, v6
	s_nop 1
	v_addc_co_u32_e32 v73, vcc, 0, v7, vcc
	global_load_dword v57, v[58:59], off nt
	s_nop 0
	global_load_dword v58, v[60:61], off nt
	global_load_dword v59, v[62:63], off nt
	s_nop 0
	global_load_dword v60, v[64:65], off nt
	global_load_dword v61, v[66:67], off nt
	global_load_dword v62, v[68:69], off nt
	global_load_dword v63, v[70:71], off nt
	s_nop 0
	global_load_dword v64, v[72:73], off nt
	v_add_co_u32_e32 v66, vcc, s48, v6
	s_nop 1
	v_addc_co_u32_e32 v67, vcc, 0, v7, vcc
	v_add_co_u32_e32 v68, vcc, s49, v6
	s_nop 1
	v_addc_co_u32_e32 v69, vcc, 0, v7, vcc
	v_add_co_u32_e32 v70, vcc, s50, v6
	s_nop 1
	v_addc_co_u32_e32 v71, vcc, 0, v7, vcc
	v_add_co_u32_e32 v72, vcc, s51, v6
	s_nop 1
	v_addc_co_u32_e32 v73, vcc, 0, v7, vcc
	v_add_co_u32_e32 v74, vcc, s52, v6
	s_nop 1
	v_addc_co_u32_e32 v75, vcc, 0, v7, vcc
	v_add_co_u32_e32 v76, vcc, s53, v6
	s_nop 1
	v_addc_co_u32_e32 v77, vcc, 0, v7, vcc
	v_add_co_u32_e32 v78, vcc, s54, v6
	s_nop 1
	v_addc_co_u32_e32 v79, vcc, 0, v7, vcc
	v_add_co_u32_e32 v80, vcc, s55, v6
	s_nop 1
	v_addc_co_u32_e32 v81, vcc, 0, v7, vcc
	global_load_dword v65, v[66:67], off nt
	s_nop 0
	global_load_dword v66, v[68:69], off nt
	global_load_dword v67, v[70:71], off nt
	s_nop 0
	global_load_dword v68, v[72:73], off nt
	global_load_dword v69, v[74:75], off nt
	global_load_dword v70, v[76:77], off nt
	global_load_dword v71, v[78:79], off nt
	s_nop 0
	global_load_dword v72, v[80:81], off nt
	v_add_co_u32_e32 v74, vcc, s56, v6
	s_nop 1
	v_addc_co_u32_e32 v75, vcc, 0, v7, vcc
	v_add_co_u32_e32 v76, vcc, s57, v6
	s_nop 1
	v_addc_co_u32_e32 v77, vcc, 0, v7, vcc
	v_add_co_u32_e32 v78, vcc, s58, v6
	s_nop 1
	v_addc_co_u32_e32 v79, vcc, 0, v7, vcc
	v_add_co_u32_e32 v80, vcc, s59, v6
	s_nop 1
	v_addc_co_u32_e32 v81, vcc, 0, v7, vcc
	v_add_co_u32_e32 v82, vcc, s60, v6
	s_nop 1
	v_addc_co_u32_e32 v83, vcc, 0, v7, vcc
	v_add_co_u32_e32 v84, vcc, s61, v6
	s_nop 1
	v_addc_co_u32_e32 v85, vcc, 0, v7, vcc
	v_add_co_u32_e32 v86, vcc, s62, v6
	s_nop 1
	v_addc_co_u32_e32 v87, vcc, 0, v7, vcc
	v_add_co_u32_e32 v88, vcc, s63, v6
	s_nop 1
	v_addc_co_u32_e32 v89, vcc, 0, v7, vcc
	global_load_dword v73, v[74:75], off nt
	s_nop 0
	global_load_dword v74, v[76:77], off nt
	global_load_dword v75, v[78:79], off nt
	s_nop 0
	global_load_dword v76, v[80:81], off nt
	global_load_dword v77, v[82:83], off nt
	global_load_dword v78, v[84:85], off nt
	global_load_dword v79, v[86:87], off nt
	s_nop 0
	global_load_dword v80, v[88:89], off nt
	v_add_co_u32_e32 v82, vcc, s64, v6
	s_nop 1
	v_addc_co_u32_e32 v83, vcc, 0, v7, vcc
	v_add_co_u32_e32 v84, vcc, s65, v6
	s_nop 1
	v_addc_co_u32_e32 v85, vcc, 0, v7, vcc
	v_add_co_u32_e32 v86, vcc, s66, v6
	s_nop 1
	v_addc_co_u32_e32 v87, vcc, 0, v7, vcc
	v_add_co_u32_e32 v88, vcc, 0x21c000, v6
	s_nop 1
	v_addc_co_u32_e32 v89, vcc, 0, v7, vcc
	v_add_co_u32_e32 v90, vcc, 0x225000, v6
	s_nop 1
	v_addc_co_u32_e32 v91, vcc, 0, v7, vcc
	v_add_co_u32_e32 v92, vcc, 0x22e000, v6
	s_nop 1
	v_addc_co_u32_e32 v93, vcc, 0, v7, vcc
	v_add_co_u32_e32 v6, vcc, 0x237000, v6
	s_nop 1
	v_addc_co_u32_e32 v7, vcc, 0, v7, vcc
	global_load_dword v81, v2, s[2:3] nt
	s_nop 0
	global_load_dword v82, v[82:83], off nt
	s_nop 0
	global_load_dword v83, v[84:85], off nt
	s_nop 0
	global_load_dword v84, v[86:87], off nt
	global_load_dword v85, v[88:89], off nt
	s_nop 0
	global_load_dword v86, v[90:91], off nt
	global_load_dword v87, v[92:93], off nt
	global_load_dword v88, v[6:7], off nt
	s_branch .LBB0_44
.LBB0_47:
	s_cmpk_gt_i32 s9, 0x1ff
	s_cbranch_scc1 .LBB0_54
	v_readlane_b32 s0, v252, 29
	v_readlane_b32 s1, v252, 30
	s_add_u32 s0, s0, 0x5000
	s_addc_u32 s1, s1, 0
	s_ashr_i32 s2, s9, 31
	s_lshr_b32 s2, s2, 23
	s_add_i32 s2, s9, s2
	s_and_b32 s2, s2, 0xfffffe00
	s_sub_i32 s2, s9, s2
	s_lshr_b32 s3, s2, 3
	s_bfe_i32 s4, s3, 0x80000
	s_bfe_u32 s4, s4, 0x2000d
	s_add_i32 s4, s3, s4
	s_bfe_i32 s5, s4, 0x80000
	s_and_b32 s4, s4, 0xfc
	s_sub_i32 s3, s3, s4
	s_sext_i32_i8 s3, s3
	s_lshl_b32 s2, s2, 6
	s_lshl_b32 s3, s3, 9
	s_and_b32 s4, s2, 0x100
	s_sext_i32_i16 s5, s5
	s_or_b32 s3, s3, s4
	s_waitcnt vmcnt(62)
	v_and_b32_e32 v1, 48, v0
	v_or_b32_e32 v2, s3, v1
	s_lshl_b32 s3, s5, 6
	v_mul_i32_i24_e32 v2, 0x2400, v2
	s_and_b32 s3, s3, 0xffffff00
	s_and_b32 s2, s2, 0xc0
	v_ashrrev_i32_e32 v3, 31, v2
	s_or_b32 s2, s3, s2
	v_and_b32_e32 v133, 15, v0
	v_lshl_add_u64 v[2:3], v[2:3], 2, s[0:1]
	s_ashr_i32 s3, s2, 31
	v_lshl_add_u64 v[2:3], s[2:3], 2, v[2:3]
	v_mov_b32_e32 v131, 0
	v_lshlrev_b32_e32 v130, 4, v133
	s_waitcnt vmcnt(29)
	v_lshl_add_u64 v[66:67], v[2:3], 0, v[130:131]
	s_mov_b32 s11, 0x9000
	v_add_co_u32_e32 v10, vcc, s11, v66
	s_mov_b32 s12, 0x12000
	s_nop 0
	v_addc_co_u32_e32 v11, vcc, 0, v67, vcc
	global_load_dwordx4 v[2:5], v[66:67], off nt
	global_load_dwordx4 v[6:9], v[10:11], off nt
	v_add_co_u32_e32 v10, vcc, s12, v66
	s_mov_b32 s13, 0x1b000
	s_nop 0
	v_addc_co_u32_e32 v11, vcc, 0, v67, vcc
	v_add_co_u32_e32 v12, vcc, s13, v66
	s_mov_b32 s14, 0x24000
	s_nop 0
	v_addc_co_u32_e32 v13, vcc, 0, v67, vcc
	global_load_dwordx4 v[14:17], v[10:11], off nt
	global_load_dwordx4 v[22:25], v[12:13], off nt
	v_add_co_u32_e32 v10, vcc, s14, v66
	s_mov_b32 s15, 0x2d000
	s_nop 0
	v_addc_co_u32_e32 v11, vcc, 0, v67, vcc
	v_add_co_u32_e32 v18, vcc, s15, v66
	s_mov_b32 s16, 0x36000
	s_nop 0
	v_addc_co_u32_e32 v19, vcc, 0, v67, vcc
	v_add_co_u32_e32 v26, vcc, s16, v66
	s_mov_b32 s17, 0x3f000
	s_nop 0
	v_addc_co_u32_e32 v27, vcc, 0, v67, vcc
	v_add_co_u32_e32 v30, vcc, s17, v66
	s_mov_b32 s19, 0x48000
	s_nop 0
	v_addc_co_u32_e32 v31, vcc, 0, v67, vcc
	global_load_dwordx4 v[10:13], v[10:11], off nt
	s_nop 0
	global_load_dwordx4 v[18:21], v[18:19], off nt
	s_nop 0
	global_load_dwordx4 v[26:29], v[26:27], off nt
	s_nop 0
	global_load_dwordx4 v[34:37], v[30:31], off nt
	v_add_co_u32_e32 v30, vcc, s19, v66
	s_mov_b32 s20, 0x51000
	s_nop 0
	v_addc_co_u32_e32 v31, vcc, 0, v67, vcc
	v_add_co_u32_e32 v38, vcc, s20, v66
	s_mov_b32 s21, 0x5a000
	s_nop 0
	v_addc_co_u32_e32 v39, vcc, 0, v67, vcc
	v_add_co_u32_e32 v42, vcc, s21, v66
	s_mov_b32 s22, 0x63000
	s_nop 0
	v_addc_co_u32_e32 v43, vcc, 0, v67, vcc
	v_add_co_u32_e32 v44, vcc, s22, v66
	s_mov_b32 s2, 0x6c000
	s_nop 0
	v_addc_co_u32_e32 v45, vcc, 0, v67, vcc
	global_load_dwordx4 v[30:33], v[30:31], off nt
	s_nop 0
	global_load_dwordx4 v[38:41], v[38:39], off nt
	s_nop 0
	global_load_dwordx4 v[46:49], v[42:43], off nt
	global_load_dwordx4 v[54:57], v[44:45], off nt
	v_add_co_u32_e32 v42, vcc, s2, v66
	s_mov_b32 s2, 0x75000
	s_nop 0
	v_addc_co_u32_e32 v43, vcc, 0, v67, vcc
	v_add_co_u32_e32 v50, vcc, s2, v66
	s_mov_b32 s2, 0x7e000
	s_nop 0
	v_addc_co_u32_e32 v51, vcc, 0, v67, vcc
	v_add_co_u32_e32 v58, vcc, s2, v66
	s_mov_b32 s2, 0x87000
	s_nop 0
	v_addc_co_u32_e32 v59, vcc, 0, v67, vcc
	v_add_co_u32_e32 v62, vcc, s2, v66
	s_mov_b32 s2, 0x240000
	s_nop 0
	v_addc_co_u32_e32 v63, vcc, 0, v67, vcc
	s_waitcnt vmcnt(40)
	v_add_co_u32_e32 v68, vcc, s2, v66
	s_mov_b32 s2, 0x249000
	s_waitcnt vmcnt(39)
	v_addc_co_u32_e32 v69, vcc, 0, v67, vcc
	s_waitcnt vmcnt(38)
	v_add_co_u32_e32 v70, vcc, s2, v66
	s_mov_b32 s2, 0x252000
	s_waitcnt vmcnt(37)
	v_addc_co_u32_e32 v71, vcc, 0, v67, vcc
	s_waitcnt vmcnt(36)
	v_add_co_u32_e32 v72, vcc, s2, v66
	s_mov_b32 s2, 0x25b000
	s_waitcnt vmcnt(35)
	v_addc_co_u32_e32 v73, vcc, 0, v67, vcc
	s_waitcnt vmcnt(30)
	v_add_co_u32_e32 v78, vcc, s2, v66
	s_mov_b32 s2, 0x264000
	s_waitcnt vmcnt(29)
	v_addc_co_u32_e32 v79, vcc, 0, v67, vcc
	s_waitcnt vmcnt(28)
	v_add_co_u32_e32 v80, vcc, s2, v66
	s_mov_b32 s2, 0x26d000
	s_waitcnt vmcnt(27)
	v_addc_co_u32_e32 v81, vcc, 0, v67, vcc
	s_waitcnt vmcnt(26)
	v_add_co_u32_e32 v82, vcc, s2, v66
	s_mov_b32 s2, 0x276000
	s_waitcnt vmcnt(25)
	v_addc_co_u32_e32 v83, vcc, 0, v67, vcc
	s_waitcnt vmcnt(24)
	v_add_co_u32_e32 v84, vcc, s2, v66
	s_mov_b32 s2, 0x27f000
	s_waitcnt vmcnt(23)
	v_addc_co_u32_e32 v85, vcc, 0, v67, vcc
	v_add_co_u32_e32 v94, vcc, s2, v66
	s_mov_b32 s2, 0x288000
	s_nop 0
	v_addc_co_u32_e32 v95, vcc, 0, v67, vcc
	v_add_co_u32_e32 v96, vcc, s2, v66
	s_mov_b32 s2, 0x291000
	s_nop 0
	v_addc_co_u32_e32 v97, vcc, 0, v67, vcc
	v_add_co_u32_e32 v98, vcc, s2, v66
	s_mov_b32 s2, 0x29a000
	s_nop 0
	v_addc_co_u32_e32 v99, vcc, 0, v67, vcc
	v_add_co_u32_e32 v100, vcc, s2, v66
	s_mov_b32 s2, 0x2a3000
	s_nop 0
	v_addc_co_u32_e32 v101, vcc, 0, v67, vcc
	v_add_co_u32_e32 v110, vcc, s2, v66
	s_mov_b32 s2, 0x2ac000
	s_nop 0
	v_addc_co_u32_e32 v111, vcc, 0, v67, vcc
	v_add_co_u32_e32 v112, vcc, s2, v66
	s_mov_b32 s2, 0x2b5000
	s_nop 0
	v_addc_co_u32_e32 v113, vcc, 0, v67, vcc
	v_add_co_u32_e32 v122, vcc, s2, v66
	s_mov_b32 s2, 0x2be000
	s_nop 0
	v_addc_co_u32_e32 v123, vcc, 0, v67, vcc
	v_add_co_u32_e32 v124, vcc, s2, v66
	s_mov_b32 s2, 0x2c7000
	s_nop 0
	v_addc_co_u32_e32 v125, vcc, 0, v67, vcc
	v_add_co_u32_e32 v126, vcc, s2, v66
	global_load_dwordx4 v[42:45], v[42:43], off nt
	s_nop 0
	global_load_dwordx4 v[50:53], v[50:51], off nt
	v_addc_co_u32_e32 v127, vcc, 0, v67, vcc
	global_load_dwordx4 v[58:61], v[58:59], off nt
	s_nop 0
	global_load_dwordx4 v[62:65], v[62:63], off nt
	s_nop 0
	global_load_dwordx4 v[66:69], v[68:69], off nt
	s_nop 0
	global_load_dwordx4 v[74:77], v[70:71], off nt
	global_load_dwordx4 v[86:89], v[72:73], off nt
	global_load_dwordx4 v[102:105], v[78:79], off nt
	s_nop 0
	global_load_dwordx4 v[70:73], v[80:81], off nt
	s_nop 0
	global_load_dwordx4 v[78:81], v[82:83], off nt
	global_load_dwordx4 v[90:93], v[84:85], off nt
	global_load_dwordx4 v[106:109], v[94:95], off nt
	s_nop 0
	global_load_dwordx4 v[82:85], v[96:97], off nt
	s_nop 0
	global_load_dwordx4 v[94:97], v[98:99], off nt
	global_load_dwordx4 v[114:117], v[100:101], off nt
	global_load_dwordx4 v[118:121], v[110:111], off nt
	s_nop 0
	global_load_dwordx4 v[98:101], v[112:113], off nt
	s_nop 0
	global_load_dwordx4 v[110:113], v[122:123], off nt
	s_nop 0
	global_load_dwordx4 v[122:125], v[124:125], off nt
	s_nop 0
	global_load_dwordx4 v[126:129], v[126:127], off nt
	v_lshrrev_b32_e32 v136, 4, v198
	s_movk_i32 s2, 0x410
	v_mov_b32_e32 v134, s10
	v_lshlrev_b32_e32 v132, 2, v133
	v_add_u32_e32 v153, s10, v130
	v_mul_u32_u24_e32 v152, 0x410, v133
	v_mad_u32_u24 v155, v133, s2, v134
	v_mul_u32_u24_e32 v133, 0x104, v136
	v_lshl_add_u64 v[134:135], s[82:83], 0, v[130:131]
	s_mov_b64 s[2:3], 0xd8800000
	v_lshlrev_b32_e32 v130, 2, v132
	v_add_u32_e32 v153, v153, v133
	v_lshl_add_u64 v[132:133], v[134:135], 0, s[2:3]
	v_readlane_b32 s3, v252, 39
	s_lshl_b32 s2, s3, 3
	v_add_u32_e32 v151, s10, v1
	s_sub_i32 s23, 0, s2
	s_lshl_b32 s2, s3, 4
	v_or_b32_e32 v137, 64, v1
	v_or_b32_e32 v138, 4, v136
	v_or_b32_e32 v139, 8, v136
	v_or_b32_e32 v140, 12, v136
	v_or_b32_e32 v141, 16, v136
	v_or_b32_e32 v142, 20, v136
	v_or_b32_e32 v143, 24, v136
	v_or_b32_e32 v144, 28, v136
	v_or_b32_e32 v145, 32, v136
	v_or_b32_e32 v146, 36, v136
	v_or_b32_e32 v147, 40, v136
	v_or_b32_e32 v148, 44, v136
	v_or_b32_e32 v149, 48, v136
	v_or_b32_e32 v150, 52, v136
	v_add_u32_e32 v151, v151, v152
	v_or_b32_e32 v152, 56, v136
	v_or_b32_e32 v154, 60, v136
	s_sub_i32 s24, s85, s2
	s_mov_b32 s25, 0x4a4000
	s_mov_b32 s26, 0x4ad000
	s_mov_b32 s27, 0x4b6000
	s_mov_b32 s28, 0x4bf000
	s_mov_b32 s29, 0x4c8000
	s_mov_b32 s30, 0x4d1000
	s_mov_b32 s31, 0x4da000
	s_mov_b32 s33, 0x4e3000
	s_mov_b32 s34, 0x4ec000
	s_mov_b32 s35, 0x4f5000
	s_mov_b32 s37, 0x4fe000
	s_mov_b32 s38, 0x507000
	s_mov_b32 s39, 0x6c0000
	s_mov_b32 s40, 0x6c9000
	s_mov_b32 s41, 0x6d2000
	s_mov_b32 s42, 0x6db000
	s_mov_b32 s43, 0x6e4000
	s_mov_b32 s44, 0x6ed000
	s_mov_b32 s45, 0x6f6000
	s_mov_b32 s46, 0x6ff000
	s_mov_b32 s47, 0x708000
	s_mov_b32 s48, 0x711000
	s_mov_b32 s49, 0x71a000
	s_mov_b32 s50, 0x723000
	s_mov_b32 s51, 0x72c000
	s_mov_b32 s52, 0x735000
	s_mov_b32 s53, 0x73e000
	s_mov_b32 s54, 0x747000
	v_add_u32_e32 v155, v155, v1
	v_readlane_b32 s55, v252, 14
	s_branch .LBB0_50

.LBB0_50:
	s_waitcnt vmcnt(31)
	v_mul_f32_e32 v134, 0x42800000, v2
	s_waitcnt vmcnt(30)
	v_mul_f32_e32 v6, 0x42800000, v6
	v_mov_b32_e32 v2, v131
	v_cvt_pk_fp8_f32 v2, v134, v6
	v_mul_f32_e32 v3, 0x42800000, v3
	v_mul_f32_e32 v6, 0x42800000, v7
	v_mov_b32_e32 v7, v131
	v_cvt_pk_fp8_f32 v7, v3, v6
	s_waitcnt vmcnt(29)
	v_mul_f32_e32 v3, 0x42800000, v15
	s_waitcnt vmcnt(28)
	v_mul_f32_e32 v6, 0x42800000, v23
	v_mul_f32_e32 v14, 0x42800000, v14
	v_cvt_pk_fp8_f32 v7, v3, v6 op_sel:[0,0,1]
	v_mul_f32_e32 v3, 0x42800000, v4
	v_mul_f32_e32 v4, 0x42800000, v8
	v_mov_b32_e32 v6, v131
	v_cvt_pk_fp8_f32 v6, v3, v4
	v_mul_f32_e32 v3, 0x42800000, v5
	v_mul_f32_e32 v4, 0x42800000, v9
	v_mov_b32_e32 v5, v131
	v_cvt_pk_fp8_f32 v5, v3, v4
	v_mul_f32_e32 v3, 0x42800000, v17
	v_mul_f32_e32 v4, 0x42800000, v25
	s_waitcnt vmcnt(27)
	v_mul_f32_e32 v9, 0x42800000, v11
	v_cvt_pk_fp8_f32 v5, v3, v4 op_sel:[0,0,1]
	v_mul_f32_e32 v4, 0x42800000, v10
	s_waitcnt vmcnt(26)
	v_mul_f32_e32 v10, 0x42800000, v19
	v_mov_b32_e32 v11, v131
	v_mul_f32_e32 v22, 0x42800000, v22
	v_cvt_pk_fp8_f32 v11, v9, v10
	v_cvt_pk_fp8_f32 v2, v14, v22 op_sel:[0,0,1]
	v_mul_f32_e32 v8, 0x42800000, v16
	v_mul_f32_e32 v14, 0x42800000, v24
	v_cvt_pk_fp8_f32 v6, v8, v14 op_sel:[0,0,1]
	v_mul_f32_e32 v8, 0x42800000, v18
	v_mov_b32_e32 v3, v131
	v_cvt_pk_fp8_f32 v3, v4, v8
	s_waitcnt vmcnt(25)
	v_mul_f32_e32 v4, 0x42800000, v27
	s_waitcnt vmcnt(24)
	v_mul_f32_e32 v8, 0x42800000, v35
	v_cvt_pk_fp8_f32 v11, v4, v8 op_sel:[0,0,1]
	v_mul_f32_e32 v9, 0x42800000, v13
	v_mul_f32_e32 v10, 0x42800000, v21
	v_mul_f32_e32 v4, 0x42800000, v26
	ds_write2_b32 v151, v7, v11 offset0:65 offset1:66
	v_mov_b32_e32 v11, v131
	v_cvt_pk_fp8_f32 v11, v9, v10
	v_mul_f32_e32 v8, 0x42800000, v34
	v_cvt_pk_fp8_f32 v3, v4, v8 op_sel:[0,0,1]
	v_mul_f32_e32 v4, 0x42800000, v12
	v_mul_f32_e32 v8, 0x42800000, v20
	v_mov_b32_e32 v7, v131
	v_cvt_pk_fp8_f32 v7, v4, v8
	v_mul_f32_e32 v4, 0x42800000, v29
	v_mul_f32_e32 v8, 0x42800000, v37
	v_cvt_pk_fp8_f32 v11, v4, v8 op_sel:[0,0,1]
	v_mul_f32_e32 v4, 0x42800000, v28
	v_mul_f32_e32 v8, 0x42800000, v36
	v_cvt_pk_fp8_f32 v7, v4, v8 op_sel:[0,0,1]
	ds_write2_b32 v151, v5, v11 offset0:195 offset1:196
	s_waitcnt vmcnt(23)
	v_mul_f32_e32 v5, 0x42800000, v30
	s_waitcnt vmcnt(22)
	v_mul_f32_e32 v8, 0x42800000, v38
	v_mov_b32_e32 v4, v131
	v_cvt_pk_fp8_f32 v4, v5, v8
	v_mul_f32_e32 v5, 0x42800000, v31
	v_mul_f32_e32 v8, 0x42800000, v39
	v_mov_b32_e32 v11, v131
	v_cvt_pk_fp8_f32 v11, v5, v8
	s_waitcnt vmcnt(21)
	v_mul_f32_e32 v9, 0x42800000, v46
	s_waitcnt vmcnt(20)
	v_mul_f32_e32 v10, 0x42800000, v54
	v_mul_f32_e32 v5, 0x42800000, v47
	v_mul_f32_e32 v8, 0x42800000, v55
	v_cvt_pk_fp8_f32 v4, v9, v10 op_sel:[0,0,1]
	v_cvt_pk_fp8_f32 v11, v5, v8 op_sel:[0,0,1]
	v_mul_f32_e32 v5, 0x42800000, v32
	v_mul_f32_e32 v9, 0x42800000, v40
	v_mov_b32_e32 v8, v131
	v_cvt_pk_fp8_f32 v8, v5, v9
	v_mul_f32_e32 v5, 0x42800000, v33
	v_mul_f32_e32 v9, 0x42800000, v41
	v_mov_b32_e32 v13, v131
	v_cvt_pk_fp8_f32 v13, v5, v9
	s_add_i32 s2, s23, s55
	v_mul_f32_e32 v10, 0x42800000, v48
	v_mul_f32_e32 v12, 0x42800000, v56
	v_mul_f32_e32 v5, 0x42800000, v49
	v_mul_f32_e32 v9, 0x42800000, v57
	s_ashr_i32 s4, s2, 31
	v_cvt_pk_fp8_f32 v8, v10, v12 op_sel:[0,0,1]
	v_cvt_pk_fp8_f32 v13, v5, v9 op_sel:[0,0,1]
	s_waitcnt vmcnt(19)
	v_mul_f32_e32 v9, 0x42800000, v42
	s_waitcnt vmcnt(18)
	v_mul_f32_e32 v10, 0x42800000, v50
	v_mov_b32_e32 v5, v131
	s_lshr_b32 s4, s4, 23
	v_cvt_pk_fp8_f32 v5, v9, v10
	v_mul_f32_e32 v9, 0x42800000, v43
	v_mul_f32_e32 v10, 0x42800000, v51
	v_mov_b32_e32 v15, v131
	s_add_i32 s4, s2, s4
	v_cvt_pk_fp8_f32 v15, v9, v10
	s_and_b32 s4, s4, 0xfffffe00
	s_sub_i32 s2, s2, s4
	s_lshr_b32 s4, s2, 3
	s_waitcnt vmcnt(17)
	v_mul_f32_e32 v12, 0x42800000, v58
	s_waitcnt vmcnt(16)
	v_mul_f32_e32 v14, 0x42800000, v62
	v_mul_f32_e32 v9, 0x42800000, v59
	v_mul_f32_e32 v10, 0x42800000, v63
	s_bfe_i32 s5, s4, 0x80000
	v_cvt_pk_fp8_f32 v5, v12, v14 op_sel:[0,0,1]
	v_cvt_pk_fp8_f32 v15, v9, v10 op_sel:[0,0,1]
	v_mul_f32_e32 v10, 0x42800000, v44
	v_mul_f32_e32 v12, 0x42800000, v52
	v_mov_b32_e32 v9, v131
	s_bfe_u32 s5, s5, 0x2000d
	v_cvt_pk_fp8_f32 v9, v10, v12
	v_mul_f32_e32 v10, 0x42800000, v45
	v_mul_f32_e32 v12, 0x42800000, v53
	v_mov_b32_e32 v17, v131
	s_add_i32 s5, s4, s5
	v_cvt_pk_fp8_f32 v17, v10, v12
	s_bfe_i32 s6, s5, 0x80000
	s_and_b32 s5, s5, 0xfc
	s_sub_i32 s4, s4, s5
	v_mul_f32_e32 v14, 0x42800000, v60
	v_mul_f32_e32 v16, 0x42800000, v64
	s_sext_i32_i8 s4, s4
	s_lshl_b32 s56, s2, 6
	v_cvt_pk_fp8_f32 v9, v14, v16 op_sel:[0,0,1]
	v_mul_f32_e32 v10, 0x42800000, v61
	v_mul_f32_e32 v12, 0x42800000, v65
	s_lshl_b32 s4, s4, 9
	s_and_b32 s2, s56, 0x100
	v_cvt_pk_fp8_f32 v17, v10, v12 op_sel:[0,0,1]
	s_sext_i32_i16 s6, s6
	s_or_b32 s2, s4, s2
	ds_write_b128 v151, v[2:5]
	ds_write2_b32 v151, v11, v15 offset0:67 offset1:68
	ds_write2_b64 v151, v[6:7], v[8:9] offset0:65 offset1:66
	ds_write2_b32 v151, v13, v17 offset0:197 offset1:198
	v_or_b32_e32 v2, s2, v1
	s_ashr_i32 s57, s6, 2
	v_mul_i32_i24_e32 v2, 0x2400, v2
	s_lshl_b32 s4, s57, 8
	s_and_b32 s5, s56, 0xc0
	v_ashrrev_i32_e32 v3, 31, v2
	s_or_b32 s4, s4, s5
	v_lshl_add_u64 v[2:3], v[2:3], 2, s[0:1]
	s_ashr_i32 s5, s4, 31
	v_lshl_add_u64 v[2:3], s[4:5], 2, v[2:3]
	v_lshl_add_u64 v[134:135], v[2:3], 0, v[130:131]
	s_mov_b32 s5, 0x480000
	v_add_co_u32_e32 v2, vcc, s5, v134
	s_mov_b32 s5, 0x489000
	s_nop 0
	v_addc_co_u32_e32 v3, vcc, 0, v135, vcc
	v_add_co_u32_e32 v6, vcc, s5, v134
	s_mov_b32 s5, 0x492000
	s_nop 0
	v_addc_co_u32_e32 v7, vcc, 0, v135, vcc
	v_add_co_u32_e32 v10, vcc, s5, v134
	s_mov_b32 s5, 0x49b000
	s_nop 0
	v_addc_co_u32_e32 v11, vcc, 0, v135, vcc
	v_add_co_u32_e32 v12, vcc, s5, v134
	global_load_dwordx4 v[2:5], v[2:3], off nt
	s_nop 0
	global_load_dwordx4 v[6:9], v[6:7], off nt
	v_addc_co_u32_e32 v13, vcc, 0, v135, vcc
	global_load_dwordx4 v[14:17], v[10:11], off nt
	global_load_dwordx4 v[22:25], v[12:13], off nt
	v_add_co_u32_e32 v10, vcc, s25, v134
	s_waitcnt vmcnt(19)
	v_mul_f32_e32 v156, 0x42800000, v66
	v_addc_co_u32_e32 v11, vcc, 0, v135, vcc
	v_add_co_u32_e32 v18, vcc, s26, v134
	s_waitcnt vmcnt(18)
	v_mul_f32_e32 v74, 0x42800000, v74
	v_addc_co_u32_e32 v19, vcc, 0, v135, vcc
	v_add_co_u32_e32 v26, vcc, s27, v134
	v_mov_b32_e32 v66, v131
	s_nop 0
	v_addc_co_u32_e32 v27, vcc, 0, v135, vcc
	v_cvt_pk_fp8_f32 v66, v156, v74
	v_mul_f32_e32 v67, 0x42800000, v67
	v_mul_f32_e32 v74, 0x42800000, v75
	v_mov_b32_e32 v75, v131
	v_add_co_u32_e32 v30, vcc, s28, v134
	v_cvt_pk_fp8_f32 v75, v67, v74
	s_nop 0
	v_addc_co_u32_e32 v31, vcc, 0, v135, vcc
	global_load_dwordx4 v[10:13], v[10:11], off nt
	s_nop 0
	global_load_dwordx4 v[18:21], v[18:19], off nt
	s_nop 0
	global_load_dwordx4 v[26:29], v[26:27], off nt
	s_nop 0
	global_load_dwordx4 v[34:37], v[30:31], off nt
	v_add_co_u32_e32 v30, vcc, s29, v134
	s_waitcnt vmcnt(21)
	v_mul_f32_e32 v67, 0x42800000, v87
	v_addc_co_u32_e32 v31, vcc, 0, v135, vcc
	s_waitcnt vmcnt(20)
	v_mul_f32_e32 v74, 0x42800000, v103
	v_add_co_u32_e32 v38, vcc, s30, v134
	v_cvt_pk_fp8_f32 v75, v67, v74 op_sel:[0,0,1]
	v_mul_f32_e32 v67, 0x42800000, v68
	v_mul_f32_e32 v68, 0x42800000, v76
	v_mov_b32_e32 v74, v131
	v_addc_co_u32_e32 v39, vcc, 0, v135, vcc
	v_cvt_pk_fp8_f32 v74, v67, v68
	v_mul_f32_e32 v67, 0x42800000, v69
	v_mul_f32_e32 v68, 0x42800000, v77
	v_mov_b32_e32 v69, v131
	v_add_co_u32_e32 v42, vcc, s31, v134
	v_cvt_pk_fp8_f32 v69, v67, v68
	s_nop 0
	v_addc_co_u32_e32 v43, vcc, 0, v135, vcc
	v_mul_f32_e32 v86, 0x42800000, v86
	v_mul_f32_e32 v102, 0x42800000, v102
	v_add_co_u32_e32 v44, vcc, s33, v134
	v_cvt_pk_fp8_f32 v66, v86, v102 op_sel:[0,0,1]
	v_mul_f32_e32 v76, 0x42800000, v88
	v_mul_f32_e32 v86, 0x42800000, v104
	v_addc_co_u32_e32 v45, vcc, 0, v135, vcc
	v_cvt_pk_fp8_f32 v74, v76, v86 op_sel:[0,0,1]
	v_mul_f32_e32 v67, 0x42800000, v89
	v_mul_f32_e32 v68, 0x42800000, v105
	s_waitcnt vmcnt(19)
	v_mul_f32_e32 v71, 0x42800000, v71
	s_waitcnt vmcnt(18)
	v_mul_f32_e32 v76, 0x42800000, v79
	v_mov_b32_e32 v77, v131
	global_load_dwordx4 v[30:33], v[30:31], off nt
	s_nop 0
	global_load_dwordx4 v[38:41], v[38:39], off nt
	s_nop 0
	global_load_dwordx4 v[46:49], v[42:43], off nt
	global_load_dwordx4 v[54:57], v[44:45], off nt
	v_add_co_u32_e32 v42, vcc, s34, v134
	v_cvt_pk_fp8_f32 v69, v67, v68 op_sel:[0,0,1]
	v_mul_f32_e32 v68, 0x42800000, v70
	v_mul_f32_e32 v70, 0x42800000, v78
	v_mov_b32_e32 v67, v131
	v_cvt_pk_fp8_f32 v77, v71, v76
	v_addc_co_u32_e32 v43, vcc, 0, v135, vcc
	v_cvt_pk_fp8_f32 v67, v68, v70
	v_add_co_u32_e32 v50, vcc, s35, v134
	s_waitcnt vmcnt(21)
	v_mul_f32_e32 v68, 0x42800000, v91
	v_addc_co_u32_e32 v51, vcc, 0, v135, vcc
	s_waitcnt vmcnt(20)
	v_mul_f32_e32 v70, 0x42800000, v107
	v_add_co_u32_e32 v58, vcc, s37, v134
	v_cvt_pk_fp8_f32 v77, v68, v70 op_sel:[0,0,1]
	v_mul_f32_e32 v68, 0x42800000, v90
	v_mul_f32_e32 v70, 0x42800000, v106
	v_addc_co_u32_e32 v59, vcc, 0, v135, vcc
	v_cvt_pk_fp8_f32 v67, v68, v70 op_sel:[0,0,1]
	v_mul_f32_e32 v68, 0x42800000, v72
	v_mul_f32_e32 v71, 0x42800000, v73
	v_mul_f32_e32 v72, 0x42800000, v81
	v_mov_b32_e32 v73, v131
	v_add_co_u32_e32 v62, vcc, s38, v134
	v_cvt_pk_fp8_f32 v73, v71, v72
	s_nop 0
	v_addc_co_u32_e32 v63, vcc, 0, v135, vcc
	global_load_dwordx4 v[42:45], v[42:43], off nt
	s_nop 0
	global_load_dwordx4 v[50:53], v[50:51], off nt
	s_nop 0
	global_load_dwordx4 v[58:61], v[58:59], off nt
	s_nop 0
	global_load_dwordx4 v[62:65], v[62:63], off nt
	ds_write2_b32 v155, v75, v77 offset0:81 offset1:82
	v_mul_f32_e32 v70, 0x42800000, v80
	v_mov_b32_e32 v75, v131
	v_cvt_pk_fp8_f32 v75, v68, v70
	v_mul_f32_e32 v68, 0x42800000, v93
	v_mul_f32_e32 v70, 0x42800000, v109
	v_cvt_pk_fp8_f32 v73, v68, v70 op_sel:[0,0,1]
	v_mul_f32_e32 v68, 0x42800000, v92
	v_mul_f32_e32 v70, 0x42800000, v108
	v_cvt_pk_fp8_f32 v75, v68, v70 op_sel:[0,0,1]
	ds_write2_b32 v155, v69, v73 offset0:211 offset1:212
	s_waitcnt vmcnt(23)
	v_mul_f32_e32 v69, 0x42800000, v82
	s_waitcnt vmcnt(22)
	v_mul_f32_e32 v70, 0x42800000, v94
	v_mov_b32_e32 v68, v131
	v_cvt_pk_fp8_f32 v68, v69, v70
	v_mul_f32_e32 v69, 0x42800000, v83
	v_mul_f32_e32 v70, 0x42800000, v95
	v_mov_b32_e32 v73, v131
	v_cvt_pk_fp8_f32 v73, v69, v70
	s_waitcnt vmcnt(21)
	v_mul_f32_e32 v71, 0x42800000, v114
	s_waitcnt vmcnt(20)
	v_mul_f32_e32 v72, 0x42800000, v118
	v_mul_f32_e32 v69, 0x42800000, v115
	v_mul_f32_e32 v70, 0x42800000, v119
	v_cvt_pk_fp8_f32 v68, v71, v72 op_sel:[0,0,1]
	v_cvt_pk_fp8_f32 v73, v69, v70 op_sel:[0,0,1]
	v_mul_f32_e32 v69, 0x42800000, v84
	v_mul_f32_e32 v71, 0x42800000, v96
	v_mov_b32_e32 v70, v131
	v_cvt_pk_fp8_f32 v70, v69, v71
	v_mul_f32_e32 v69, 0x42800000, v85
	v_mul_f32_e32 v71, 0x42800000, v97
	v_mov_b32_e32 v77, v131
	v_cvt_pk_fp8_f32 v77, v69, v71
	v_mul_f32_e32 v72, 0x42800000, v116
	v_mul_f32_e32 v76, 0x42800000, v120
	v_mul_f32_e32 v69, 0x42800000, v117
	v_mul_f32_e32 v71, 0x42800000, v121
	v_cvt_pk_fp8_f32 v70, v72, v76 op_sel:[0,0,1]
	v_cvt_pk_fp8_f32 v77, v69, v71 op_sel:[0,0,1]
	s_waitcnt vmcnt(19)
	v_mul_f32_e32 v71, 0x42800000, v98
	s_waitcnt vmcnt(18)
	v_mul_f32_e32 v72, 0x42800000, v110
	v_mov_b32_e32 v69, v131
	v_cvt_pk_fp8_f32 v69, v71, v72
	v_mul_f32_e32 v71, 0x42800000, v99
	v_mul_f32_e32 v72, 0x42800000, v111
	v_mov_b32_e32 v79, v131
	v_cvt_pk_fp8_f32 v79, v71, v72
	s_waitcnt vmcnt(17)
	v_mul_f32_e32 v76, 0x42800000, v122
	s_waitcnt vmcnt(16)
	v_mul_f32_e32 v78, 0x42800000, v126
	v_mul_f32_e32 v71, 0x42800000, v123
	v_mul_f32_e32 v72, 0x42800000, v127
	v_cvt_pk_fp8_f32 v69, v76, v78 op_sel:[0,0,1]
	v_cvt_pk_fp8_f32 v79, v71, v72 op_sel:[0,0,1]
	v_mul_f32_e32 v72, 0x42800000, v100
	v_mul_f32_e32 v76, 0x42800000, v112
	v_mov_b32_e32 v71, v131
	v_cvt_pk_fp8_f32 v71, v72, v76
	v_mul_f32_e32 v72, 0x42800000, v101
	v_mul_f32_e32 v76, 0x42800000, v113
	v_mov_b32_e32 v81, v131
	v_cvt_pk_fp8_f32 v81, v72, v76
	v_mul_f32_e32 v78, 0x42800000, v124
	v_mul_f32_e32 v80, 0x42800000, v128
	v_cvt_pk_fp8_f32 v71, v78, v80 op_sel:[0,0,1]
	v_mul_f32_e32 v72, 0x42800000, v125
	v_mul_f32_e32 v76, 0x42800000, v129
	v_cvt_pk_fp8_f32 v81, v72, v76 op_sel:[0,0,1]
	ds_write_b128 v155, v[66:69] offset:64
	ds_write2_b32 v155, v73, v79 offset0:83 offset1:84
	ds_write2_b64 v155, v[74:75], v[70:71] offset0:73 offset1:74
	ds_write2_b32 v155, v77, v81 offset0:213 offset1:214
	v_add_co_u32_e32 v66, vcc, s39, v134
	v_mov_b32_e32 v156, v131
	s_nop 0
	v_addc_co_u32_e32 v67, vcc, 0, v135, vcc
	v_add_co_u32_e32 v70, vcc, s40, v134
	v_mov_b32_e32 v159, v131
	s_nop 0
	v_addc_co_u32_e32 v71, vcc, 0, v135, vcc
	global_load_dwordx4 v[66:69], v[66:67], off nt
	s_nop 0
	global_load_dwordx4 v[74:77], v[70:71], off nt
	v_add_co_u32_e32 v70, vcc, s41, v134
	s_waitcnt vmcnt(15)
	v_mul_f32_e32 v157, 0x42800000, v14
	v_addc_co_u32_e32 v71, vcc, 0, v135, vcc
	v_add_co_u32_e32 v72, vcc, s42, v134
	s_waitcnt vmcnt(14)
	v_mul_f32_e32 v158, 0x42800000, v22
	v_addc_co_u32_e32 v73, vcc, 0, v135, vcc
	global_load_dwordx4 v[86:89], v[70:71], off nt
	global_load_dwordx4 v[102:105], v[72:73], off nt
	v_add_co_u32_e32 v70, vcc, s43, v134
	v_mov_b32_e32 v161, v131
	s_nop 0
	v_addc_co_u32_e32 v71, vcc, 0, v135, vcc
	v_add_co_u32_e32 v78, vcc, s44, v134
	v_mul_f32_e32 v160, 0x42800000, v24
	s_nop 0
	v_addc_co_u32_e32 v79, vcc, 0, v135, vcc
	v_add_co_u32_e32 v82, vcc, s45, v134
	global_load_dwordx4 v[70:73], v[70:71], off nt
	s_nop 0
	global_load_dwordx4 v[78:81], v[78:79], off nt
	v_addc_co_u32_e32 v83, vcc, 0, v135, vcc
	v_add_co_u32_e32 v84, vcc, s46, v134
	s_waitcnt vmcnt(16)
	v_mul_f32_e32 v162, 0x42800000, v19
	v_addc_co_u32_e32 v85, vcc, 0, v135, vcc
	global_load_dwordx4 v[90:93], v[82:83], off nt
	global_load_dwordx4 v[106:109], v[84:85], off nt
	v_add_co_u32_e32 v82, vcc, s47, v134
	v_mov_b32_e32 v163, v131
	s_nop 0
	v_addc_co_u32_e32 v83, vcc, 0, v135, vcc
	v_add_co_u32_e32 v94, vcc, s48, v134
	s_waitcnt vmcnt(14)
	v_mul_f32_e32 v164, 0x42800000, v40
	v_addc_co_u32_e32 v95, vcc, 0, v135, vcc
	v_add_co_u32_e32 v98, vcc, s49, v134
	global_load_dwordx4 v[82:85], v[82:83], off nt
	s_nop 0
	global_load_dwordx4 v[94:97], v[94:95], off nt
	v_addc_co_u32_e32 v99, vcc, 0, v135, vcc
	v_add_co_u32_e32 v100, vcc, s50, v134
	v_mov_b32_e32 v165, v131
	s_nop 0
	v_addc_co_u32_e32 v101, vcc, 0, v135, vcc
	global_load_dwordx4 v[114:117], v[98:99], off nt
	global_load_dwordx4 v[118:121], v[100:101], off nt
	v_add_co_u32_e32 v98, vcc, s51, v134
	s_waitcnt vmcnt(14)
	v_mul_f32_e32 v166, 0x42800000, v50
	v_addc_co_u32_e32 v99, vcc, 0, v135, vcc
	v_add_co_u32_e32 v110, vcc, s52, v134
	s_add_i32 s3, s24, s55
	s_nop 0
	v_addc_co_u32_e32 v111, vcc, 0, v135, vcc
	v_add_co_u32_e32 v122, vcc, s53, v134
	global_load_dwordx4 v[98:101], v[98:99], off nt
	s_nop 0
	global_load_dwordx4 v[110:113], v[110:111], off nt
	v_addc_co_u32_e32 v123, vcc, 0, v135, vcc
	v_add_co_u32_e32 v126, vcc, s54, v134
	v_mul_f32_e32 v134, 0x42800000, v2
	s_nop 0
	v_addc_co_u32_e32 v127, vcc, 0, v135, vcc
	global_load_dwordx4 v[122:125], v[122:123], off nt
	s_nop 0
	global_load_dwordx4 v[126:129], v[126:127], off nt
	v_mul_f32_e32 v135, 0x42800000, v6
	v_cvt_pk_fp8_f32 v156, v134, v135
	v_mul_f32_e32 v134, 0x42800000, v3
	v_mul_f32_e32 v135, 0x42800000, v7
	v_cvt_pk_fp8_f32 v159, v134, v135
	v_mul_f32_e32 v134, 0x42800000, v15
	v_mul_f32_e32 v135, 0x42800000, v23
	v_cvt_pk_fp8_f32 v156, v157, v158 op_sel:[0,0,1]
	v_cvt_pk_fp8_f32 v159, v134, v135 op_sel:[0,0,1]
	v_mul_f32_e32 v135, 0x42800000, v4
	v_mul_f32_e32 v157, 0x42800000, v8
	v_mov_b32_e32 v134, v131
	v_cvt_pk_fp8_f32 v134, v135, v157
	v_mul_f32_e32 v135, 0x42800000, v5
	v_mul_f32_e32 v157, 0x42800000, v9
	v_mul_f32_e32 v158, 0x42800000, v16
	v_cvt_pk_fp8_f32 v161, v135, v157
	v_cvt_pk_fp8_f32 v134, v158, v160 op_sel:[0,0,1]
	v_mul_f32_e32 v160, 0x42800000, v11
	v_cvt_pk_fp8_f32 v163, v160, v162
	v_mul_f32_e32 v135, 0x42800000, v17
	v_mul_f32_e32 v157, 0x42800000, v25
	v_cvt_pk_fp8_f32 v161, v135, v157 op_sel:[0,0,1]
	v_mul_f32_e32 v135, 0x42800000, v10
	v_mul_f32_e32 v158, 0x42800000, v18
	v_mov_b32_e32 v157, v131
	v_cvt_pk_fp8_f32 v157, v135, v158
	v_mul_f32_e32 v135, 0x42800000, v27
	v_mul_f32_e32 v158, 0x42800000, v35
	v_cvt_pk_fp8_f32 v163, v135, v158 op_sel:[0,0,1]
	v_mul_f32_e32 v135, 0x42800000, v26
	v_mul_f32_e32 v158, 0x42800000, v34
	v_cvt_pk_fp8_f32 v157, v135, v158 op_sel:[0,0,1]
	ds_write2_b32 v155, v159, v163 offset0:97 offset1:98
	v_mul_f32_e32 v158, 0x42800000, v12
	v_mul_f32_e32 v159, 0x42800000, v20
	v_mov_b32_e32 v135, v131
	v_cvt_pk_fp8_f32 v135, v158, v159
	v_mul_f32_e32 v158, 0x42800000, v13
	v_mul_f32_e32 v159, 0x42800000, v21
	v_mov_b32_e32 v163, v131
	v_cvt_pk_fp8_f32 v163, v158, v159
	v_mul_f32_e32 v160, 0x42800000, v28
	v_mul_f32_e32 v162, 0x42800000, v36
	v_mul_f32_e32 v158, 0x42800000, v29
	v_mul_f32_e32 v159, 0x42800000, v37
	v_cvt_pk_fp8_f32 v135, v160, v162 op_sel:[0,0,1]
	v_cvt_pk_fp8_f32 v163, v158, v159 op_sel:[0,0,1]
	v_mul_f32_e32 v159, 0x42800000, v30
	v_mul_f32_e32 v160, 0x42800000, v38
	v_mov_b32_e32 v158, v131
	v_cvt_pk_fp8_f32 v158, v159, v160
	v_mul_f32_e32 v159, 0x42800000, v46
	v_mul_f32_e32 v160, 0x42800000, v54
	ds_write2_b32 v155, v161, v163 offset0:227 offset1:228
	v_cvt_pk_fp8_f32 v158, v159, v160 op_sel:[0,0,1]
	v_mul_f32_e32 v159, 0x42800000, v31
	v_mul_f32_e32 v160, 0x42800000, v39
	v_mov_b32_e32 v163, v131
	v_cvt_pk_fp8_f32 v163, v159, v160
	v_mul_f32_e32 v159, 0x42800000, v32
	v_mov_b32_e32 v160, v131
	v_cvt_pk_fp8_f32 v160, v159, v164
	v_mul_f32_e32 v161, 0x42800000, v47
	v_mul_f32_e32 v162, 0x42800000, v55
	v_cvt_pk_fp8_f32 v163, v161, v162 op_sel:[0,0,1]
	v_mul_f32_e32 v159, 0x42800000, v48
	v_mul_f32_e32 v161, 0x42800000, v56
	v_cvt_pk_fp8_f32 v160, v159, v161 op_sel:[0,0,1]
	v_mul_f32_e32 v159, 0x42800000, v33
	v_mul_f32_e32 v161, 0x42800000, v41
	v_cvt_pk_fp8_f32 v165, v159, v161
	v_mul_f32_e32 v161, 0x42800000, v42
	v_mov_b32_e32 v159, v131
	v_cvt_pk_fp8_f32 v159, v161, v166
	v_mul_f32_e32 v162, 0x42800000, v49
	v_mul_f32_e32 v164, 0x42800000, v57
	v_cvt_pk_fp8_f32 v165, v162, v164 op_sel:[0,0,1]
	s_waitcnt vmcnt(17)
	v_mul_f32_e32 v161, 0x42800000, v58
	s_waitcnt vmcnt(16)
	v_mul_f32_e32 v162, 0x42800000, v62
	v_cvt_pk_fp8_f32 v159, v161, v162 op_sel:[0,0,1]
	v_mul_f32_e32 v161, 0x42800000, v43
	v_mul_f32_e32 v162, 0x42800000, v51
	v_mov_b32_e32 v164, v131
	v_cvt_pk_fp8_f32 v164, v161, v162
	ds_write_b128 v155, v[156:159] offset:128
	v_mul_f32_e32 v156, 0x42800000, v59
	v_mul_f32_e32 v157, 0x42800000, v63
	v_cvt_pk_fp8_f32 v164, v156, v157 op_sel:[0,0,1]
	v_mul_f32_e32 v156, 0x42800000, v44
	v_mul_f32_e32 v157, 0x42800000, v52
	v_mov_b32_e32 v161, v131
	v_cvt_pk_fp8_f32 v161, v156, v157
	v_mul_f32_e32 v156, 0x42800000, v60
	v_mul_f32_e32 v157, 0x42800000, v64
	v_mov_b32_e32 v158, v131
	v_cvt_pk_fp8_f32 v161, v156, v157 op_sel:[0,0,1]
	v_mul_f32_e32 v156, 0x42800000, v45
	v_mul_f32_e32 v157, 0x42800000, v53
	v_cvt_pk_fp8_f32 v158, v156, v157
	ds_write2_b64 v155, v[134:135], v[160:161] offset0:81 offset1:82
	v_mul_f32_e32 v134, 0x42800000, v61
	v_mul_f32_e32 v135, 0x42800000, v65
	v_cvt_pk_fp8_f32 v158, v134, v135 op_sel:[0,0,1]
	s_cmpk_lt_i32 s3, 0x200
	s_cselect_b64 s[6:7], -1, 0
	s_cmpk_gt_i32 s3, 0x1ff
	ds_write2_b32 v155, v163, v164 offset0:99 offset1:100
	ds_write2_b32 v155, v165, v158 offset0:229 offset1:230
	s_cbranch_scc1 .LBB0_52
	s_ashr_i32 s5, s3, 31
	s_lshr_b32 s5, s5, 23
	s_add_i32 s5, s3, s5
	s_and_b32 s5, s5, 0xfffffe00
	s_sub_i32 s5, s3, s5
	s_lshr_b32 s58, s5, 3
	s_bfe_i32 s59, s58, 0x80000
	s_bfe_u32 s59, s59, 0x2000d
	s_add_i32 s59, s58, s59
	s_bfe_i32 s60, s59, 0x80000
	s_and_b32 s59, s59, 0xfc
	s_sub_i32 s58, s58, s59
	s_sext_i32_i8 s58, s58
	s_lshl_b32 s5, s5, 6
	s_lshl_b32 s58, s58, 9
	s_and_b32 s59, s5, 0x100
	s_sext_i32_i16 s60, s60
	s_or_b32 s58, s58, s59
	v_or_b32_e32 v2, s58, v1
	s_lshl_b32 s58, s60, 6
	v_mul_i32_i24_e32 v2, 0x2400, v2
	s_and_b32 s58, s58, 0xffffff00
	s_and_b32 s5, s5, 0xc0
	v_ashrrev_i32_e32 v3, 31, v2
	s_or_b32 s58, s58, s5
	v_lshl_add_u64 v[2:3], v[2:3], 2, s[0:1]
	s_ashr_i32 s59, s58, 31
	v_lshl_add_u64 v[2:3], s[58:59], 2, v[2:3]
	v_lshl_add_u64 v[58:59], v[2:3], 0, v[130:131]
	v_add_co_u32_e32 v6, vcc, s11, v58
	s_nop 1
	v_addc_co_u32_e32 v7, vcc, 0, v59, vcc
	v_add_co_u32_e32 v10, vcc, s12, v58
	global_load_dwordx4 v[2:5], v[58:59], off nt
	s_nop 0
	global_load_dwordx4 v[6:9], v[6:7], off nt
	v_addc_co_u32_e32 v11, vcc, 0, v59, vcc
	v_add_co_u32_e32 v12, vcc, s13, v58
	s_nop 1
	v_addc_co_u32_e32 v13, vcc, 0, v59, vcc
	global_load_dwordx4 v[14:17], v[10:11], off nt
	global_load_dwordx4 v[22:25], v[12:13], off nt
	v_add_co_u32_e32 v10, vcc, s14, v58
	s_nop 1
	v_addc_co_u32_e32 v11, vcc, 0, v59, vcc
	v_add_co_u32_e32 v18, vcc, s15, v58
	s_nop 1
	v_addc_co_u32_e32 v19, vcc, 0, v59, vcc
	v_add_co_u32_e32 v26, vcc, s16, v58
	global_load_dwordx4 v[10:13], v[10:11], off nt
	s_nop 0
	global_load_dwordx4 v[18:21], v[18:19], off nt
	v_addc_co_u32_e32 v27, vcc, 0, v59, vcc
	v_add_co_u32_e32 v30, vcc, s17, v58
	s_nop 1
	v_addc_co_u32_e32 v31, vcc, 0, v59, vcc
	global_load_dwordx4 v[26:29], v[26:27], off nt
	s_nop 0
	global_load_dwordx4 v[34:37], v[30:31], off nt
	v_add_co_u32_e32 v30, vcc, s19, v58
	s_nop 1
	v_addc_co_u32_e32 v31, vcc, 0, v59, vcc
	v_add_co_u32_e32 v38, vcc, s20, v58
	s_nop 1
	v_addc_co_u32_e32 v39, vcc, 0, v59, vcc
	v_add_co_u32_e32 v42, vcc, s21, v58
	global_load_dwordx4 v[30:33], v[30:31], off nt
	s_nop 0
	global_load_dwordx4 v[38:41], v[38:39], off nt
	v_addc_co_u32_e32 v43, vcc, 0, v59, vcc
	v_add_co_u32_e32 v44, vcc, s22, v58
	s_nop 1
	v_addc_co_u32_e32 v45, vcc, 0, v59, vcc
	global_load_dwordx4 v[46:49], v[42:43], off nt
	global_load_dwordx4 v[54:57], v[44:45], off nt
	v_add_co_u32_e32 v42, vcc, 0x6c000, v58
	s_nop 1
	v_addc_co_u32_e32 v43, vcc, 0, v59, vcc
	v_add_co_u32_e32 v50, vcc, 0x75000, v58
	s_nop 1
	v_addc_co_u32_e32 v51, vcc, 0, v59, vcc
	v_add_co_u32_e32 v60, vcc, 0x7e000, v58
	global_load_dwordx4 v[42:45], v[42:43], off nt
	s_nop 0
	global_load_dwordx4 v[50:53], v[50:51], off nt
	v_addc_co_u32_e32 v61, vcc, 0, v59, vcc
	v_add_co_u32_e32 v62, vcc, 0x87000, v58
	s_nop 1
	v_addc_co_u32_e32 v63, vcc, 0, v59, vcc
	global_load_dwordx4 v[58:61], v[60:61], off nt
	s_nop 0
	global_load_dwordx4 v[62:65], v[62:63], off nt
.LBB0_52:
	s_waitcnt vmcnt(15)
	v_mul_f32_e32 v134, 0x42800000, v66
	s_waitcnt vmcnt(14)
	v_mul_f32_e32 v135, 0x42800000, v74
	v_mov_b32_e32 v156, v131
	v_cvt_pk_fp8_f32 v156, v134, v135
	v_mul_f32_e32 v134, 0x42800000, v67
	v_mul_f32_e32 v135, 0x42800000, v75
	v_mov_b32_e32 v159, v131
	v_cvt_pk_fp8_f32 v159, v134, v135
	s_waitcnt vmcnt(13)
	v_mul_f32_e32 v157, 0x42800000, v86
	s_waitcnt vmcnt(12)
	v_mul_f32_e32 v158, 0x42800000, v102
	v_mul_f32_e32 v134, 0x42800000, v87
	v_mul_f32_e32 v135, 0x42800000, v103
	v_cvt_pk_fp8_f32 v156, v157, v158 op_sel:[0,0,1]
	v_cvt_pk_fp8_f32 v159, v134, v135 op_sel:[0,0,1]
	v_mul_f32_e32 v135, 0x42800000, v68
	v_mul_f32_e32 v157, 0x42800000, v76
	v_mov_b32_e32 v134, v131
	v_cvt_pk_fp8_f32 v134, v135, v157
	v_mul_f32_e32 v135, 0x42800000, v69
	v_mul_f32_e32 v157, 0x42800000, v77
	v_mov_b32_e32 v161, v131
	v_mul_f32_e32 v158, 0x42800000, v88
	v_mul_f32_e32 v160, 0x42800000, v104
	v_cvt_pk_fp8_f32 v161, v135, v157
	v_cvt_pk_fp8_f32 v134, v158, v160 op_sel:[0,0,1]
	s_waitcnt vmcnt(11)
	v_mul_f32_e32 v160, 0x42800000, v71
	s_waitcnt vmcnt(10)
	v_mul_f32_e32 v162, 0x42800000, v79
	v_mov_b32_e32 v163, v131
	v_cvt_pk_fp8_f32 v163, v160, v162
	v_mul_f32_e32 v135, 0x42800000, v89
	v_mul_f32_e32 v157, 0x42800000, v105
	v_cvt_pk_fp8_f32 v161, v135, v157 op_sel:[0,0,1]
	v_mul_f32_e32 v135, 0x42800000, v70
	v_mul_f32_e32 v158, 0x42800000, v78
	v_mov_b32_e32 v157, v131
	v_cvt_pk_fp8_f32 v157, v135, v158
	s_waitcnt vmcnt(9)
	v_mul_f32_e32 v135, 0x42800000, v91
	s_waitcnt vmcnt(8)
	v_mul_f32_e32 v158, 0x42800000, v107
	v_cvt_pk_fp8_f32 v163, v135, v158 op_sel:[0,0,1]
	v_mul_f32_e32 v135, 0x42800000, v90
	v_mul_f32_e32 v158, 0x42800000, v106
	v_cvt_pk_fp8_f32 v157, v135, v158 op_sel:[0,0,1]
	ds_write2_b32 v155, v159, v163 offset0:113 offset1:114
	v_mul_f32_e32 v158, 0x42800000, v72
	v_mul_f32_e32 v159, 0x42800000, v80
	v_mov_b32_e32 v135, v131
	v_cvt_pk_fp8_f32 v135, v158, v159
	v_mul_f32_e32 v158, 0x42800000, v73
	v_mul_f32_e32 v159, 0x42800000, v81
	v_mov_b32_e32 v163, v131
	v_cvt_pk_fp8_f32 v163, v158, v159
	v_mul_f32_e32 v160, 0x42800000, v92
	v_mul_f32_e32 v162, 0x42800000, v108
	v_mul_f32_e32 v158, 0x42800000, v93
	v_mul_f32_e32 v159, 0x42800000, v109
	v_cvt_pk_fp8_f32 v135, v160, v162 op_sel:[0,0,1]
	v_cvt_pk_fp8_f32 v163, v158, v159 op_sel:[0,0,1]
	s_waitcnt vmcnt(7)
	v_mul_f32_e32 v159, 0x42800000, v82
	s_waitcnt vmcnt(6)
	v_mul_f32_e32 v160, 0x42800000, v94
	v_mov_b32_e32 v158, v131
	v_cvt_pk_fp8_f32 v158, v159, v160
	s_waitcnt vmcnt(5)
	v_mul_f32_e32 v159, 0x42800000, v114
	s_waitcnt vmcnt(4)
	v_mul_f32_e32 v160, 0x42800000, v118
	ds_write2_b32 v155, v161, v163 offset0:243 offset1:244
	v_cvt_pk_fp8_f32 v158, v159, v160 op_sel:[0,0,1]
	v_mul_f32_e32 v159, 0x42800000, v83
	v_mul_f32_e32 v160, 0x42800000, v95
	v_mov_b32_e32 v163, v131
	v_cvt_pk_fp8_f32 v163, v159, v160
	v_mul_f32_e32 v159, 0x42800000, v84
	v_mul_f32_e32 v164, 0x42800000, v96
	v_mov_b32_e32 v160, v131
	v_cvt_pk_fp8_f32 v160, v159, v164
	v_mul_f32_e32 v161, 0x42800000, v115
	v_mul_f32_e32 v162, 0x42800000, v119
	v_cvt_pk_fp8_f32 v163, v161, v162 op_sel:[0,0,1]
	v_mul_f32_e32 v159, 0x42800000, v116
	v_mul_f32_e32 v161, 0x42800000, v120
	v_cvt_pk_fp8_f32 v160, v159, v161 op_sel:[0,0,1]
	v_mul_f32_e32 v159, 0x42800000, v85
	v_mul_f32_e32 v161, 0x42800000, v97
	v_mov_b32_e32 v165, v131
	v_cvt_pk_fp8_f32 v165, v159, v161
	s_waitcnt vmcnt(3)
	v_mul_f32_e32 v161, 0x42800000, v98
	s_waitcnt vmcnt(2)
	v_mul_f32_e32 v166, 0x42800000, v110
	v_mov_b32_e32 v159, v131
	v_cvt_pk_fp8_f32 v159, v161, v166
	v_mul_f32_e32 v162, 0x42800000, v117
	v_mul_f32_e32 v164, 0x42800000, v121
	v_cvt_pk_fp8_f32 v165, v162, v164 op_sel:[0,0,1]
	s_waitcnt vmcnt(1)
	v_mul_f32_e32 v161, 0x42800000, v122
	s_waitcnt vmcnt(0)
	v_mul_f32_e32 v162, 0x42800000, v126
	v_cvt_pk_fp8_f32 v159, v161, v162 op_sel:[0,0,1]
	v_mul_f32_e32 v161, 0x42800000, v99
	v_mul_f32_e32 v162, 0x42800000, v111
	v_mov_b32_e32 v164, v131
	v_cvt_pk_fp8_f32 v164, v161, v162
	ds_write_b128 v155, v[156:159] offset:192
	v_mul_f32_e32 v156, 0x42800000, v123
	v_mul_f32_e32 v157, 0x42800000, v127
	v_cvt_pk_fp8_f32 v164, v156, v157 op_sel:[0,0,1]
	v_mul_f32_e32 v156, 0x42800000, v100
	v_mul_f32_e32 v157, 0x42800000, v112
	v_mov_b32_e32 v161, v131
	v_cvt_pk_fp8_f32 v161, v156, v157
	v_mul_f32_e32 v156, 0x42800000, v124
	v_mul_f32_e32 v157, 0x42800000, v128
	v_mov_b32_e32 v158, v131
	v_cvt_pk_fp8_f32 v161, v156, v157 op_sel:[0,0,1]
	v_mul_f32_e32 v156, 0x42800000, v101
	v_mul_f32_e32 v157, 0x42800000, v113
	v_cvt_pk_fp8_f32 v158, v156, v157
	ds_write2_b64 v155, v[134:135], v[160:161] offset0:89 offset1:90
	v_mul_f32_e32 v134, 0x42800000, v125
	v_mul_f32_e32 v135, 0x42800000, v129
	v_cvt_pk_fp8_f32 v158, v134, v135 op_sel:[0,0,1]
	s_andn2_b64 vcc, exec, s[6:7]
	ds_write2_b32 v155, v163, v164 offset0:115 offset1:116
	ds_write2_b32 v155, v165, v158 offset0:245 offset1:246
	s_cbranch_vccnz .LBB0_49
	s_ashr_i32 s5, s3, 31
	s_lshr_b32 s5, s5, 23
	s_add_i32 s5, s3, s5
	s_and_b32 s5, s5, 0xfffffe00
	s_sub_i32 s3, s3, s5
	s_lshr_b32 s5, s3, 3
	s_bfe_i32 s6, s5, 0x80000
	s_bfe_u32 s6, s6, 0x2000d
	s_add_i32 s6, s5, s6
	s_bfe_i32 s7, s6, 0x80000
	s_and_b32 s6, s6, 0xfc
	s_sub_i32 s5, s5, s6
	s_sext_i32_i8 s5, s5
	s_lshl_b32 s3, s3, 6
	s_lshl_b32 s5, s5, 9
	s_and_b32 s6, s3, 0x100
	s_sext_i32_i16 s7, s7
	s_or_b32 s5, s5, s6
	v_or_b32_e32 v66, s5, v137
	s_lshl_b32 s5, s7, 6
	v_mul_i32_i24_e32 v66, 0x2400, v66
	s_and_b32 s5, s5, 0xffffff00
	s_and_b32 s3, s3, 0xc0
	v_ashrrev_i32_e32 v67, 31, v66
	s_or_b32 s6, s5, s3
	v_lshl_add_u64 v[66:67], v[66:67], 2, s[0:1]
	s_ashr_i32 s7, s6, 31
	v_lshl_add_u64 v[66:67], s[6:7], 2, v[66:67]
	v_lshl_add_u64 v[122:123], v[66:67], 0, v[130:131]
	v_add_co_u32_e32 v70, vcc, s11, v122
	s_nop 1
	v_addc_co_u32_e32 v71, vcc, 0, v123, vcc
	global_load_dwordx4 v[66:69], v[122:123], off nt
	global_load_dwordx4 v[74:77], v[70:71], off nt
	v_add_co_u32_e32 v70, vcc, s12, v122
	s_nop 1
	v_addc_co_u32_e32 v71, vcc, 0, v123, vcc
	v_add_co_u32_e32 v72, vcc, s13, v122
	s_nop 1
	v_addc_co_u32_e32 v73, vcc, 0, v123, vcc
	global_load_dwordx4 v[86:89], v[70:71], off nt
	global_load_dwordx4 v[102:105], v[72:73], off nt
	v_add_co_u32_e32 v70, vcc, s14, v122
	s_nop 1
	v_addc_co_u32_e32 v71, vcc, 0, v123, vcc
	v_add_co_u32_e32 v78, vcc, s15, v122
	s_nop 1
	v_addc_co_u32_e32 v79, vcc, 0, v123, vcc
	v_add_co_u32_e32 v82, vcc, s16, v122
	global_load_dwordx4 v[70:73], v[70:71], off nt
	s_nop 0
	global_load_dwordx4 v[78:81], v[78:79], off nt
	v_addc_co_u32_e32 v83, vcc, 0, v123, vcc
	v_add_co_u32_e32 v84, vcc, s17, v122
	s_nop 1
	v_addc_co_u32_e32 v85, vcc, 0, v123, vcc
	global_load_dwordx4 v[90:93], v[82:83], off nt
	global_load_dwordx4 v[106:109], v[84:85], off nt
	v_add_co_u32_e32 v82, vcc, s19, v122
	s_nop 1
	v_addc_co_u32_e32 v83, vcc, 0, v123, vcc
	v_add_co_u32_e32 v94, vcc, s20, v122
	s_nop 1
	v_addc_co_u32_e32 v95, vcc, 0, v123, vcc
	v_add_co_u32_e32 v98, vcc, s21, v122
	global_load_dwordx4 v[82:85], v[82:83], off nt
	s_nop 0
	global_load_dwordx4 v[94:97], v[94:95], off nt
	v_addc_co_u32_e32 v99, vcc, 0, v123, vcc
	v_add_co_u32_e32 v100, vcc, s22, v122
	s_nop 1
	v_addc_co_u32_e32 v101, vcc, 0, v123, vcc
	global_load_dwordx4 v[114:117], v[98:99], off nt
	global_load_dwordx4 v[118:121], v[100:101], off nt
	v_add_co_u32_e32 v98, vcc, 0x6c000, v122
	s_nop 1
	v_addc_co_u32_e32 v99, vcc, 0, v123, vcc
	v_add_co_u32_e32 v110, vcc, 0x75000, v122
	s_nop 1
	v_addc_co_u32_e32 v111, vcc, 0, v123, vcc
	v_add_co_u32_e32 v124, vcc, 0x7e000, v122
	global_load_dwordx4 v[98:101], v[98:99], off nt
	s_nop 0
	global_load_dwordx4 v[110:113], v[110:111], off nt
	v_addc_co_u32_e32 v125, vcc, 0, v123, vcc
	v_add_co_u32_e32 v126, vcc, 0x87000, v122
	s_nop 1
	v_addc_co_u32_e32 v127, vcc, 0, v123, vcc
	global_load_dwordx4 v[122:125], v[124:125], off nt
	s_nop 0
	global_load_dwordx4 v[126:129], v[126:127], off nt
	s_branch .LBB0_49

.LBB0_56:
.LBB0_57:
	s_ashr_i32 s0, s9, 31
	s_lshr_b32 s0, s0, 25
	s_add_i32 s0, s9, s0
	s_and_b32 s0, s0, 0xff80
	s_sub_i32 s2, s9, s0
	s_bfe_i32 s0, s2, 0x80000
	s_bfe_u32 s0, s0, 0x5000a
	s_add_i32 s3, s2, s0
	s_bfe_i32 s0, s3, 0x80000
	s_sext_i32_i16 s0, s0
	s_lshl_b32 s0, s0, 1
	s_andn2_b32 s0, s0, 63
	s_ashr_i32 s1, s0, 31
	s_lshl_b64 s[0:1], s[0:1], 13
	v_readlane_b32 s4, v252, 35
	v_readlane_b32 s5, v252, 36
	s_add_u32 s4, s4, s0
	s_addc_u32 s5, s5, s1
	s_and_b32 s0, s3, 0xe0
	s_sub_i32 s0, s2, s0
	s_sext_i32_i8 s0, s0
	s_lshl_b32 s0, s0, 6
	s_ashr_i32 s1, s0, 31
	s_lshl_b64 s[0:1], s[0:1], 2
	s_add_u32 s0, s4, s0
	s_addc_u32 s1, s5, s1
	v_mov_b32_e32 v3, 0
	v_lshlrev_b32_e32 v2, 2, v198
	v_lshl_add_u64 v[4:5], s[0:1], 0, v[2:3]
	global_load_dword v1, v2, s[0:1] nt
	s_movk_i32 s0, 0x2000
	v_add_co_u32_e32 v6, vcc, s0, v4
	s_movk_i32 s1, 0x4000
	s_nop 0
	v_addc_co_u32_e32 v7, vcc, 0, v5, vcc
	global_load_dword v8, v[6:7], off nt
	v_add_co_u32_e32 v6, vcc, s1, v4
	s_movk_i32 s2, 0x6000
	s_nop 0
	v_addc_co_u32_e32 v7, vcc, 0, v5, vcc
	global_load_dword v9, v[6:7], off nt
	v_add_co_u32_e32 v6, vcc, s2, v4
	s_mov_b32 s3, 0x8000
	s_nop 0
	v_addc_co_u32_e32 v7, vcc, 0, v5, vcc
	global_load_dword v10, v[6:7], off nt
	v_add_co_u32_e32 v6, vcc, s3, v4
	s_mov_b32 s4, 0xa000
	s_nop 0
	v_addc_co_u32_e32 v7, vcc, 0, v5, vcc
	global_load_dword v11, v[6:7], off nt
	v_add_co_u32_e32 v6, vcc, s4, v4
	s_mov_b32 s5, 0xc000
	s_nop 0
	v_addc_co_u32_e32 v7, vcc, 0, v5, vcc
	global_load_dword v12, v[6:7], off nt
	v_add_co_u32_e32 v6, vcc, s5, v4
	s_mov_b32 s6, 0xe000
	s_nop 0
	v_addc_co_u32_e32 v7, vcc, 0, v5, vcc
	global_load_dword v13, v[6:7], off nt
	v_add_co_u32_e32 v6, vcc, s6, v4
	s_mov_b32 s7, 0x10000
	s_nop 0
	v_addc_co_u32_e32 v7, vcc, 0, v5, vcc
	global_load_dword v14, v[6:7], off nt
	v_add_co_u32_e32 v6, vcc, s7, v4
	s_mov_b32 s11, 0x12000
	s_nop 0
	v_addc_co_u32_e32 v7, vcc, 0, v5, vcc
	global_load_dword v15, v[6:7], off nt
	v_add_co_u32_e32 v6, vcc, s11, v4
	s_mov_b32 s12, 0x14000
	s_nop 0
	v_addc_co_u32_e32 v7, vcc, 0, v5, vcc
	global_load_dword v16, v[6:7], off nt
	v_add_co_u32_e32 v6, vcc, s12, v4
	s_mov_b32 s13, 0x16000
	s_nop 0
	v_addc_co_u32_e32 v7, vcc, 0, v5, vcc
	global_load_dword v17, v[6:7], off nt
	v_add_co_u32_e32 v6, vcc, s13, v4
	s_mov_b32 s14, 0x18000
	s_nop 0
	v_addc_co_u32_e32 v7, vcc, 0, v5, vcc
	global_load_dword v18, v[6:7], off nt
	v_add_co_u32_e32 v6, vcc, s14, v4
	s_mov_b32 s15, 0x1a000
	s_nop 0
	v_addc_co_u32_e32 v7, vcc, 0, v5, vcc
	global_load_dword v19, v[6:7], off nt
	v_add_co_u32_e32 v6, vcc, s15, v4
	s_mov_b32 s16, 0x1c000
	s_nop 0
	v_addc_co_u32_e32 v7, vcc, 0, v5, vcc
	global_load_dword v20, v[6:7], off nt
	v_add_co_u32_e32 v6, vcc, s16, v4
	s_mov_b32 s17, 0x1e000
	s_nop 0
	v_addc_co_u32_e32 v7, vcc, 0, v5, vcc
	global_load_dword v21, v[6:7], off nt
	v_add_co_u32_e32 v6, vcc, s17, v4
	s_mov_b32 s19, 0x20000
	s_nop 0
	v_addc_co_u32_e32 v7, vcc, 0, v5, vcc
	global_load_dword v22, v[6:7], off nt
	v_add_co_u32_e32 v6, vcc, s19, v4
	s_mov_b32 s20, 0x22000
	s_nop 0
	v_addc_co_u32_e32 v7, vcc, 0, v5, vcc
	global_load_dword v23, v[6:7], off nt
	v_add_co_u32_e32 v6, vcc, s20, v4
	s_mov_b32 s21, 0x24000
	s_nop 0
	v_addc_co_u32_e32 v7, vcc, 0, v5, vcc
	global_load_dword v24, v[6:7], off nt
	v_add_co_u32_e32 v6, vcc, s21, v4
	s_mov_b32 s22, 0x26000
	s_nop 0
	v_addc_co_u32_e32 v7, vcc, 0, v5, vcc
	global_load_dword v25, v[6:7], off nt
	v_add_co_u32_e32 v6, vcc, s22, v4
	s_mov_b32 s23, 0x28000
	s_nop 0
	v_addc_co_u32_e32 v7, vcc, 0, v5, vcc
	global_load_dword v26, v[6:7], off nt
	v_add_co_u32_e32 v6, vcc, s23, v4
	s_mov_b32 s24, 0x2a000
	s_nop 0
	v_addc_co_u32_e32 v7, vcc, 0, v5, vcc
	global_load_dword v27, v[6:7], off nt
	v_add_co_u32_e32 v6, vcc, s24, v4
	s_mov_b32 s25, 0x2c000
	s_nop 0
	v_addc_co_u32_e32 v7, vcc, 0, v5, vcc
	global_load_dword v28, v[6:7], off nt
	v_add_co_u32_e32 v6, vcc, s25, v4
	s_mov_b32 s26, 0x2e000
	s_nop 0
	v_addc_co_u32_e32 v7, vcc, 0, v5, vcc
	global_load_dword v29, v[6:7], off nt
	v_add_co_u32_e32 v6, vcc, s26, v4
	s_mov_b32 s27, 0x30000
	s_nop 0
	v_addc_co_u32_e32 v7, vcc, 0, v5, vcc
	global_load_dword v30, v[6:7], off nt
	v_add_co_u32_e32 v6, vcc, s27, v4
	s_mov_b32 s28, 0x32000
	s_nop 0
	v_addc_co_u32_e32 v7, vcc, 0, v5, vcc
	global_load_dword v31, v[6:7], off nt
	v_add_co_u32_e32 v6, vcc, s28, v4
	s_mov_b32 s29, 0x34000
	s_nop 0
	v_addc_co_u32_e32 v7, vcc, 0, v5, vcc
	global_load_dword v32, v[6:7], off nt
	v_add_co_u32_e32 v6, vcc, s29, v4
	s_mov_b32 s30, 0x36000
	s_nop 0
	v_addc_co_u32_e32 v7, vcc, 0, v5, vcc
	global_load_dword v33, v[6:7], off nt
	v_add_co_u32_e32 v6, vcc, s30, v4
	s_mov_b32 s31, 0x38000
	s_nop 0
	v_addc_co_u32_e32 v7, vcc, 0, v5, vcc
	global_load_dword v34, v[6:7], off nt
	v_add_co_u32_e32 v6, vcc, s31, v4
	s_mov_b32 s33, 0x3a000
	s_nop 0
	v_addc_co_u32_e32 v7, vcc, 0, v5, vcc
	global_load_dword v35, v[6:7], off nt
	v_add_co_u32_e32 v6, vcc, s33, v4
	s_mov_b32 s34, 0x3c000
	s_nop 0
	v_addc_co_u32_e32 v7, vcc, 0, v5, vcc
	global_load_dword v36, v[6:7], off nt
	v_add_co_u32_e32 v6, vcc, s34, v4
	s_mov_b32 s35, 0x3e000
	s_nop 0
	v_addc_co_u32_e32 v7, vcc, 0, v5, vcc
	global_load_dword v37, v[6:7], off nt
	v_add_co_u32_e32 v6, vcc, s35, v4
	s_mov_b32 s37, 0x40000
	s_nop 0
	v_addc_co_u32_e32 v7, vcc, 0, v5, vcc
	global_load_dword v38, v[6:7], off nt
	v_add_co_u32_e32 v6, vcc, s37, v4
	s_mov_b32 s38, 0x42000
	s_nop 0
	v_addc_co_u32_e32 v7, vcc, 0, v5, vcc
	global_load_dword v42, v[6:7], off nt
	v_add_co_u32_e32 v6, vcc, s38, v4
	s_mov_b32 s39, 0x44000
	s_nop 0
	v_addc_co_u32_e32 v7, vcc, 0, v5, vcc
	global_load_dword v50, v[6:7], off nt
	v_add_co_u32_e32 v6, vcc, s39, v4
	s_mov_b32 s40, 0x46000
	s_nop 0
	v_addc_co_u32_e32 v7, vcc, 0, v5, vcc
	global_load_dword v51, v[6:7], off nt
	v_add_co_u32_e32 v6, vcc, s40, v4
	s_mov_b32 s41, 0x48000
	s_nop 0
	v_addc_co_u32_e32 v7, vcc, 0, v5, vcc
	global_load_dword v52, v[6:7], off nt
	v_add_co_u32_e32 v6, vcc, s41, v4
	s_mov_b32 s42, 0x4a000
	s_nop 0
	v_addc_co_u32_e32 v7, vcc, 0, v5, vcc
	global_load_dword v53, v[6:7], off nt
	v_add_co_u32_e32 v6, vcc, s42, v4
	s_mov_b32 s43, 0x4c000
	s_nop 0
	v_addc_co_u32_e32 v7, vcc, 0, v5, vcc
	global_load_dword v54, v[6:7], off nt
	v_add_co_u32_e32 v6, vcc, s43, v4
	s_mov_b32 s44, 0x4e000
	s_nop 0
	v_addc_co_u32_e32 v7, vcc, 0, v5, vcc
	global_load_dword v55, v[6:7], off nt
	v_add_co_u32_e32 v6, vcc, s44, v4
	s_mov_b32 s45, 0x50000
	s_nop 0
	v_addc_co_u32_e32 v7, vcc, 0, v5, vcc
	global_load_dword v56, v[6:7], off nt
	v_add_co_u32_e32 v6, vcc, s45, v4
	s_mov_b32 s46, 0x52000
	s_nop 0
	v_addc_co_u32_e32 v7, vcc, 0, v5, vcc
	global_load_dword v57, v[6:7], off nt
	v_add_co_u32_e32 v6, vcc, s46, v4
	s_mov_b32 s47, 0x54000
	s_nop 0
	v_addc_co_u32_e32 v7, vcc, 0, v5, vcc
	global_load_dword v58, v[6:7], off nt
	v_add_co_u32_e32 v6, vcc, s47, v4
	s_mov_b32 s48, 0x56000
	s_nop 0
	v_addc_co_u32_e32 v7, vcc, 0, v5, vcc
	global_load_dword v59, v[6:7], off nt
	v_add_co_u32_e32 v6, vcc, s48, v4
	s_mov_b32 s49, 0x58000
	s_nop 0
	v_addc_co_u32_e32 v7, vcc, 0, v5, vcc
	global_load_dword v60, v[6:7], off nt
	v_add_co_u32_e32 v6, vcc, s49, v4
	s_mov_b32 s50, 0x5a000
	s_nop 0
	v_addc_co_u32_e32 v7, vcc, 0, v5, vcc
	global_load_dword v61, v[6:7], off nt
	v_add_co_u32_e32 v6, vcc, s50, v4
	s_mov_b32 s51, 0x5c000
	s_nop 0
	v_addc_co_u32_e32 v7, vcc, 0, v5, vcc
	global_load_dword v62, v[6:7], off nt
	v_add_co_u32_e32 v6, vcc, s51, v4
	s_mov_b32 s52, 0x5e000
	s_nop 0
	v_addc_co_u32_e32 v7, vcc, 0, v5, vcc
	global_load_dword v63, v[6:7], off nt
	v_add_co_u32_e32 v6, vcc, s52, v4
	s_mov_b32 s53, 0x60000
	s_nop 0
	v_addc_co_u32_e32 v7, vcc, 0, v5, vcc
	global_load_dword v64, v[6:7], off nt
	v_add_co_u32_e32 v6, vcc, s53, v4
	s_mov_b32 s54, 0x62000
	s_nop 0
	v_addc_co_u32_e32 v7, vcc, 0, v5, vcc
	global_load_dword v65, v[6:7], off nt
	v_add_co_u32_e32 v6, vcc, s54, v4
	s_mov_b32 s55, 0x64000
	s_nop 0
	v_addc_co_u32_e32 v7, vcc, 0, v5, vcc
	global_load_dword v66, v[6:7], off nt
	v_add_co_u32_e32 v6, vcc, s55, v4
	s_mov_b32 s56, 0x66000
	s_nop 0
	v_addc_co_u32_e32 v7, vcc, 0, v5, vcc
	global_load_dword v67, v[6:7], off nt
	v_add_co_u32_e32 v6, vcc, s56, v4
	s_mov_b32 s57, 0x68000
	s_nop 0
	v_addc_co_u32_e32 v7, vcc, 0, v5, vcc
	global_load_dword v68, v[6:7], off nt
	v_add_co_u32_e32 v6, vcc, s57, v4
	s_mov_b32 s58, 0x6a000
	s_nop 0
	v_addc_co_u32_e32 v7, vcc, 0, v5, vcc
	global_load_dword v69, v[6:7], off nt
	v_add_co_u32_e32 v6, vcc, s58, v4
	s_mov_b32 s59, 0x6c000
	s_nop 0
	v_addc_co_u32_e32 v7, vcc, 0, v5, vcc
	global_load_dword v70, v[6:7], off nt
	v_add_co_u32_e32 v6, vcc, s59, v4
	s_mov_b32 s60, 0x6e000
	s_nop 0
	v_addc_co_u32_e32 v7, vcc, 0, v5, vcc
	global_load_dword v71, v[6:7], off nt
	v_add_co_u32_e32 v6, vcc, s60, v4
	s_mov_b32 s61, 0x70000
	s_nop 0
	v_addc_co_u32_e32 v7, vcc, 0, v5, vcc
	global_load_dword v72, v[6:7], off nt
	v_add_co_u32_e32 v6, vcc, s61, v4
	s_mov_b32 s62, 0x72000
	s_nop 0
	v_addc_co_u32_e32 v7, vcc, 0, v5, vcc
	global_load_dword v73, v[6:7], off nt
	v_add_co_u32_e32 v6, vcc, s62, v4
	s_mov_b32 s63, 0x74000
	s_nop 0
	v_addc_co_u32_e32 v7, vcc, 0, v5, vcc
	global_load_dword v74, v[6:7], off nt
	v_add_co_u32_e32 v6, vcc, s63, v4
	s_mov_b32 s64, 0x76000
	s_nop 0
	v_addc_co_u32_e32 v7, vcc, 0, v5, vcc
	global_load_dword v75, v[6:7], off nt
	v_add_co_u32_e32 v6, vcc, s64, v4
	s_mov_b32 s65, 0x78000
	s_nop 0
	v_addc_co_u32_e32 v7, vcc, 0, v5, vcc
	global_load_dword v76, v[6:7], off nt
	v_add_co_u32_e32 v6, vcc, s65, v4
	s_mov_b32 s65, 0x7a000
	s_nop 0
	v_addc_co_u32_e32 v7, vcc, 0, v5, vcc
	global_load_dword v77, v[6:7], off nt
	v_add_co_u32_e32 v6, vcc, s65, v4
	s_mov_b32 s65, 0x7c000
	s_nop 0
	v_addc_co_u32_e32 v7, vcc, 0, v5, vcc
	global_load_dword v78, v[6:7], off nt
	v_add_co_u32_e32 v6, vcc, s65, v4
	s_mov_b32 s65, 0x7e000
	s_nop 0
	v_addc_co_u32_e32 v7, vcc, 0, v5, vcc
	v_add_co_u32_e32 v4, vcc, s65, v4
	global_load_dword v79, v[6:7], off nt
	s_nop 0
	v_addc_co_u32_e32 v5, vcc, 0, v5, vcc
	global_load_dword v80, v[4:5], off nt
	s_waitcnt vmcnt(62)
	v_add_u32_e32 v39, s10, v2
	v_lshlrev_b32_e32 v2, 3, v0
	v_and_b32_e32 v2, 56, v2
	v_lshrrev_b32_e32 v40, 3, v198
	v_mul_u32_u24_e32 v6, 0x104, v2
	v_lshlrev_b32_e32 v2, 1, v2
	v_lshl_add_u64 v[4:5], s[82:83], 0, v[2:3]
	v_lshlrev_b32_e32 v2, 2, v40
	v_readlane_b32 s65, v252, 39
	s_mov_b64 s[66:67], 0x3f00000
	v_add3_u32 v41, s10, v6, v2
	s_lshl_b32 s10, s65, 4
	s_lshl_b32 s65, s65, 3
	v_mov_b32_e32 v199, v3
	v_lshl_add_u64 v[4:5], v[4:5], 0, s[66:67]
	v_or_b32_e32 v43, 8, v40
	v_or_b32_e32 v44, 16, v40
	v_or_b32_e32 v45, 24, v40
	v_or_b32_e32 v46, 32, v40
	v_or_b32_e32 v47, 40, v40
	v_or_b32_e32 v48, 48, v40
	v_or_b32_e32 v49, 56, v40
	s_sub_i32 s10, s85, s10
	s_sub_i32 s65, 0, s65
	s_movk_i32 s66, 0x7fff
	s_mov_b32 s67, 0xffff0000
	v_readlane_b32 s68, v252, 14
	s_branch .LBB0_59

.LBB0_59:
	v_add_u32_e32 v2, 0x400, v39
	s_waitcnt vmcnt(62)
	ds_write2_b32 v39, v1, v8 offset1:65
	s_waitcnt vmcnt(60)
	ds_write2_b32 v39, v9, v10 offset0:130 offset1:195
	s_waitcnt vmcnt(58)
	ds_write2_b32 v2, v11, v12 offset0:4 offset1:69
	s_waitcnt vmcnt(56)
	ds_write2_b32 v2, v13, v14 offset0:134 offset1:199
	v_add_u32_e32 v2, 0x800, v39
	s_waitcnt vmcnt(54)
	ds_write2_b32 v2, v15, v16 offset0:8 offset1:73
	s_waitcnt vmcnt(52)
	ds_write2_b32 v2, v17, v18 offset0:138 offset1:203
	v_add_u32_e32 v2, 0xc00, v39
	s_waitcnt vmcnt(50)
	ds_write2_b32 v2, v19, v20 offset0:12 offset1:77
	s_waitcnt vmcnt(48)
	ds_write2_b32 v2, v21, v22 offset0:142 offset1:207
	v_add_u32_e32 v2, 0x1000, v39
	s_waitcnt vmcnt(46)
	ds_write2_b32 v2, v23, v24 offset0:16 offset1:81
	s_waitcnt vmcnt(44)
	ds_write2_b32 v2, v25, v26 offset0:146 offset1:211
	v_add_u32_e32 v2, 0x1400, v39
	s_waitcnt vmcnt(42)
	ds_write2_b32 v2, v27, v28 offset0:20 offset1:85
	s_waitcnt vmcnt(40)
	ds_write2_b32 v2, v29, v30 offset0:150 offset1:215
	v_add_u32_e32 v2, 0x1800, v39
	s_waitcnt vmcnt(38)
	ds_write2_b32 v2, v31, v32 offset0:24 offset1:89
	s_waitcnt vmcnt(36)
	ds_write2_b32 v2, v33, v34 offset0:154 offset1:219
	v_add_u32_e32 v2, 0x1c00, v39
	s_waitcnt vmcnt(34)
	ds_write2_b32 v2, v35, v36 offset0:28 offset1:93
	s_waitcnt vmcnt(32)
	ds_write2_b32 v2, v37, v38 offset0:158 offset1:223
	v_add_u32_e32 v2, 0x2000, v39
	s_waitcnt vmcnt(30)
	ds_write2_b32 v2, v42, v50 offset0:32 offset1:97
	s_waitcnt vmcnt(28)
	ds_write2_b32 v2, v51, v52 offset0:162 offset1:227
	v_add_u32_e32 v2, 0x2400, v39
	s_waitcnt vmcnt(26)
	ds_write2_b32 v2, v53, v54 offset0:36 offset1:101
	s_waitcnt vmcnt(24)
	ds_write2_b32 v2, v55, v56 offset0:166 offset1:231
	v_add_u32_e32 v2, 0x2800, v39
	s_waitcnt vmcnt(22)
	ds_write2_b32 v2, v57, v58 offset0:40 offset1:105
	s_waitcnt vmcnt(20)
	ds_write2_b32 v2, v59, v60 offset0:170 offset1:235
	v_add_u32_e32 v2, 0x2c00, v39
	s_waitcnt vmcnt(18)
	ds_write2_b32 v2, v61, v62 offset0:44 offset1:109
	s_waitcnt vmcnt(16)
	ds_write2_b32 v2, v63, v64 offset0:174 offset1:239
	v_add_u32_e32 v2, 0x3000, v39
	s_waitcnt vmcnt(14)
	ds_write2_b32 v2, v65, v66 offset0:48 offset1:113
	s_waitcnt vmcnt(12)
	ds_write2_b32 v2, v67, v68 offset0:178 offset1:243
	v_add_u32_e32 v2, 0x3400, v39
	s_waitcnt vmcnt(10)
	ds_write2_b32 v2, v69, v70 offset0:52 offset1:117
	s_waitcnt vmcnt(8)
	ds_write2_b32 v2, v71, v72 offset0:182 offset1:247
	v_add_u32_e32 v2, 0x3800, v39
	s_waitcnt vmcnt(6)
	ds_write2_b32 v2, v73, v74 offset0:56 offset1:121
	s_waitcnt vmcnt(4)
	ds_write2_b32 v2, v75, v76 offset0:186 offset1:251
	v_add_u32_e32 v2, 0x3c00, v39
	s_waitcnt vmcnt(2)
	ds_write2_b32 v2, v77, v78 offset0:60 offset1:125
	s_waitcnt vmcnt(0)
	ds_write2_b32 v2, v79, v80 offset0:190 offset1:255
	s_waitcnt lgkmcnt(0)
	s_add_i32 s69, s10, s68
	s_cmpk_gt_i32 s69, 0x7f
	s_cbranch_scc1 .LBB0_58
	s_ashr_i32 s70, s69, 31
	s_lshr_b32 s70, s70, 25
	s_add_i32 s70, s69, s70
	s_and_b32 s70, s70, 0xff80
	s_sub_i32 s69, s69, s70
	s_bfe_i32 s70, s69, 0x80000
	s_bfe_u32 s70, s70, 0x5000a
	s_add_i32 s72, s69, s70
	s_bfe_i32 s70, s72, 0x80000
	s_sext_i32_i16 s70, s70
	s_lshl_b32 s70, s70, 1
	s_andn2_b32 s70, s70, 63
	s_ashr_i32 s71, s70, 31
	s_lshl_b64 s[70:71], s[70:71], 13
	v_readlane_b32 s76, v252, 35
	v_readlane_b32 s77, v252, 36
	s_add_u32 s73, s76, s70
	s_addc_u32 s74, s77, s71
	s_and_b32 s70, s72, 0xe0
	s_sub_i32 s69, s69, s70
	s_sext_i32_i8 s69, s69
	s_lshl_b32 s70, s69, 6
	s_ashr_i32 s71, s70, 31
	s_lshl_b64 s[70:71], s[70:71], 2
	s_add_u32 s70, s73, s70
	s_addc_u32 s71, s74, s71
	v_lshlrev_b32_e32 v2, 2, v198
	v_lshl_add_u64 v[6:7], s[70:71], 0, v[2:3]
	v_add_co_u32_e32 v8, vcc, s0, v6
	global_load_dword v1, v2, s[70:71] nt
	s_nop 0
	v_addc_co_u32_e32 v9, vcc, 0, v7, vcc
	v_add_co_u32_e32 v10, vcc, s1, v6
	global_load_dword v8, v[8:9], off nt
	s_nop 0
	v_addc_co_u32_e32 v11, vcc, 0, v7, vcc
	global_load_dword v9, v[10:11], off nt
	v_add_co_u32_e32 v10, vcc, s2, v6
	s_nop 1
	v_addc_co_u32_e32 v11, vcc, 0, v7, vcc
	v_add_co_u32_e32 v12, vcc, s3, v6
	global_load_dword v10, v[10:11], off nt
	s_nop 0
	v_addc_co_u32_e32 v13, vcc, 0, v7, vcc
	global_load_dword v11, v[12:13], off nt
	v_add_co_u32_e32 v12, vcc, s4, v6
	s_nop 1
	v_addc_co_u32_e32 v13, vcc, 0, v7, vcc
	v_add_co_u32_e32 v14, vcc, s5, v6
	global_load_dword v12, v[12:13], off nt
	s_nop 0
	v_addc_co_u32_e32 v15, vcc, 0, v7, vcc
	global_load_dword v13, v[14:15], off nt
	v_add_co_u32_e32 v14, vcc, s6, v6
	s_nop 1
	v_addc_co_u32_e32 v15, vcc, 0, v7, vcc
	v_add_co_u32_e32 v16, vcc, s7, v6
	global_load_dword v14, v[14:15], off nt
	s_nop 0
	v_addc_co_u32_e32 v17, vcc, 0, v7, vcc
	global_load_dword v15, v[16:17], off nt
	v_add_co_u32_e32 v16, vcc, s11, v6
	s_nop 1
	v_addc_co_u32_e32 v17, vcc, 0, v7, vcc
	v_add_co_u32_e32 v18, vcc, s12, v6
	global_load_dword v16, v[16:17], off nt
	s_nop 0
	v_addc_co_u32_e32 v19, vcc, 0, v7, vcc
	global_load_dword v17, v[18:19], off nt
	v_add_co_u32_e32 v18, vcc, s13, v6
	s_nop 1
	v_addc_co_u32_e32 v19, vcc, 0, v7, vcc
	v_add_co_u32_e32 v20, vcc, s14, v6
	global_load_dword v18, v[18:19], off nt
	s_nop 0
	v_addc_co_u32_e32 v21, vcc, 0, v7, vcc
	global_load_dword v19, v[20:21], off nt
	v_add_co_u32_e32 v20, vcc, s15, v6
	s_nop 1
	v_addc_co_u32_e32 v21, vcc, 0, v7, vcc
	v_add_co_u32_e32 v22, vcc, s16, v6
	global_load_dword v20, v[20:21], off nt
	s_nop 0
	v_addc_co_u32_e32 v23, vcc, 0, v7, vcc
	global_load_dword v21, v[22:23], off nt
	v_add_co_u32_e32 v22, vcc, s17, v6
	s_nop 1
	v_addc_co_u32_e32 v23, vcc, 0, v7, vcc
	v_add_co_u32_e32 v24, vcc, s19, v6
	global_load_dword v22, v[22:23], off nt
	s_nop 0
	v_addc_co_u32_e32 v25, vcc, 0, v7, vcc
	global_load_dword v23, v[24:25], off nt
	v_add_co_u32_e32 v24, vcc, s20, v6
	s_nop 1
	v_addc_co_u32_e32 v25, vcc, 0, v7, vcc
	v_add_co_u32_e32 v26, vcc, s21, v6
	global_load_dword v24, v[24:25], off nt
	s_nop 0
	v_addc_co_u32_e32 v27, vcc, 0, v7, vcc
	global_load_dword v25, v[26:27], off nt
	v_add_co_u32_e32 v26, vcc, s22, v6
	s_nop 1
	v_addc_co_u32_e32 v27, vcc, 0, v7, vcc
	v_add_co_u32_e32 v28, vcc, s23, v6
	global_load_dword v26, v[26:27], off nt
	s_nop 0
	v_addc_co_u32_e32 v29, vcc, 0, v7, vcc
	global_load_dword v27, v[28:29], off nt
	v_add_co_u32_e32 v28, vcc, s24, v6
	s_nop 1
	v_addc_co_u32_e32 v29, vcc, 0, v7, vcc
	v_add_co_u32_e32 v30, vcc, s25, v6
	global_load_dword v28, v[28:29], off nt
	s_nop 0
	v_addc_co_u32_e32 v31, vcc, 0, v7, vcc
	global_load_dword v29, v[30:31], off nt
	v_add_co_u32_e32 v30, vcc, s26, v6
	s_nop 1
	v_addc_co_u32_e32 v31, vcc, 0, v7, vcc
	v_add_co_u32_e32 v32, vcc, s27, v6
	global_load_dword v30, v[30:31], off nt
	s_nop 0
	v_addc_co_u32_e32 v33, vcc, 0, v7, vcc
	global_load_dword v31, v[32:33], off nt
	v_add_co_u32_e32 v32, vcc, s28, v6
	s_nop 1
	v_addc_co_u32_e32 v33, vcc, 0, v7, vcc
	v_add_co_u32_e32 v34, vcc, s29, v6
	global_load_dword v32, v[32:33], off nt
	s_nop 0
	v_addc_co_u32_e32 v35, vcc, 0, v7, vcc
	global_load_dword v33, v[34:35], off nt
	v_add_co_u32_e32 v34, vcc, s30, v6
	s_nop 1
	v_addc_co_u32_e32 v35, vcc, 0, v7, vcc
	v_add_co_u32_e32 v36, vcc, s31, v6
	global_load_dword v34, v[34:35], off nt
	s_nop 0
	v_addc_co_u32_e32 v37, vcc, 0, v7, vcc
	global_load_dword v35, v[36:37], off nt
	v_add_co_u32_e32 v36, vcc, s33, v6
	s_nop 1
	v_addc_co_u32_e32 v37, vcc, 0, v7, vcc
	v_add_co_u32_e32 v50, vcc, s34, v6
	global_load_dword v36, v[36:37], off nt
	s_nop 0
	v_addc_co_u32_e32 v51, vcc, 0, v7, vcc
	global_load_dword v37, v[50:51], off nt
	v_add_co_u32_e32 v50, vcc, s35, v6
	s_nop 1
	v_addc_co_u32_e32 v51, vcc, 0, v7, vcc
	global_load_dword v38, v[50:51], off nt
	v_add_co_u32_e32 v50, vcc, s37, v6
	s_nop 1
	v_addc_co_u32_e32 v51, vcc, 0, v7, vcc
	global_load_dword v42, v[50:51], off nt
	v_add_co_u32_e32 v50, vcc, s38, v6
	s_nop 1
	v_addc_co_u32_e32 v51, vcc, 0, v7, vcc
	v_add_co_u32_e32 v52, vcc, s39, v6
	global_load_dword v50, v[50:51], off nt
	s_nop 0
	v_addc_co_u32_e32 v53, vcc, 0, v7, vcc
	global_load_dword v51, v[52:53], off nt
	v_add_co_u32_e32 v52, vcc, s40, v6
	s_nop 1
	v_addc_co_u32_e32 v53, vcc, 0, v7, vcc
	v_add_co_u32_e32 v54, vcc, s41, v6
	global_load_dword v52, v[52:53], off nt
	s_nop 0
	v_addc_co_u32_e32 v55, vcc, 0, v7, vcc
	global_load_dword v53, v[54:55], off nt
	v_add_co_u32_e32 v54, vcc, s42, v6
	s_nop 1
	v_addc_co_u32_e32 v55, vcc, 0, v7, vcc
	v_add_co_u32_e32 v56, vcc, s43, v6
	global_load_dword v54, v[54:55], off nt
	s_nop 0
	v_addc_co_u32_e32 v57, vcc, 0, v7, vcc
	global_load_dword v55, v[56:57], off nt
	v_add_co_u32_e32 v56, vcc, s44, v6
	s_nop 1
	v_addc_co_u32_e32 v57, vcc, 0, v7, vcc
	v_add_co_u32_e32 v58, vcc, s45, v6
	global_load_dword v56, v[56:57], off nt
	s_nop 0
	v_addc_co_u32_e32 v59, vcc, 0, v7, vcc
	global_load_dword v57, v[58:59], off nt
	v_add_co_u32_e32 v58, vcc, s46, v6
	s_nop 1
	v_addc_co_u32_e32 v59, vcc, 0, v7, vcc
	v_add_co_u32_e32 v60, vcc, s47, v6
	global_load_dword v58, v[58:59], off nt
	s_nop 0
	v_addc_co_u32_e32 v61, vcc, 0, v7, vcc
	global_load_dword v59, v[60:61], off nt
	v_add_co_u32_e32 v60, vcc, s48, v6
	s_nop 1
	v_addc_co_u32_e32 v61, vcc, 0, v7, vcc
	v_add_co_u32_e32 v62, vcc, s49, v6
	global_load_dword v60, v[60:61], off nt
	s_nop 0
	v_addc_co_u32_e32 v63, vcc, 0, v7, vcc
	global_load_dword v61, v[62:63], off nt
	v_add_co_u32_e32 v62, vcc, s50, v6
	s_nop 1
	v_addc_co_u32_e32 v63, vcc, 0, v7, vcc
	v_add_co_u32_e32 v64, vcc, s51, v6
	global_load_dword v62, v[62:63], off nt
	s_nop 0
	v_addc_co_u32_e32 v65, vcc, 0, v7, vcc
	global_load_dword v63, v[64:65], off nt
	v_add_co_u32_e32 v64, vcc, s52, v6
	s_nop 1
	v_addc_co_u32_e32 v65, vcc, 0, v7, vcc
	v_add_co_u32_e32 v66, vcc, s53, v6
	global_load_dword v64, v[64:65], off nt
	s_nop 0
	v_addc_co_u32_e32 v67, vcc, 0, v7, vcc
	global_load_dword v65, v[66:67], off nt
	v_add_co_u32_e32 v66, vcc, s54, v6
	s_nop 1
	v_addc_co_u32_e32 v67, vcc, 0, v7, vcc
	v_add_co_u32_e32 v68, vcc, s55, v6
	global_load_dword v66, v[66:67], off nt
	s_nop 0
	v_addc_co_u32_e32 v69, vcc, 0, v7, vcc
	global_load_dword v67, v[68:69], off nt
	v_add_co_u32_e32 v68, vcc, s56, v6
	s_nop 1
	v_addc_co_u32_e32 v69, vcc, 0, v7, vcc
	v_add_co_u32_e32 v70, vcc, s57, v6
	global_load_dword v68, v[68:69], off nt
	s_nop 0
	v_addc_co_u32_e32 v71, vcc, 0, v7, vcc
	global_load_dword v69, v[70:71], off nt
	v_add_co_u32_e32 v70, vcc, s58, v6
	s_nop 1
	v_addc_co_u32_e32 v71, vcc, 0, v7, vcc
	v_add_co_u32_e32 v72, vcc, s59, v6
	global_load_dword v70, v[70:71], off nt
	s_nop 0
	v_addc_co_u32_e32 v73, vcc, 0, v7, vcc
	global_load_dword v71, v[72:73], off nt
	v_add_co_u32_e32 v72, vcc, s60, v6
	s_nop 1
	v_addc_co_u32_e32 v73, vcc, 0, v7, vcc
	v_add_co_u32_e32 v74, vcc, s61, v6
	global_load_dword v72, v[72:73], off nt
	s_nop 0
	v_addc_co_u32_e32 v75, vcc, 0, v7, vcc
	global_load_dword v73, v[74:75], off nt
	v_add_co_u32_e32 v74, vcc, s62, v6
	s_nop 1
	v_addc_co_u32_e32 v75, vcc, 0, v7, vcc
	v_add_co_u32_e32 v76, vcc, s63, v6
	global_load_dword v74, v[74:75], off nt
	s_nop 0
	v_addc_co_u32_e32 v77, vcc, 0, v7, vcc
	global_load_dword v75, v[76:77], off nt
	v_add_co_u32_e32 v76, vcc, s64, v6
	s_nop 1
	v_addc_co_u32_e32 v77, vcc, 0, v7, vcc
	v_add_co_u32_e32 v78, vcc, 0x78000, v6
	global_load_dword v76, v[76:77], off nt
	s_nop 0
	v_addc_co_u32_e32 v79, vcc, 0, v7, vcc
	global_load_dword v77, v[78:79], off nt
	v_add_co_u32_e32 v78, vcc, 0x7a000, v6
	s_nop 1
	v_addc_co_u32_e32 v79, vcc, 0, v7, vcc
	v_add_co_u32_e32 v80, vcc, 0x7c000, v6
	global_load_dword v78, v[78:79], off nt
	s_nop 0
	v_addc_co_u32_e32 v81, vcc, 0, v7, vcc
	v_add_co_u32_e32 v6, vcc, 0x7e000, v6
	global_load_dword v79, v[80:81], off nt
	s_nop 0
	v_addc_co_u32_e32 v7, vcc, 0, v7, vcc
	global_load_dword v80, v[6:7], off nt
	s_branch .LBB0_58
.LBB0_61:
	v_readlane_b32 s2, v252, 37
	v_readlane_b32 s3, v252, 38
	s_and_b64 s[0:1], s[2:3], exec
	v_readlane_b32 s0, v252, 14
	s_cselect_b32 s0, s0, s9
	s_cmpk_gt_i32 s0, 0x3fff
	s_cbranch_scc1 .LBB0_70
	s_and_b64 s[2:3], s[2:3], exec
	s_cselect_b32 s19, s85, s8
	s_ashr_i32 s1, s0, 31
	s_lshl_b64 s[2:3], s[0:1], 13
	v_readlane_b32 s20, v252, 21
	v_readlane_b32 s21, v252, 22
	s_add_u32 s2, s20, s2
	s_waitcnt vmcnt(21)
	v_lshlrev_b64 v[66:67], 4, v[198:199]
	s_addc_u32 s3, s21, s3
	v_lshl_add_u64 v[18:19], s[2:3], 0, v[66:67]
	s_movk_i32 s2, 0x1000
	v_add_co_u32_e32 v34, vcc, s2, v18
	global_load_dwordx4 v[2:5], v[18:19], off nt
	global_load_dwordx4 v[6:9], v[18:19], off offset:1024 nt
	global_load_dwordx4 v[10:13], v[18:19], off offset:2048 nt
	global_load_dwordx4 v[14:17], v[18:19], off offset:3072 nt
	v_addc_co_u32_e32 v35, vcc, 0, v19, vcc
	global_load_dwordx4 v[18:21], v[34:35], off nt
	global_load_dwordx4 v[22:25], v[34:35], off offset:1024 nt
	global_load_dwordx4 v[26:29], v[34:35], off offset:2048 nt
	global_load_dwordx4 v[30:33], v[34:35], off offset:3072 nt
	v_mbcnt_lo_u32_b32 v1, -1, 0
	v_mbcnt_hi_u32_b32 v34, -1, v1
	v_and_b32_e32 v1, 64, v34
	v_add_u32_e32 v35, 64, v1
	v_xor_b32_e32 v1, 1, v34
	v_cmp_lt_i32_e32 vcc, v1, v35
	v_xor_b32_e32 v36, 2, v34
	v_readlane_b32 s26, v252, 27
	v_cndmask_b32_e32 v1, v34, v1, vcc
	v_cmp_lt_i32_e32 vcc, v36, v35
	v_readlane_b32 s27, v252, 28
	s_mov_b64 s[4:5], 0x1000
	v_cndmask_b32_e32 v36, v34, v36, vcc
	s_waitcnt vmcnt(17)
	v_lshlrev_b32_e32 v87, 2, v36
	v_xor_b32_e32 v36, 4, v34
	v_cmp_lt_i32_e32 vcc, v36, v35
	v_lshl_add_u64 v[68:69], s[26:27], 0, v[66:67]
	v_lshl_add_u64 v[70:71], v[68:69], 0, s[4:5]
	v_cndmask_b32_e32 v36, v34, v36, vcc
	v_lshlrev_b32_e32 v92, 2, v36
	v_xor_b32_e32 v36, 8, v34
	v_cmp_lt_i32_e32 vcc, v36, v35
	s_mov_b64 s[4:5], 0x1400
	v_lshl_add_u64 v[72:73], v[68:69], 0, s[4:5]
	v_cndmask_b32_e32 v36, v34, v36, vcc
	v_lshlrev_b32_e32 v93, 2, v36
	v_xor_b32_e32 v36, 16, v34
	v_cmp_lt_i32_e32 vcc, v36, v35
	s_mov_b64 s[4:5], 0x1800
	s_add_i32 s8, s19, s0
	v_cndmask_b32_e32 v36, v34, v36, vcc
	v_lshlrev_b32_e32 v94, 2, v36
	v_xor_b32_e32 v36, 32, v34
	v_cmp_lt_i32_e32 vcc, v36, v35
	s_lshl_b32 s2, s19, 1
	v_lshl_add_u64 v[74:75], v[68:69], 0, s[4:5]
	v_cndmask_b32_e32 v34, v34, v36, vcc
	s_mov_b64 s[4:5], 0x1c00
	s_ashr_i32 s9, s8, 31
	v_lshlrev_b32_e32 v95, 2, v34
	v_lshl_add_u64 v[76:77], v[68:69], 0, s[4:5]
	s_lshl_b64 s[4:5], s[0:1], 11
	v_lshlrev_b64 v[34:35], 2, v[198:199]
	s_ashr_i32 s3, s2, 31
	s_lshl_b64 s[6:7], s[0:1], 12
	v_lshlrev_b64 v[36:37], 3, v[198:199]
	s_lshl_b64 s[10:11], s[8:9], 11
	v_lshl_add_u64 v[78:79], s[4:5], 0, v[34:35]
	s_lshl_b64 s[4:5], s[2:3], 11
	s_waitcnt vmcnt(16)
	v_lshl_add_u64 v[80:81], s[6:7], 0, v[36:37]
	s_lshl_b64 s[6:7], s[2:3], 12
	v_lshl_add_u64 v[82:83], s[10:11], 0, v[34:35]
	s_lshl_b64 s[10:11], s[8:9], 12
	s_lshl_b64 s[8:9], s[8:9], 13
	v_lshl_add_u64 v[84:85], s[10:11], 0, v[36:37]
	s_add_u32 s10, s20, s8
	s_addc_u32 s11, s21, s9
	s_add_i32 s8, s0, s2
	s_ashr_i32 s9, s8, 31
	s_lshl_b64 s[12:13], s[2:3], 13
	s_lshl_b64 s[8:9], s[8:9], 13
	s_add_u32 s14, s20, s8
	v_lshlrev_b32_e32 v1, 2, v1
	s_addc_u32 s15, s21, s9
	v_mov_b32_e32 v96, 0x358637bd
	s_mov_b32 s1, 0xf800000
	v_mov_b32_e32 v97, 0x260
	s_movk_i32 s3, 0x7fff
	s_mov_b32 s20, 0x38a00000
	s_mov_b32 s21, 0xc6800000
	v_mov_b32_e32 v98, 1
	v_readlane_b32 s22, v252, 23
	v_readlane_b32 s23, v252, 24
	v_readlane_b32 s24, v252, 25
	v_readlane_b32 s25, v252, 26
	s_branch .LBB0_65
.LBB0_63:
	v_mov_b32_e32 v90, v35
	v_mov_b32_e32 v91, v39
	v_mov_b32_e32 v88, v34
	v_mov_b32_e32 v89, v38
	v_pk_mul_f32 v[90:91], v[90:91], v[90:91]
	v_mov_b32_e32 v100, v37
	v_mov_b32_e32 v101, v41
	v_pk_fma_f32 v[88:89], v[88:89], v[88:89], v[90:91]
	v_mov_b32_e32 v90, v36
	v_mov_b32_e32 v91, v40
	v_pk_mul_f32 v[100:101], v[100:101], v[100:101]
	v_mul_f32_e32 v86, v50, v50
	v_pk_fma_f32 v[90:91], v[90:91], v[90:91], v[100:101]
	v_pk_mul_f32 v[100:101], v[42:43], v[42:43]
	v_pk_add_f32 v[88:89], v[88:89], v[90:91]
	v_pk_mul_f32 v[90:91], v[44:45], v[44:45]
	v_mul_f32_e32 v99, v51, v51
	v_pk_mov_b32 v[102:103], v[100:101], v[90:91] op_sel:[1,0]
	v_mov_b32_e32 v101, v91
	v_pk_add_f32 v[90:91], v[102:103], v[100:101]
	v_pk_add_f32 v[88:89], v[88:89], v[88:89] op_sel:[0,1] op_sel_hi:[1,0]
	v_pk_add_f32 v[90:91], v[90:91], v[90:91] op_sel:[0,1] op_sel_hi:[1,0]
	v_mov_b32_e32 v89, v86
	v_mov_b32_e32 v91, v99
	v_mul_f32_e32 v86, v47, v47
	v_mul_f32_e32 v100, v52, v52
	v_pk_add_f32 v[88:89], v[88:89], v[90:91]
	v_pk_fma_f32 v[90:91], v[46:47], v[46:47], v[86:87] op_sel_hi:[1,1,0]
	v_mul_f32_e32 v86, v49, v49
	v_mul_f32_e32 v102, v53, v53
	v_mov_b32_e32 v91, v100
	v_pk_fma_f32 v[100:101], v[48:49], v[48:49], v[86:87] op_sel_hi:[1,1,0]
	v_mul_f32_e32 v86, v62, v62
	v_mov_b32_e32 v101, v102
	v_pk_add_f32 v[90:91], v[90:91], v[100:101]
	v_pk_mul_f32 v[100:101], v[54:55], v[54:55]
	v_pk_add_f32 v[88:89], v[88:89], v[90:91]
	v_pk_mul_f32 v[90:91], v[56:57], v[56:57]
	v_mul_f32_e32 v99, v63, v63
	v_pk_mov_b32 v[102:103], v[100:101], v[90:91] op_sel:[1,0]
	v_mov_b32_e32 v101, v91
	v_pk_add_f32 v[90:91], v[102:103], v[100:101]
	v_pk_add_f32 v[88:89], v[88:89], v[88:89] op_sel:[0,1] op_sel_hi:[1,0]
	v_pk_add_f32 v[90:91], v[90:91], v[90:91] op_sel:[0,1] op_sel_hi:[1,0]
	v_mov_b32_e32 v89, v86
	v_mov_b32_e32 v91, v99
	v_mul_f32_e32 v86, v59, v59
	v_pk_add_f32 v[100:101], v[88:89], v[90:91]
	v_pk_fma_f32 v[88:89], v[58:59], v[58:59], v[86:87] op_sel_hi:[1,1,0]
	v_mul_f32_e32 v86, v61, v61
	v_mul_f32_e32 v102, v64, v64
	v_mul_f32_e32 v103, v65, v65
	v_pk_fma_f32 v[90:91], v[60:61], v[60:61], v[86:87] op_sel_hi:[1,1,0]
	v_mov_b32_e32 v89, v102
	v_mov_b32_e32 v91, v103
	v_pk_add_f32 v[102:103], v[88:89], v[90:91]
	global_load_dwordx4 v[88:91], v[68:69], off nt
	v_pk_add_f32 v[100:101], v[100:101], v[102:103]
	s_nop 0
	v_add_f32_e32 v86, v100, v101
	ds_bpermute_b32 v99, v1, v86
	s_waitcnt lgkmcnt(0)
	v_add_f32_e32 v86, v86, v99
	ds_bpermute_b32 v99, v87, v86
	s_waitcnt lgkmcnt(0)
	v_add_f32_e32 v86, v86, v99
	ds_bpermute_b32 v99, v92, v86
	s_waitcnt lgkmcnt(0)
	v_add_f32_e32 v86, v86, v99
	ds_bpermute_b32 v99, v93, v86
	s_waitcnt lgkmcnt(0)
	v_add_f32_e32 v86, v86, v99
	ds_bpermute_b32 v99, v94, v86
	s_waitcnt lgkmcnt(0)
	v_add_f32_e32 v86, v86, v99
	ds_bpermute_b32 v99, v95, v86
	s_waitcnt lgkmcnt(0)
	v_add_f32_e32 v86, v86, v99
	v_fmamk_f32 v86, v86, 0x3a000000, v96
	v_mul_f32_e32 v99, 0x4f800000, v86
	v_cmp_gt_f32_e32 vcc, s1, v86
	s_nop 1
	v_cndmask_b32_e32 v86, v86, v99, vcc
	v_sqrt_f32_e32 v99, v86
	s_nop 0
	v_add_u32_e32 v100, -1, v99
	v_fma_f32 v101, -v100, v99, v86
	v_cmp_ge_f32_e64 s[8:9], 0, v101
	v_add_u32_e32 v101, 1, v99
	s_nop 0
	v_cndmask_b32_e64 v100, v99, v100, s[8:9]
	v_fma_f32 v99, -v101, v99, v86
	v_cmp_lt_f32_e64 s[8:9], 0, v99
	s_nop 1
	v_cndmask_b32_e64 v99, v100, v101, s[8:9]
	v_mul_f32_e32 v100, 0x37800000, v99
	v_cndmask_b32_e32 v99, v99, v100, vcc
	v_cmp_class_f32_e32 vcc, v86, v97
	s_nop 1
	v_cndmask_b32_e32 v86, v99, v86, vcc
	v_div_scale_f32 v99, s[8:9], v86, v86, 1.0
	v_rcp_f32_e32 v100, v99
	s_nop 0
	v_fma_f32 v101, -v99, v100, 1.0
	v_fmac_f32_e32 v100, v101, v100
	v_div_scale_f32 v101, vcc, 1.0, v86, 1.0
	v_mul_f32_e32 v102, v101, v100
	v_fma_f32 v103, -v99, v102, v101
	v_fmac_f32_e32 v102, v103, v100
	v_fma_f32 v99, -v99, v102, v101
	v_div_fmas_f32 v99, v99, v100, v102
	v_div_fixup_f32 v86, v99, v86, 1.0
	v_pk_mul_f32 v[106:107], v[86:87], v[36:37] op_sel_hi:[0,1]
	v_pk_mul_f32 v[104:105], v[86:87], v[34:35] op_sel_hi:[0,1]
	s_waitcnt vmcnt(0)
	v_pk_mul_f32 v[90:91], v[106:107], v[90:91]
	v_pk_mul_f32 v[88:89], v[104:105], v[88:89]
	v_and_b32_sdwa v105, v91, v98 dst_sel:DWORD dst_unused:UNUSED_PAD src0_sel:WORD_1 src1_sel:DWORD
	v_and_b32_sdwa v99, v90, v98 dst_sel:DWORD dst_unused:UNUSED_PAD src0_sel:WORD_1 src1_sel:DWORD
	v_add3_u32 v105, v91, v105, s3
	v_add3_u32 v99, v90, v99, s3
	v_and_b32_e32 v105, 0xffff0000, v105
	v_or_b32_sdwa v105, v105, v99 dst_sel:DWORD dst_unused:UNUSED_PAD src0_sel:DWORD src1_sel:WORD_1
	v_mov_b32_e32 v99, 0
	v_cvt_pk_fp8_f32 v99, v88, v89
	v_lshl_add_u64 v[100:101], s[82:83], 0, v[84:85]
	v_and_b32_sdwa v104, v88, v98 dst_sel:DWORD dst_unused:UNUSED_PAD src0_sel:WORD_1 src1_sel:DWORD
	v_add3_u32 v104, v88, v104, s3
	v_and_b32_sdwa v106, v89, v98 dst_sel:DWORD dst_unused:UNUSED_PAD src0_sel:WORD_1 src1_sel:DWORD
	v_add_co_u32_e32 v88, vcc, s20, v100
	v_cvt_pk_fp8_f32 v99, v90, v91 op_sel:[0,0,1]
	v_lshl_add_u64 v[102:103], s[82:83], 0, v[82:83]
	v_add3_u32 v106, v89, v106, s3
	v_addc_co_u32_e32 v89, vcc, 0, v101, vcc
	v_and_b32_e32 v106, 0xffff0000, v106
	v_add_co_u32_e32 v90, vcc, s21, v102
	v_or_b32_sdwa v104, v106, v104 dst_sel:DWORD dst_unused:UNUSED_PAD src0_sel:DWORD src1_sel:WORD_1
	s_nop 0
	v_addc_co_u32_e32 v91, vcc, 0, v103, vcc
	global_store_dwordx2 v[88:89], v[104:105], off
	global_store_dword v[90:91], v99, off
	global_load_dwordx4 v[100:103], v[68:69], off offset:1024 nt
	v_pk_mul_f32 v[104:105], v[86:87], v[38:39] op_sel_hi:[0,1]
	v_mov_b32_e32 v99, 0
	v_pk_mul_f32 v[106:107], v[86:87], v[40:41] op_sel_hi:[0,1]
	s_waitcnt vmcnt(0)
	v_pk_mul_f32 v[100:101], v[104:105], v[100:101]
	s_nop 0
	v_cvt_pk_fp8_f32 v99, v100, v101
	v_pk_mul_f32 v[102:103], v[106:107], v[102:103]
	v_and_b32_sdwa v105, v100, v98 dst_sel:DWORD dst_unused:UNUSED_PAD src0_sel:WORD_1 src1_sel:DWORD
	v_and_b32_sdwa v106, v103, v98 dst_sel:DWORD dst_unused:UNUSED_PAD src0_sel:WORD_1 src1_sel:DWORD
	v_and_b32_sdwa v107, v101, v98 dst_sel:DWORD dst_unused:UNUSED_PAD src0_sel:WORD_1 src1_sel:DWORD
	v_and_b32_sdwa v104, v102, v98 dst_sel:DWORD dst_unused:UNUSED_PAD src0_sel:WORD_1 src1_sel:DWORD
	v_add3_u32 v100, v100, v105, s3
	v_add3_u32 v105, v103, v106, s3
	v_add3_u32 v101, v101, v107, s3
	v_cvt_pk_fp8_f32 v99, v102, v103 op_sel:[0,0,1]
	v_add3_u32 v104, v102, v104, s3
	v_and_b32_e32 v105, 0xffff0000, v105
	v_and_b32_e32 v106, 0xffff0000, v101
	v_or_b32_sdwa v101, v105, v104 dst_sel:DWORD dst_unused:UNUSED_PAD src0_sel:DWORD src1_sel:WORD_1
	v_or_b32_sdwa v100, v106, v100 dst_sel:DWORD dst_unused:UNUSED_PAD src0_sel:DWORD src1_sel:WORD_1
	global_store_dwordx2 v[88:89], v[100:101], off offset:512
	global_store_dword v[90:91], v99, off offset:256
	global_load_dwordx4 v[100:103], v[68:69], off offset:2048 nt
	v_pk_mul_f32 v[104:105], v[86:87], v[42:43] op_sel_hi:[0,1]
	v_mov_b32_e32 v99, 0
	v_pk_mul_f32 v[106:107], v[86:87], v[44:45] op_sel_hi:[0,1]
	s_waitcnt vmcnt(0)
	v_pk_mul_f32 v[100:101], v[104:105], v[100:101]
	s_nop 0
	v_cvt_pk_fp8_f32 v99, v100, v101
	v_pk_mul_f32 v[102:103], v[106:107], v[102:103]
	v_and_b32_sdwa v105, v100, v98 dst_sel:DWORD dst_unused:UNUSED_PAD src0_sel:WORD_1 src1_sel:DWORD
	v_and_b32_sdwa v106, v103, v98 dst_sel:DWORD dst_unused:UNUSED_PAD src0_sel:WORD_1 src1_sel:DWORD
	v_and_b32_sdwa v107, v101, v98 dst_sel:DWORD dst_unused:UNUSED_PAD src0_sel:WORD_1 src1_sel:DWORD
	v_and_b32_sdwa v104, v102, v98 dst_sel:DWORD dst_unused:UNUSED_PAD src0_sel:WORD_1 src1_sel:DWORD
	v_add3_u32 v100, v100, v105, s3
	v_add3_u32 v105, v103, v106, s3
	v_add3_u32 v101, v101, v107, s3
	v_cvt_pk_fp8_f32 v99, v102, v103 op_sel:[0,0,1]
	v_add3_u32 v104, v102, v104, s3
	v_and_b32_e32 v105, 0xffff0000, v105
	v_and_b32_e32 v106, 0xffff0000, v101
	v_or_b32_sdwa v101, v105, v104 dst_sel:DWORD dst_unused:UNUSED_PAD src0_sel:DWORD src1_sel:WORD_1
	v_or_b32_sdwa v100, v106, v100 dst_sel:DWORD dst_unused:UNUSED_PAD src0_sel:DWORD src1_sel:WORD_1
	global_store_dwordx2 v[88:89], v[100:101], off offset:1024
	global_store_dword v[90:91], v99, off offset:512
	global_load_dwordx4 v[100:103], v[68:69], off offset:3072 nt
	v_pk_mul_f32 v[104:105], v[86:87], v[46:47] op_sel_hi:[0,1]
	v_mov_b32_e32 v99, 0
	v_pk_mul_f32 v[106:107], v[86:87], v[48:49] op_sel_hi:[0,1]
	s_waitcnt vmcnt(0)
	v_pk_mul_f32 v[100:101], v[104:105], v[100:101]
	s_nop 0
	v_cvt_pk_fp8_f32 v99, v100, v101
	v_pk_mul_f32 v[102:103], v[106:107], v[102:103]
	v_and_b32_sdwa v105, v100, v98 dst_sel:DWORD dst_unused:UNUSED_PAD src0_sel:WORD_1 src1_sel:DWORD
	v_and_b32_sdwa v106, v103, v98 dst_sel:DWORD dst_unused:UNUSED_PAD src0_sel:WORD_1 src1_sel:DWORD
	v_and_b32_sdwa v107, v101, v98 dst_sel:DWORD dst_unused:UNUSED_PAD src0_sel:WORD_1 src1_sel:DWORD
	v_and_b32_sdwa v104, v102, v98 dst_sel:DWORD dst_unused:UNUSED_PAD src0_sel:WORD_1 src1_sel:DWORD
	v_add3_u32 v100, v100, v105, s3
	v_add3_u32 v105, v103, v106, s3
	v_add3_u32 v101, v101, v107, s3
	v_cvt_pk_fp8_f32 v99, v102, v103 op_sel:[0,0,1]
	v_add3_u32 v104, v102, v104, s3
	v_and_b32_e32 v105, 0xffff0000, v105
	v_and_b32_e32 v106, 0xffff0000, v101
	v_or_b32_sdwa v101, v105, v104 dst_sel:DWORD dst_unused:UNUSED_PAD src0_sel:DWORD src1_sel:WORD_1
	v_or_b32_sdwa v100, v106, v100 dst_sel:DWORD dst_unused:UNUSED_PAD src0_sel:DWORD src1_sel:WORD_1
	global_store_dwordx2 v[88:89], v[100:101], off offset:1536
	global_store_dword v[90:91], v99, off offset:768
	global_load_dwordx4 v[100:103], v[70:71], off nt
	v_pk_mul_f32 v[104:105], v[86:87], v[50:51] op_sel_hi:[0,1]
	v_mov_b32_e32 v99, 0
	v_pk_mul_f32 v[106:107], v[86:87], v[52:53] op_sel_hi:[0,1]
	s_waitcnt vmcnt(0)
	v_pk_mul_f32 v[100:101], v[104:105], v[100:101]
	s_nop 0
	v_cvt_pk_fp8_f32 v99, v100, v101
	v_pk_mul_f32 v[102:103], v[106:107], v[102:103]
	v_and_b32_sdwa v105, v100, v98 dst_sel:DWORD dst_unused:UNUSED_PAD src0_sel:WORD_1 src1_sel:DWORD
	v_and_b32_sdwa v106, v103, v98 dst_sel:DWORD dst_unused:UNUSED_PAD src0_sel:WORD_1 src1_sel:DWORD
	v_and_b32_sdwa v107, v101, v98 dst_sel:DWORD dst_unused:UNUSED_PAD src0_sel:WORD_1 src1_sel:DWORD
	v_and_b32_sdwa v104, v102, v98 dst_sel:DWORD dst_unused:UNUSED_PAD src0_sel:WORD_1 src1_sel:DWORD
	v_add3_u32 v100, v100, v105, s3
	v_add3_u32 v105, v103, v106, s3
	v_add3_u32 v101, v101, v107, s3
	v_cvt_pk_fp8_f32 v99, v102, v103 op_sel:[0,0,1]
	v_add3_u32 v104, v102, v104, s3
	v_and_b32_e32 v105, 0xffff0000, v105
	v_and_b32_e32 v106, 0xffff0000, v101
	v_or_b32_sdwa v101, v105, v104 dst_sel:DWORD dst_unused:UNUSED_PAD src0_sel:DWORD src1_sel:WORD_1
	v_or_b32_sdwa v100, v106, v100 dst_sel:DWORD dst_unused:UNUSED_PAD src0_sel:DWORD src1_sel:WORD_1
	global_store_dwordx2 v[88:89], v[100:101], off offset:2048
	global_store_dword v[90:91], v99, off offset:1024
	global_load_dwordx4 v[100:103], v[72:73], off nt
	v_pk_mul_f32 v[104:105], v[86:87], v[54:55] op_sel_hi:[0,1]
	v_mov_b32_e32 v99, 0
	v_pk_mul_f32 v[106:107], v[86:87], v[56:57] op_sel_hi:[0,1]
	s_waitcnt vmcnt(0)
	v_pk_mul_f32 v[100:101], v[104:105], v[100:101]
	s_nop 0
	v_cvt_pk_fp8_f32 v99, v100, v101
	v_pk_mul_f32 v[102:103], v[106:107], v[102:103]
	v_and_b32_sdwa v105, v100, v98 dst_sel:DWORD dst_unused:UNUSED_PAD src0_sel:WORD_1 src1_sel:DWORD
	v_and_b32_sdwa v106, v103, v98 dst_sel:DWORD dst_unused:UNUSED_PAD src0_sel:WORD_1 src1_sel:DWORD
	v_and_b32_sdwa v107, v101, v98 dst_sel:DWORD dst_unused:UNUSED_PAD src0_sel:WORD_1 src1_sel:DWORD
	v_and_b32_sdwa v104, v102, v98 dst_sel:DWORD dst_unused:UNUSED_PAD src0_sel:WORD_1 src1_sel:DWORD
	v_add3_u32 v100, v100, v105, s3
	v_add3_u32 v105, v103, v106, s3
	v_add3_u32 v101, v101, v107, s3
	v_cvt_pk_fp8_f32 v99, v102, v103 op_sel:[0,0,1]
	v_add3_u32 v104, v102, v104, s3
	v_and_b32_e32 v105, 0xffff0000, v105
	v_and_b32_e32 v106, 0xffff0000, v101
	v_or_b32_sdwa v101, v105, v104 dst_sel:DWORD dst_unused:UNUSED_PAD src0_sel:DWORD src1_sel:WORD_1
	v_or_b32_sdwa v100, v106, v100 dst_sel:DWORD dst_unused:UNUSED_PAD src0_sel:DWORD src1_sel:WORD_1
	global_store_dwordx2 v[88:89], v[100:101], off offset:2560
	global_store_dword v[90:91], v99, off offset:1280
	global_load_dwordx4 v[100:103], v[74:75], off nt
	v_pk_mul_f32 v[104:105], v[86:87], v[58:59] op_sel_hi:[0,1]
	v_mov_b32_e32 v99, 0
	v_pk_mul_f32 v[106:107], v[86:87], v[60:61] op_sel_hi:[0,1]
	s_waitcnt vmcnt(0)
	v_pk_mul_f32 v[100:101], v[104:105], v[100:101]
	s_nop 0
	v_cvt_pk_fp8_f32 v99, v100, v101
	v_pk_mul_f32 v[102:103], v[106:107], v[102:103]
	v_and_b32_sdwa v105, v100, v98 dst_sel:DWORD dst_unused:UNUSED_PAD src0_sel:WORD_1 src1_sel:DWORD
	v_and_b32_sdwa v106, v103, v98 dst_sel:DWORD dst_unused:UNUSED_PAD src0_sel:WORD_1 src1_sel:DWORD
	v_and_b32_sdwa v107, v101, v98 dst_sel:DWORD dst_unused:UNUSED_PAD src0_sel:WORD_1 src1_sel:DWORD
	v_and_b32_sdwa v104, v102, v98 dst_sel:DWORD dst_unused:UNUSED_PAD src0_sel:WORD_1 src1_sel:DWORD
	v_add3_u32 v100, v100, v105, s3
	v_add3_u32 v105, v103, v106, s3
	v_add3_u32 v101, v101, v107, s3
	v_cvt_pk_fp8_f32 v99, v102, v103 op_sel:[0,0,1]
	v_add3_u32 v104, v102, v104, s3
	v_and_b32_e32 v105, 0xffff0000, v105
	v_and_b32_e32 v106, 0xffff0000, v101
	v_or_b32_sdwa v101, v105, v104 dst_sel:DWORD dst_unused:UNUSED_PAD src0_sel:DWORD src1_sel:WORD_1
	v_or_b32_sdwa v100, v106, v100 dst_sel:DWORD dst_unused:UNUSED_PAD src0_sel:DWORD src1_sel:WORD_1
	global_store_dwordx2 v[88:89], v[100:101], off offset:3072
	global_store_dword v[90:91], v99, off offset:1536
	global_load_dwordx4 v[100:103], v[76:77], off nt
	v_pk_mul_f32 v[104:105], v[86:87], v[62:63] op_sel_hi:[0,1]
	v_mov_b32_e32 v99, 0
	v_pk_mul_f32 v[106:107], v[86:87], v[64:65] op_sel_hi:[0,1]
	s_waitcnt vmcnt(0)
	v_pk_mul_f32 v[100:101], v[104:105], v[100:101]
	s_nop 0
	v_cvt_pk_fp8_f32 v99, v100, v101
	v_pk_mul_f32 v[102:103], v[106:107], v[102:103]
	v_and_b32_sdwa v104, v100, v98 dst_sel:DWORD dst_unused:UNUSED_PAD src0_sel:WORD_1 src1_sel:DWORD
	v_and_b32_sdwa v105, v103, v98 dst_sel:DWORD dst_unused:UNUSED_PAD src0_sel:WORD_1 src1_sel:DWORD
	v_and_b32_sdwa v106, v101, v98 dst_sel:DWORD dst_unused:UNUSED_PAD src0_sel:WORD_1 src1_sel:DWORD
	v_and_b32_sdwa v86, v102, v98 dst_sel:DWORD dst_unused:UNUSED_PAD src0_sel:WORD_1 src1_sel:DWORD
	v_add3_u32 v100, v100, v104, s3
	v_add3_u32 v104, v103, v105, s3
	v_add3_u32 v101, v101, v106, s3
	v_cvt_pk_fp8_f32 v99, v102, v103 op_sel:[0,0,1]
	v_add3_u32 v86, v102, v86, s3
	v_and_b32_e32 v104, 0xffff0000, v104
	v_and_b32_e32 v105, 0xffff0000, v101
	v_or_b32_sdwa v101, v104, v86 dst_sel:DWORD dst_unused:UNUSED_PAD src0_sel:DWORD src1_sel:WORD_1
	v_or_b32_sdwa v100, v105, v100 dst_sel:DWORD dst_unused:UNUSED_PAD src0_sel:DWORD src1_sel:WORD_1
	global_store_dwordx2 v[88:89], v[100:101], off offset:3584
	global_store_dword v[90:91], v99, off offset:1792

.LBB0_65:
	s_add_i32 s8, s19, s0
	s_cmpk_lt_i32 s8, 0x4000
	s_cselect_b64 s[16:17], -1, 0
	s_cmpk_gt_i32 s8, 0x3fff
	s_cbranch_scc1 .LBB0_67
	v_lshl_add_u64 v[50:51], s[10:11], 0, v[66:67]
	v_add_co_u32_e32 v62, vcc, 0x1000, v50
	global_load_dwordx4 v[34:37], v[50:51], off nt
	global_load_dwordx4 v[38:41], v[50:51], off offset:1024 nt
	global_load_dwordx4 v[42:45], v[50:51], off offset:2048 nt
	global_load_dwordx4 v[46:49], v[50:51], off offset:3072 nt
	v_addc_co_u32_e32 v63, vcc, 0, v51, vcc
	global_load_dwordx4 v[50:53], v[62:63], off nt
	global_load_dwordx4 v[54:57], v[62:63], off offset:1024 nt
	global_load_dwordx4 v[58:61], v[62:63], off offset:2048 nt
	s_nop 0
	global_load_dwordx4 v[62:65], v[62:63], off offset:3072 nt
.LBB0_67:
	s_waitcnt vmcnt(7)
	v_mov_b32_e32 v90, v3
	s_waitcnt vmcnt(6)
	v_mov_b32_e32 v91, v7
	v_mov_b32_e32 v88, v2
	v_mov_b32_e32 v89, v6
	v_pk_mul_f32 v[90:91], v[90:91], v[90:91]
	v_mov_b32_e32 v100, v5
	v_mov_b32_e32 v101, v9
	v_pk_fma_f32 v[88:89], v[88:89], v[88:89], v[90:91]
	v_mov_b32_e32 v90, v4
	v_mov_b32_e32 v91, v8
	v_pk_mul_f32 v[100:101], v[100:101], v[100:101]
	s_waitcnt vmcnt(3)
	v_mul_f32_e32 v86, v18, v18
	v_pk_fma_f32 v[90:91], v[90:91], v[90:91], v[100:101]
	v_pk_mul_f32 v[100:101], v[10:11], v[10:11]
	v_pk_add_f32 v[88:89], v[88:89], v[90:91]
	v_pk_mul_f32 v[90:91], v[12:13], v[12:13]
	v_mul_f32_e32 v99, v19, v19
	v_pk_mov_b32 v[102:103], v[100:101], v[90:91] op_sel:[1,0]
	v_mov_b32_e32 v101, v91
	v_pk_add_f32 v[90:91], v[102:103], v[100:101]
	v_pk_add_f32 v[88:89], v[88:89], v[88:89] op_sel:[0,1] op_sel_hi:[1,0]
	v_pk_add_f32 v[90:91], v[90:91], v[90:91] op_sel:[0,1] op_sel_hi:[1,0]
	v_mov_b32_e32 v89, v86
	v_mov_b32_e32 v91, v99
	v_mul_f32_e32 v86, v15, v15
	v_mul_f32_e32 v100, v20, v20
	v_pk_add_f32 v[88:89], v[88:89], v[90:91]
	v_pk_fma_f32 v[90:91], v[14:15], v[14:15], v[86:87] op_sel_hi:[1,1,0]
	v_mul_f32_e32 v86, v17, v17
	v_mul_f32_e32 v102, v21, v21
	v_mov_b32_e32 v91, v100
	v_pk_fma_f32 v[100:101], v[16:17], v[16:17], v[86:87] op_sel_hi:[1,1,0]
	s_waitcnt vmcnt(0)
	v_mul_f32_e32 v86, v30, v30
	v_mov_b32_e32 v101, v102
	v_pk_add_f32 v[90:91], v[90:91], v[100:101]
	v_pk_mul_f32 v[100:101], v[22:23], v[22:23]
	v_pk_add_f32 v[88:89], v[88:89], v[90:91]
	v_pk_mul_f32 v[90:91], v[24:25], v[24:25]
	v_mul_f32_e32 v99, v31, v31
	v_pk_mov_b32 v[102:103], v[100:101], v[90:91] op_sel:[1,0]
	v_mov_b32_e32 v101, v91
	v_pk_add_f32 v[90:91], v[102:103], v[100:101]
	v_pk_add_f32 v[88:89], v[88:89], v[88:89] op_sel:[0,1] op_sel_hi:[1,0]
	v_pk_add_f32 v[90:91], v[90:91], v[90:91] op_sel:[0,1] op_sel_hi:[1,0]
	v_mov_b32_e32 v89, v86
	v_mov_b32_e32 v91, v99
	v_mul_f32_e32 v86, v27, v27
	v_pk_add_f32 v[100:101], v[88:89], v[90:91]
	v_pk_fma_f32 v[88:89], v[26:27], v[26:27], v[86:87] op_sel_hi:[1,1,0]
	v_mul_f32_e32 v86, v29, v29
	v_mul_f32_e32 v102, v32, v32
	v_mul_f32_e32 v103, v33, v33
	v_pk_fma_f32 v[90:91], v[28:29], v[28:29], v[86:87] op_sel_hi:[1,1,0]
	v_mov_b32_e32 v89, v102
	v_mov_b32_e32 v91, v103
	v_pk_add_f32 v[102:103], v[88:89], v[90:91]
	global_load_dwordx4 v[88:91], v[68:69], off nt
	v_pk_add_f32 v[100:101], v[100:101], v[102:103]
	s_add_i32 s0, s2, s0
	v_add_f32_e32 v86, v100, v101
	ds_bpermute_b32 v99, v1, v86
	s_waitcnt lgkmcnt(0)
	v_add_f32_e32 v86, v86, v99
	ds_bpermute_b32 v99, v87, v86
	s_waitcnt lgkmcnt(0)
	v_add_f32_e32 v86, v86, v99
	ds_bpermute_b32 v99, v92, v86
	s_waitcnt lgkmcnt(0)
	v_add_f32_e32 v86, v86, v99
	ds_bpermute_b32 v99, v93, v86
	s_waitcnt lgkmcnt(0)
	v_add_f32_e32 v86, v86, v99
	ds_bpermute_b32 v99, v94, v86
	s_waitcnt lgkmcnt(0)
	v_add_f32_e32 v86, v86, v99
	ds_bpermute_b32 v99, v95, v86
	s_waitcnt lgkmcnt(0)
	v_add_f32_e32 v86, v86, v99
	v_fmamk_f32 v86, v86, 0x3a000000, v96
	v_mul_f32_e32 v99, 0x4f800000, v86
	v_cmp_gt_f32_e32 vcc, s1, v86
	s_nop 1
	v_cndmask_b32_e32 v86, v86, v99, vcc
	v_sqrt_f32_e32 v99, v86
	s_nop 0
	v_add_u32_e32 v100, -1, v99
	v_fma_f32 v101, -v100, v99, v86
	v_cmp_ge_f32_e64 s[8:9], 0, v101
	v_add_u32_e32 v101, 1, v99
	s_nop 0
	v_cndmask_b32_e64 v100, v99, v100, s[8:9]
	v_fma_f32 v99, -v101, v99, v86
	v_cmp_lt_f32_e64 s[8:9], 0, v99
	s_nop 1
	v_cndmask_b32_e64 v99, v100, v101, s[8:9]
	v_mul_f32_e32 v100, 0x37800000, v99
	v_cndmask_b32_e32 v99, v99, v100, vcc
	v_cmp_class_f32_e32 vcc, v86, v97
	s_nop 1
	v_cndmask_b32_e32 v86, v99, v86, vcc
	v_div_scale_f32 v99, s[8:9], v86, v86, 1.0
	v_rcp_f32_e32 v100, v99
	s_nop 0
	v_fma_f32 v101, -v99, v100, 1.0
	v_fmac_f32_e32 v100, v101, v100
	v_div_scale_f32 v101, vcc, 1.0, v86, 1.0
	v_mul_f32_e32 v102, v101, v100
	v_fma_f32 v103, -v99, v102, v101
	v_fmac_f32_e32 v102, v103, v100
	v_fma_f32 v99, -v99, v102, v101
	v_div_fmas_f32 v99, v99, v100, v102
	v_div_fixup_f32 v86, v99, v86, 1.0
	v_pk_mul_f32 v[106:107], v[86:87], v[4:5] op_sel_hi:[0,1]
	s_waitcnt vmcnt(0)
	v_pk_mul_f32 v[106:107], v[106:107], v[90:91]
	v_pk_mul_f32 v[104:105], v[86:87], v[2:3] op_sel_hi:[0,1]
	v_and_b32_sdwa v99, v107, v98 dst_sel:DWORD dst_unused:UNUSED_PAD src0_sel:WORD_1 src1_sel:DWORD
	v_and_b32_sdwa v90, v106, v98 dst_sel:DWORD dst_unused:UNUSED_PAD src0_sel:WORD_1 src1_sel:DWORD
	v_add3_u32 v99, v107, v99, s3
	v_add3_u32 v90, v106, v90, s3
	v_and_b32_e32 v99, 0xffff0000, v99
	v_pk_mul_f32 v[88:89], v[104:105], v[88:89]
	v_or_b32_sdwa v105, v99, v90 dst_sel:DWORD dst_unused:UNUSED_PAD src0_sel:DWORD src1_sel:WORD_1
	v_mov_b32_e32 v99, 0
	v_cvt_pk_fp8_f32 v99, v88, v89
	v_and_b32_sdwa v104, v89, v98 dst_sel:DWORD dst_unused:UNUSED_PAD src0_sel:WORD_1 src1_sel:DWORD
	v_lshl_add_u64 v[100:101], s[82:83], 0, v[80:81]
	v_and_b32_sdwa v91, v88, v98 dst_sel:DWORD dst_unused:UNUSED_PAD src0_sel:WORD_1 src1_sel:DWORD
	v_add3_u32 v104, v89, v104, s3
	v_add3_u32 v91, v88, v91, s3
	v_and_b32_e32 v104, 0xffff0000, v104
	v_add_co_u32_e32 v90, vcc, s20, v100
	v_cvt_pk_fp8_f32 v99, v106, v107 op_sel:[0,0,1]
	v_lshl_add_u64 v[102:103], s[82:83], 0, v[78:79]
	v_or_b32_sdwa v104, v104, v91 dst_sel:DWORD dst_unused:UNUSED_PAD src0_sel:DWORD src1_sel:WORD_1
	v_addc_co_u32_e32 v91, vcc, 0, v101, vcc
	v_add_co_u32_e32 v88, vcc, s21, v102
	global_store_dwordx2 v[90:91], v[104:105], off
	s_nop 0
	v_addc_co_u32_e32 v89, vcc, 0, v103, vcc
	global_store_dword v[88:89], v99, off
	global_load_dwordx4 v[100:103], v[68:69], off offset:1024 nt
	v_pk_mul_f32 v[104:105], v[86:87], v[6:7] op_sel_hi:[0,1]
	v_mov_b32_e32 v99, 0
	v_pk_mul_f32 v[106:107], v[86:87], v[8:9] op_sel_hi:[0,1]
	s_andn2_b64 vcc, exec, s[16:17]
	s_waitcnt vmcnt(0)
	v_pk_mul_f32 v[100:101], v[104:105], v[100:101]
	s_nop 0
	v_cvt_pk_fp8_f32 v99, v100, v101
	v_pk_mul_f32 v[102:103], v[106:107], v[102:103]
	v_and_b32_sdwa v105, v100, v98 dst_sel:DWORD dst_unused:UNUSED_PAD src0_sel:WORD_1 src1_sel:DWORD
	v_and_b32_sdwa v106, v103, v98 dst_sel:DWORD dst_unused:UNUSED_PAD src0_sel:WORD_1 src1_sel:DWORD
	v_and_b32_sdwa v107, v101, v98 dst_sel:DWORD dst_unused:UNUSED_PAD src0_sel:WORD_1 src1_sel:DWORD
	v_and_b32_sdwa v104, v102, v98 dst_sel:DWORD dst_unused:UNUSED_PAD src0_sel:WORD_1 src1_sel:DWORD
	v_add3_u32 v100, v100, v105, s3
	v_add3_u32 v105, v103, v106, s3
	v_add3_u32 v101, v101, v107, s3
	v_cvt_pk_fp8_f32 v99, v102, v103 op_sel:[0,0,1]
	v_add3_u32 v104, v102, v104, s3
	v_and_b32_e32 v105, 0xffff0000, v105
	v_and_b32_e32 v106, 0xffff0000, v101
	v_or_b32_sdwa v101, v105, v104 dst_sel:DWORD dst_unused:UNUSED_PAD src0_sel:DWORD src1_sel:WORD_1
	v_or_b32_sdwa v100, v106, v100 dst_sel:DWORD dst_unused:UNUSED_PAD src0_sel:DWORD src1_sel:WORD_1
	global_store_dwordx2 v[90:91], v[100:101], off offset:512
	global_store_dword v[88:89], v99, off offset:256
	global_load_dwordx4 v[100:103], v[68:69], off offset:2048 nt
	v_pk_mul_f32 v[104:105], v[86:87], v[10:11] op_sel_hi:[0,1]
	v_mov_b32_e32 v99, 0
	v_pk_mul_f32 v[106:107], v[86:87], v[12:13] op_sel_hi:[0,1]
	s_waitcnt vmcnt(0)
	v_pk_mul_f32 v[100:101], v[104:105], v[100:101]
	s_nop 0
	v_cvt_pk_fp8_f32 v99, v100, v101
	v_pk_mul_f32 v[102:103], v[106:107], v[102:103]
	v_and_b32_sdwa v105, v100, v98 dst_sel:DWORD dst_unused:UNUSED_PAD src0_sel:WORD_1 src1_sel:DWORD
	v_and_b32_sdwa v106, v103, v98 dst_sel:DWORD dst_unused:UNUSED_PAD src0_sel:WORD_1 src1_sel:DWORD
	v_and_b32_sdwa v107, v101, v98 dst_sel:DWORD dst_unused:UNUSED_PAD src0_sel:WORD_1 src1_sel:DWORD
	v_and_b32_sdwa v104, v102, v98 dst_sel:DWORD dst_unused:UNUSED_PAD src0_sel:WORD_1 src1_sel:DWORD
	v_add3_u32 v100, v100, v105, s3
	v_add3_u32 v105, v103, v106, s3
	v_add3_u32 v101, v101, v107, s3
	v_cvt_pk_fp8_f32 v99, v102, v103 op_sel:[0,0,1]
	v_add3_u32 v104, v102, v104, s3
	v_and_b32_e32 v105, 0xffff0000, v105
	v_and_b32_e32 v106, 0xffff0000, v101
	v_or_b32_sdwa v101, v105, v104 dst_sel:DWORD dst_unused:UNUSED_PAD src0_sel:DWORD src1_sel:WORD_1
	v_or_b32_sdwa v100, v106, v100 dst_sel:DWORD dst_unused:UNUSED_PAD src0_sel:DWORD src1_sel:WORD_1
	global_store_dwordx2 v[90:91], v[100:101], off offset:1024
	global_store_dword v[88:89], v99, off offset:512
	global_load_dwordx4 v[100:103], v[68:69], off offset:3072 nt
	v_pk_mul_f32 v[104:105], v[86:87], v[14:15] op_sel_hi:[0,1]
	v_mov_b32_e32 v99, 0
	v_pk_mul_f32 v[106:107], v[86:87], v[16:17] op_sel_hi:[0,1]
	s_waitcnt vmcnt(0)
	v_pk_mul_f32 v[100:101], v[104:105], v[100:101]
	s_nop 0
	v_cvt_pk_fp8_f32 v99, v100, v101
	v_pk_mul_f32 v[102:103], v[106:107], v[102:103]
	v_and_b32_sdwa v105, v100, v98 dst_sel:DWORD dst_unused:UNUSED_PAD src0_sel:WORD_1 src1_sel:DWORD
	v_and_b32_sdwa v106, v103, v98 dst_sel:DWORD dst_unused:UNUSED_PAD src0_sel:WORD_1 src1_sel:DWORD
	v_and_b32_sdwa v107, v101, v98 dst_sel:DWORD dst_unused:UNUSED_PAD src0_sel:WORD_1 src1_sel:DWORD
	v_and_b32_sdwa v104, v102, v98 dst_sel:DWORD dst_unused:UNUSED_PAD src0_sel:WORD_1 src1_sel:DWORD
	v_add3_u32 v100, v100, v105, s3
	v_add3_u32 v105, v103, v106, s3
	v_add3_u32 v101, v101, v107, s3
	v_cvt_pk_fp8_f32 v99, v102, v103 op_sel:[0,0,1]
	v_add3_u32 v104, v102, v104, s3
	v_and_b32_e32 v105, 0xffff0000, v105
	v_and_b32_e32 v106, 0xffff0000, v101
	v_or_b32_sdwa v101, v105, v104 dst_sel:DWORD dst_unused:UNUSED_PAD src0_sel:DWORD src1_sel:WORD_1
	v_or_b32_sdwa v100, v106, v100 dst_sel:DWORD dst_unused:UNUSED_PAD src0_sel:DWORD src1_sel:WORD_1
	global_store_dwordx2 v[90:91], v[100:101], off offset:1536
	global_store_dword v[88:89], v99, off offset:768
	global_load_dwordx4 v[100:103], v[70:71], off nt
	v_pk_mul_f32 v[104:105], v[86:87], v[18:19] op_sel_hi:[0,1]
	v_mov_b32_e32 v99, 0
	v_pk_mul_f32 v[106:107], v[86:87], v[20:21] op_sel_hi:[0,1]
	s_waitcnt vmcnt(0)
	v_pk_mul_f32 v[100:101], v[104:105], v[100:101]
	s_nop 0
	v_cvt_pk_fp8_f32 v99, v100, v101
	v_pk_mul_f32 v[102:103], v[106:107], v[102:103]
	v_and_b32_sdwa v105, v100, v98 dst_sel:DWORD dst_unused:UNUSED_PAD src0_sel:WORD_1 src1_sel:DWORD
	v_and_b32_sdwa v106, v103, v98 dst_sel:DWORD dst_unused:UNUSED_PAD src0_sel:WORD_1 src1_sel:DWORD
	v_and_b32_sdwa v107, v101, v98 dst_sel:DWORD dst_unused:UNUSED_PAD src0_sel:WORD_1 src1_sel:DWORD
	v_and_b32_sdwa v104, v102, v98 dst_sel:DWORD dst_unused:UNUSED_PAD src0_sel:WORD_1 src1_sel:DWORD
	v_add3_u32 v100, v100, v105, s3
	v_add3_u32 v105, v103, v106, s3
	v_add3_u32 v101, v101, v107, s3
	v_cvt_pk_fp8_f32 v99, v102, v103 op_sel:[0,0,1]
	v_add3_u32 v104, v102, v104, s3
	v_and_b32_e32 v105, 0xffff0000, v105
	v_and_b32_e32 v106, 0xffff0000, v101
	v_or_b32_sdwa v101, v105, v104 dst_sel:DWORD dst_unused:UNUSED_PAD src0_sel:DWORD src1_sel:WORD_1
	v_or_b32_sdwa v100, v106, v100 dst_sel:DWORD dst_unused:UNUSED_PAD src0_sel:DWORD src1_sel:WORD_1
	global_store_dwordx2 v[90:91], v[100:101], off offset:2048
	global_store_dword v[88:89], v99, off offset:1024
	global_load_dwordx4 v[100:103], v[72:73], off nt
	v_pk_mul_f32 v[104:105], v[86:87], v[22:23] op_sel_hi:[0,1]
	v_mov_b32_e32 v99, 0
	v_pk_mul_f32 v[106:107], v[86:87], v[24:25] op_sel_hi:[0,1]
	s_waitcnt vmcnt(0)
	v_pk_mul_f32 v[100:101], v[104:105], v[100:101]
	s_nop 0
	v_cvt_pk_fp8_f32 v99, v100, v101
	v_pk_mul_f32 v[102:103], v[106:107], v[102:103]
	v_and_b32_sdwa v105, v100, v98 dst_sel:DWORD dst_unused:UNUSED_PAD src0_sel:WORD_1 src1_sel:DWORD
	v_and_b32_sdwa v106, v103, v98 dst_sel:DWORD dst_unused:UNUSED_PAD src0_sel:WORD_1 src1_sel:DWORD
	v_and_b32_sdwa v107, v101, v98 dst_sel:DWORD dst_unused:UNUSED_PAD src0_sel:WORD_1 src1_sel:DWORD
	v_and_b32_sdwa v104, v102, v98 dst_sel:DWORD dst_unused:UNUSED_PAD src0_sel:WORD_1 src1_sel:DWORD
	v_add3_u32 v100, v100, v105, s3
	v_add3_u32 v105, v103, v106, s3
	v_add3_u32 v101, v101, v107, s3
	v_cvt_pk_fp8_f32 v99, v102, v103 op_sel:[0,0,1]
	v_add3_u32 v104, v102, v104, s3
	v_and_b32_e32 v105, 0xffff0000, v105
	v_and_b32_e32 v106, 0xffff0000, v101
	v_or_b32_sdwa v101, v105, v104 dst_sel:DWORD dst_unused:UNUSED_PAD src0_sel:DWORD src1_sel:WORD_1
	v_or_b32_sdwa v100, v106, v100 dst_sel:DWORD dst_unused:UNUSED_PAD src0_sel:DWORD src1_sel:WORD_1
	global_store_dwordx2 v[90:91], v[100:101], off offset:2560
	global_store_dword v[88:89], v99, off offset:1280
	global_load_dwordx4 v[100:103], v[74:75], off nt
	v_pk_mul_f32 v[104:105], v[86:87], v[26:27] op_sel_hi:[0,1]
	v_mov_b32_e32 v99, 0
	v_pk_mul_f32 v[106:107], v[86:87], v[28:29] op_sel_hi:[0,1]
	s_waitcnt vmcnt(0)
	v_pk_mul_f32 v[100:101], v[104:105], v[100:101]
	s_nop 0
	v_cvt_pk_fp8_f32 v99, v100, v101
	v_pk_mul_f32 v[102:103], v[106:107], v[102:103]
	v_and_b32_sdwa v105, v100, v98 dst_sel:DWORD dst_unused:UNUSED_PAD src0_sel:WORD_1 src1_sel:DWORD
	v_and_b32_sdwa v106, v103, v98 dst_sel:DWORD dst_unused:UNUSED_PAD src0_sel:WORD_1 src1_sel:DWORD
	v_and_b32_sdwa v107, v101, v98 dst_sel:DWORD dst_unused:UNUSED_PAD src0_sel:WORD_1 src1_sel:DWORD
	v_and_b32_sdwa v104, v102, v98 dst_sel:DWORD dst_unused:UNUSED_PAD src0_sel:WORD_1 src1_sel:DWORD
	v_add3_u32 v100, v100, v105, s3
	v_add3_u32 v105, v103, v106, s3
	v_add3_u32 v101, v101, v107, s3
	v_cvt_pk_fp8_f32 v99, v102, v103 op_sel:[0,0,1]
	v_add3_u32 v104, v102, v104, s3
	v_and_b32_e32 v105, 0xffff0000, v105
	v_and_b32_e32 v106, 0xffff0000, v101
	v_or_b32_sdwa v101, v105, v104 dst_sel:DWORD dst_unused:UNUSED_PAD src0_sel:DWORD src1_sel:WORD_1
	v_or_b32_sdwa v100, v106, v100 dst_sel:DWORD dst_unused:UNUSED_PAD src0_sel:DWORD src1_sel:WORD_1
	global_store_dwordx2 v[90:91], v[100:101], off offset:3072
	global_store_dword v[88:89], v99, off offset:1536
	global_load_dwordx4 v[100:103], v[76:77], off nt
	v_pk_mul_f32 v[104:105], v[86:87], v[30:31] op_sel_hi:[0,1]
	v_mov_b32_e32 v99, 0
	v_pk_mul_f32 v[106:107], v[86:87], v[32:33] op_sel_hi:[0,1]
	s_waitcnt vmcnt(0)
	v_pk_mul_f32 v[100:101], v[104:105], v[100:101]
	s_nop 0
	v_cvt_pk_fp8_f32 v99, v100, v101
	v_pk_mul_f32 v[102:103], v[106:107], v[102:103]
	v_and_b32_sdwa v104, v100, v98 dst_sel:DWORD dst_unused:UNUSED_PAD src0_sel:WORD_1 src1_sel:DWORD
	v_and_b32_sdwa v105, v103, v98 dst_sel:DWORD dst_unused:UNUSED_PAD src0_sel:WORD_1 src1_sel:DWORD
	v_and_b32_sdwa v106, v101, v98 dst_sel:DWORD dst_unused:UNUSED_PAD src0_sel:WORD_1 src1_sel:DWORD
	v_cvt_pk_fp8_f32 v99, v102, v103 op_sel:[0,0,1]
	v_and_b32_sdwa v86, v102, v98 dst_sel:DWORD dst_unused:UNUSED_PAD src0_sel:WORD_1 src1_sel:DWORD
	v_add3_u32 v100, v100, v104, s3
	v_add3_u32 v104, v103, v105, s3
	v_add3_u32 v101, v101, v106, s3
	v_add3_u32 v86, v102, v86, s3
	v_and_b32_e32 v104, 0xffff0000, v104
	v_and_b32_e32 v105, 0xffff0000, v101
	v_or_b32_sdwa v101, v104, v86 dst_sel:DWORD dst_unused:UNUSED_PAD src0_sel:DWORD src1_sel:WORD_1
	v_or_b32_sdwa v100, v105, v100 dst_sel:DWORD dst_unused:UNUSED_PAD src0_sel:DWORD src1_sel:WORD_1
	global_store_dwordx2 v[90:91], v[100:101], off offset:3584
	global_store_dword v[88:89], v99, off offset:1792
	s_cbranch_vccnz .LBB0_64
	s_cmpk_gt_i32 s0, 0x3fff
	s_cbranch_scc1 .LBB0_63
	v_lshl_add_u64 v[18:19], s[14:15], 0, v[66:67]
	v_add_co_u32_e32 v30, vcc, 0x1000, v18
	global_load_dwordx4 v[2:5], v[18:19], off nt
	global_load_dwordx4 v[6:9], v[18:19], off offset:1024 nt
	global_load_dwordx4 v[10:13], v[18:19], off offset:2048 nt
	global_load_dwordx4 v[14:17], v[18:19], off offset:3072 nt
	v_addc_co_u32_e32 v31, vcc, 0, v19, vcc
	global_load_dwordx4 v[18:21], v[30:31], off nt
	global_load_dwordx4 v[22:25], v[30:31], off offset:1024 nt
	global_load_dwordx4 v[26:29], v[30:31], off offset:2048 nt
	s_nop 0
	global_load_dwordx4 v[30:33], v[30:31], off offset:3072 nt
	s_branch .LBB0_63

.LBB0_74:
	v_add_u32_e32 v6, s1, v19
	v_ashrrev_i32_e32 v8, 6, v6
	v_readlane_b32 s12, v252, 21
	v_ashrrev_i32_e32 v9, 31, v8
	v_readlane_b32 s16, v252, 25
	v_readlane_b32 s17, v252, 26
	v_readlane_b32 s14, v252, 23
	v_readlane_b32 s15, v252, 24
	v_lshl_add_u64 v[8:9], v[8:9], 2, s[16:17]
	global_load_dword v6, v[8:9], off nt
	v_add_u32_e32 v8, s40, v19
	v_cmp_gt_i32_e64 s[14:15], s38, v8
	v_mov_b32_e32 v12, 0
	v_readlane_b32 s13, v252, 22
	v_readlane_b32 s18, v252, 27
	v_readlane_b32 s19, v252, 28
	s_and_saveexec_b64 s[10:11], s[14:15]
	s_cbranch_execz .LBB0_76
	v_ashrrev_i32_e32 v8, 6, v8
	v_readlane_b32 s16, v252, 21
	v_ashrrev_i32_e32 v9, 31, v8
	v_readlane_b32 s20, v252, 25
	v_readlane_b32 s21, v252, 26
	v_readlane_b32 s17, v252, 22
	v_readlane_b32 s18, v252, 23
	v_lshl_add_u64 v[8:9], v[8:9], 2, s[20:21]
	global_load_dword v8, v[8:9], off nt
	v_readlane_b32 s19, v252, 24
	v_readlane_b32 s22, v252, 27
	v_readlane_b32 s23, v252, 28
	s_waitcnt vmcnt(0)
	v_cvt_f32_i32_e32 v12, v8
.LBB0_76:
	s_or_b64 exec, exec, s[10:11]
	v_add_u32_e32 v10, s25, v19
	v_cmp_gt_i32_e64 s[12:13], s38, v10
	v_mov_b32_e32 v9, 0
	v_mov_b32_e32 v11, 0
	s_and_saveexec_b64 s[10:11], s[12:13]
	s_cbranch_execz .LBB0_78
	s_waitcnt vmcnt(59)
	v_ashrrev_i32_e32 v20, 6, v10
	v_readlane_b32 s16, v252, 21
	s_waitcnt vmcnt(58)
	v_ashrrev_i32_e32 v21, 31, v20
	v_readlane_b32 s20, v252, 25
	v_readlane_b32 s21, v252, 26
	v_readlane_b32 s17, v252, 22
	v_readlane_b32 s18, v252, 23
	v_lshl_add_u64 v[20:21], v[20:21], 2, s[20:21]
	global_load_dword v8, v[20:21], off nt
	v_readlane_b32 s19, v252, 24
	v_readlane_b32 s22, v252, 27
	v_readlane_b32 s23, v252, 28
	s_waitcnt vmcnt(0)
	v_cvt_f32_i32_e32 v11, v8
.LBB0_78:
	s_or_b64 exec, exec, s[10:11]
	v_add_u32_e32 v8, s39, v19
	v_cmp_gt_i32_e64 s[10:11], s38, v8
	s_and_saveexec_b64 s[16:17], s[10:11]
	s_cbranch_execz .LBB0_80
	s_waitcnt vmcnt(59)
	v_ashrrev_i32_e32 v20, 6, v8
	v_readlane_b32 s56, v252, 21
	s_waitcnt vmcnt(58)
	v_ashrrev_i32_e32 v21, 31, v20
	v_readlane_b32 s60, v252, 25
	v_readlane_b32 s61, v252, 26
	v_readlane_b32 s57, v252, 22
	v_readlane_b32 s58, v252, 23
	v_lshl_add_u64 v[20:21], v[20:21], 2, s[60:61]
	global_load_dword v9, v[20:21], off nt
	v_readlane_b32 s59, v252, 24
	v_readlane_b32 s62, v252, 27
	v_readlane_b32 s63, v252, 28
	s_waitcnt vmcnt(0)
	v_cvt_f32_i32_e32 v9, v9

.LBB0_123:
	global_load_dwordx4 v[14:17], v[36:37], off nt
	v_add_u32_e32 v3, s75, v55
	v_cmp_gt_i32_e32 vcc, s1, v3
	v_mov_b32_e32 v2, 0
	v_mov_b32_e32 v6, 0
	v_mov_b32_e32 v7, 0
	v_mov_b32_e32 v8, 0
	v_mov_b32_e32 v9, 0
	s_and_saveexec_b64 s[8:9], vcc
	s_cbranch_execz .LBB0_125
	v_lshl_add_u64 v[4:5], v[36:37], 0, s[24:25]
	global_load_dwordx4 v[6:9], v[4:5], off nt
.LBB0_125:
	s_or_b64 exec, exec, s[8:9]
	v_add_u32_e32 v38, s75, v1
	v_add_u32_e32 v10, s0, v3
	v_cmp_gt_i32_e64 s[8:9], s1, v10
	v_ashrrev_i32_e32 v39, 31, v38
	v_mov_b32_e32 v3, 0
	v_mov_b32_e32 v4, 0
	v_mov_b32_e32 v5, 0
	s_and_saveexec_b64 s[10:11], s[8:9]
	s_cbranch_execz .LBB0_127
	v_readlane_b32 s12, v252, 21
	v_readlane_b32 s14, v252, 23
	v_readlane_b32 s15, v252, 24
	v_readlane_b32 s13, v252, 22
	v_readlane_b32 s16, v252, 25
	v_lshl_add_u64 v[2:3], v[38:39], 4, s[14:15]
	global_load_dwordx4 v[2:5], v[2:3], off nt
	v_readlane_b32 s17, v252, 26
	v_readlane_b32 s18, v252, 27
	v_readlane_b32 s19, v252, 28
.LBB0_127:
	s_or_b64 exec, exec, s[10:11]
	v_add_u32_e32 v40, s75, v50
	v_add_u32_e32 v11, s0, v10
	v_cmp_gt_i32_e64 s[10:11], s1, v11
	v_mov_b32_e32 v10, 0
	v_ashrrev_i32_e32 v41, 31, v40
	v_mov_b32_e32 v18, 0
	v_mov_b32_e32 v19, 0
	v_mov_b32_e32 v20, 0
	v_mov_b32_e32 v21, 0
	s_and_saveexec_b64 s[12:13], s[10:11]
	s_cbranch_execz .LBB0_129
	v_readlane_b32 s40, v252, 21
	v_readlane_b32 s42, v252, 23
	v_readlane_b32 s43, v252, 24
	v_readlane_b32 s41, v252, 22
	v_readlane_b32 s44, v252, 25
	v_lshl_add_u64 v[12:13], v[40:41], 4, s[42:43]
	global_load_dwordx4 v[18:21], v[12:13], off nt
	v_readlane_b32 s45, v252, 26
	v_readlane_b32 s46, v252, 27
	v_readlane_b32 s47, v252, 28
.LBB0_129:
	s_or_b64 exec, exec, s[12:13]
	v_add_u32_e32 v42, s75, v51
	v_add_u32_e32 v22, s0, v11
	v_cmp_gt_i32_e64 s[12:13], s1, v22
	v_ashrrev_i32_e32 v43, 31, v42
	v_mov_b32_e32 v11, 0
	v_mov_b32_e32 v12, 0
	v_mov_b32_e32 v13, 0
	s_and_saveexec_b64 s[14:15], s[12:13]
	s_cbranch_execz .LBB0_131
	v_readlane_b32 s40, v252, 21
	v_readlane_b32 s42, v252, 23
	v_readlane_b32 s43, v252, 24
	v_readlane_b32 s41, v252, 22
	v_readlane_b32 s44, v252, 25
	v_lshl_add_u64 v[10:11], v[42:43], 4, s[42:43]
	global_load_dwordx4 v[10:13], v[10:11], off nt
	v_readlane_b32 s45, v252, 26
	v_readlane_b32 s46, v252, 27
	v_readlane_b32 s47, v252, 28
.LBB0_131:
	s_or_b64 exec, exec, s[14:15]
	v_add_u32_e32 v44, s75, v52
	v_add_u32_e32 v23, s0, v22
	v_cmp_gt_i32_e64 s[14:15], s1, v23
	v_mov_b32_e32 v22, 0
	v_ashrrev_i32_e32 v45, 31, v44
	v_mov_b32_e32 v26, 0
	v_mov_b32_e32 v27, 0
	v_mov_b32_e32 v28, 0
	v_mov_b32_e32 v29, 0
	s_and_saveexec_b64 s[16:17], s[14:15]
	s_cbranch_execz .LBB0_133
	v_readlane_b32 s40, v252, 21
	v_readlane_b32 s42, v252, 23
	v_readlane_b32 s43, v252, 24
	v_readlane_b32 s41, v252, 22
	v_readlane_b32 s44, v252, 25
	v_lshl_add_u64 v[24:25], v[44:45], 4, s[42:43]
	global_load_dwordx4 v[26:29], v[24:25], off nt
	v_readlane_b32 s45, v252, 26
	v_readlane_b32 s46, v252, 27
	v_readlane_b32 s47, v252, 28
.LBB0_133:
	s_or_b64 exec, exec, s[16:17]
	v_add_u32_e32 v46, s75, v53
	v_add_u32_e32 v30, s0, v23
	v_cmp_gt_i32_e64 s[16:17], s1, v30
	v_ashrrev_i32_e32 v47, 31, v46
	v_mov_b32_e32 v23, 0
	v_mov_b32_e32 v24, 0
	v_mov_b32_e32 v25, 0
	s_and_saveexec_b64 s[18:19], s[16:17]
	s_cbranch_execz .LBB0_135
	v_readlane_b32 s40, v252, 21
	v_readlane_b32 s42, v252, 23
	v_readlane_b32 s43, v252, 24
	v_readlane_b32 s41, v252, 22
	v_readlane_b32 s44, v252, 25
	v_lshl_add_u64 v[22:23], v[46:47], 4, s[42:43]
	global_load_dwordx4 v[22:25], v[22:23], off nt
	v_readlane_b32 s45, v252, 26
	v_readlane_b32 s46, v252, 27
	v_readlane_b32 s47, v252, 28
.LBB0_135:
	s_or_b64 exec, exec, s[18:19]
	v_add_u32_e32 v48, s75, v54
	s_waitcnt vmcnt(33)
	v_add_u32_e32 v56, s0, v30
	v_cmp_gt_i32_e64 s[18:19], s1, v56
	v_mov_b32_e32 v30, 0
	v_ashrrev_i32_e32 v49, 31, v48
	v_mov_b32_e32 v31, 0
	v_mov_b32_e32 v32, 0
	v_mov_b32_e32 v33, 0
	s_and_saveexec_b64 s[30:31], s[18:19]
	s_cbranch_execz .LBB0_137
	v_readlane_b32 s40, v252, 21
	v_readlane_b32 s42, v252, 23
	v_readlane_b32 s43, v252, 24
	v_readlane_b32 s41, v252, 22
	v_readlane_b32 s44, v252, 25
	v_lshl_add_u64 v[30:31], v[48:49], 4, s[42:43]
	global_load_dwordx4 v[30:33], v[30:31], off nt
	v_readlane_b32 s45, v252, 26
	v_readlane_b32 s46, v252, 27
	v_readlane_b32 s47, v252, 28

.LBB0_188:
	v_readlane_b32 s4, v252, 0
	s_cmp_lt_i32 s4, 2
	s_cselect_b64 s[2:3], -1, 0
	s_add_u32 s95, s82, 0x38a00000
	v_readlane_b32 s5, v252, 1
	s_addc_u32 s4, s83, 0
	v_readlane_b32 s6, v252, 2
	v_readlane_b32 s7, v252, 3
	v_writelane_b32 v252, s4, 21
	s_and_b64 s[4:5], s[2:3], s[0:1]
	s_andn2_b64 vcc, exec, s[4:5]
	s_cbranch_vccnz .LBB0_400
	v_writelane_b32 v252, s4, 45
	s_waitcnt vmcnt(62)
	v_lshrrev_b32_e32 v1, 3, v198
	v_writelane_b32 v252, s5, 46
	s_nop 0
	v_readlane_b32 s0, v252, 4
	v_readlane_b32 s1, v252, 5
	s_load_dwordx4 s[8:11], s[0:1], 0x78
	s_load_dwordx2 s[20:21], s[0:1], 0x88
	s_load_dwordx2 s[16:17], s[0:1], 0xa8
	s_load_dwordx2 s[14:15], s[0:1], 0xb8
	s_load_dwordx2 s[18:19], s[0:1], 0xd0
	v_readlane_b32 s2, v252, 13
	s_mulk_i32 s2, 0x4100
	s_add_i32 s6, s2, 0
	v_readlane_b32 s2, v252, 14
	s_cmpk_gt_i32 s2, 0xff
	s_cbranch_scc1 .LBB0_194
	v_readlane_b32 s55, v252, 14
	s_ashr_i32 s2, s55, 31
	s_lshr_b32 s2, s2, 24
	s_add_i32 s2, s55, s2
	s_and_b32 s2, s2, 0xff00
	s_sub_i32 s4, s55, s2
	s_sext_i32_i16 s2, s4
	s_bfe_u32 s2, s2, 0x4001b
	s_add_i32 s5, s4, s2
	s_load_dwordx2 s[0:1], s[0:1], 0x68
	s_sext_i32_i16 s2, s5
	s_lshl_b32 s2, s2, 2
	s_andn2_b32 s2, s2, 63
	s_ashr_i32 s3, s2, 31
	s_lshl_b64 s[2:3], s[2:3], 12
	s_waitcnt lgkmcnt(0)
	s_add_u32 s7, s0, s2
	s_addc_u32 s22, s1, s3
	s_and_b32 s2, s5, 0xfff0
	s_sub_i32 s2, s4, s2
	s_sext_i32_i16 s2, s2
	s_lshl_b32 s2, s2, 6
	s_ashr_i32 s3, s2, 31
	s_lshl_b64 s[2:3], s[2:3], 2
	s_add_u32 s2, s7, s2
	s_addc_u32 s3, s22, s3
	v_mov_b32_e32 v3, 0
	v_lshlrev_b32_e32 v2, 2, v198
	v_lshl_add_u64 v[4:5], s[2:3], 0, v[2:3]
	s_movk_i32 s7, 0x2000
	v_add_co_u32_e32 v6, vcc, s7, v4
	s_movk_i32 s22, 0x4000
	s_nop 0
	v_addc_co_u32_e32 v7, vcc, 0, v5, vcc
	v_add_co_u32_e32 v8, vcc, s22, v4
	s_movk_i32 s23, 0x6000
	s_nop 0
	v_addc_co_u32_e32 v9, vcc, 0, v5, vcc
	v_add_co_u32_e32 v10, vcc, s23, v4
	s_mov_b32 s24, 0x8000
	s_nop 0
	v_addc_co_u32_e32 v11, vcc, 0, v5, vcc
	s_waitcnt vmcnt(58)
	v_add_co_u32_e32 v20, vcc, s24, v4
	s_mov_b32 s25, 0xa000
	s_waitcnt vmcnt(57)
	v_addc_co_u32_e32 v21, vcc, 0, v5, vcc
	s_waitcnt vmcnt(56)
	v_add_co_u32_e32 v22, vcc, s25, v4
	s_mov_b32 s26, 0xc000
	s_waitcnt vmcnt(55)
	v_addc_co_u32_e32 v23, vcc, 0, v5, vcc
	s_waitcnt vmcnt(54)
	v_add_co_u32_e32 v24, vcc, s26, v4
	s_mov_b32 s27, 0xe000
	s_waitcnt vmcnt(53)
	v_addc_co_u32_e32 v25, vcc, 0, v5, vcc
	s_waitcnt vmcnt(52)
	v_add_co_u32_e32 v26, vcc, s27, v4
	s_mov_b32 s28, 0x10000
	s_waitcnt vmcnt(51)
	v_addc_co_u32_e32 v27, vcc, 0, v5, vcc
	global_load_dword v12, v[20:21], off offset:-4096 nt
	global_load_dword v13, v[20:21], off nt
	global_load_dword v14, v[22:23], off offset:-4096 nt
	global_load_dword v15, v[22:23], off nt
	global_load_dword v16, v[24:25], off offset:-4096 nt
	global_load_dword v17, v[24:25], off nt
	global_load_dword v18, v[26:27], off offset:-4096 nt
	global_load_dword v19, v[26:27], off nt
	v_add_co_u32_e32 v22, vcc, s28, v4
	s_mov_b32 s29, 0x12000
	s_nop 0
	v_addc_co_u32_e32 v23, vcc, 0, v5, vcc
	v_add_co_u32_e32 v24, vcc, s29, v4
	s_mov_b32 s30, 0x14000
	s_nop 0
	v_addc_co_u32_e32 v25, vcc, 0, v5, vcc
	v_add_co_u32_e32 v26, vcc, s30, v4
	s_mov_b32 s31, 0x16000
	s_nop 0
	v_addc_co_u32_e32 v27, vcc, 0, v5, vcc
	s_waitcnt vmcnt(58)
	v_add_co_u32_e32 v28, vcc, s31, v4
	s_mov_b32 s33, 0x18000
	s_waitcnt vmcnt(57)
	v_addc_co_u32_e32 v29, vcc, 0, v5, vcc
	s_waitcnt vmcnt(56)
	v_add_co_u32_e32 v30, vcc, s33, v4
	s_mov_b32 s34, 0x1a000
	s_waitcnt vmcnt(55)
	v_addc_co_u32_e32 v31, vcc, 0, v5, vcc
	s_waitcnt vmcnt(54)
	v_add_co_u32_e32 v32, vcc, s34, v4
	s_mov_b32 s35, 0x1c000
	s_waitcnt vmcnt(53)
	v_addc_co_u32_e32 v33, vcc, 0, v5, vcc
	s_waitcnt vmcnt(52)
	v_add_co_u32_e32 v34, vcc, s35, v4
	s_mov_b32 s36, 0x1e000
	s_waitcnt vmcnt(51)
	v_addc_co_u32_e32 v35, vcc, 0, v5, vcc
	s_waitcnt vmcnt(50)
	v_add_co_u32_e32 v36, vcc, s36, v4
	s_mov_b32 s37, 0x20000
	s_waitcnt vmcnt(49)
	v_addc_co_u32_e32 v37, vcc, 0, v5, vcc
	global_load_dword v20, v[22:23], off offset:-4096 nt
	global_load_dword v21, v[22:23], off nt
	s_nop 0
	global_load_dword v22, v[24:25], off offset:-4096 nt
	global_load_dword v23, v[24:25], off nt
	s_nop 0
	global_load_dword v24, v[26:27], off offset:-4096 nt
	global_load_dword v25, v[26:27], off nt
	s_nop 0
	global_load_dword v26, v[28:29], off offset:-4096 nt
	global_load_dword v27, v[28:29], off nt
	s_nop 0
	global_load_dword v28, v[30:31], off offset:-4096 nt
	global_load_dword v29, v[30:31], off nt
	s_nop 0
	global_load_dword v30, v[32:33], off offset:-4096 nt
	global_load_dword v31, v[32:33], off nt
	s_nop 0
	global_load_dword v32, v[34:35], off offset:-4096 nt
	global_load_dword v33, v[34:35], off nt
	s_nop 0
	global_load_dword v34, v[36:37], off offset:-4096 nt
	global_load_dword v35, v[36:37], off nt
	v_add_co_u32_e32 v36, vcc, s37, v4
	s_mov_b32 s38, 0x22000
	s_nop 0
	v_addc_co_u32_e32 v37, vcc, 0, v5, vcc
	s_waitcnt vmcnt(62)
	v_add_co_u32_e32 v38, vcc, s38, v4
	s_mov_b32 s39, 0x24000
	s_nop 0
	v_addc_co_u32_e32 v39, vcc, 0, v5, vcc
	v_add_co_u32_e32 v46, vcc, s39, v4
	s_mov_b32 s40, 0x26000
	s_nop 0
	v_addc_co_u32_e32 v47, vcc, 0, v5, vcc
	s_waitcnt vmcnt(60)
	v_add_co_u32_e32 v52, vcc, s40, v4
	s_mov_b32 s41, 0x28000
	s_waitcnt vmcnt(59)
	v_addc_co_u32_e32 v53, vcc, 0, v5, vcc
	global_load_dword v41, v[36:37], off offset:-4096 nt
	global_load_dword v42, v[36:37], off nt
	global_load_dword v43, v[38:39], off offset:-4096 nt
	global_load_dword v44, v[38:39], off nt
	global_load_dword v48, v[46:47], off offset:-4096 nt
	global_load_dword v50, v[46:47], off nt
	global_load_dword v51, v[52:53], off offset:-4096 nt
	s_nop 0
	global_load_dword v52, v[52:53], off nt
	v_add_co_u32_e32 v36, vcc, s41, v4
	s_mov_b32 s42, 0x2a000
	s_nop 0
	v_addc_co_u32_e32 v37, vcc, 0, v5, vcc
	v_add_co_u32_e32 v38, vcc, s42, v4
	s_mov_b32 s43, 0x2c000
	s_nop 0
	v_addc_co_u32_e32 v39, vcc, 0, v5, vcc
	v_add_co_u32_e32 v46, vcc, s43, v4
	s_mov_b32 s44, 0x2e000
	s_nop 0
	v_addc_co_u32_e32 v47, vcc, 0, v5, vcc
	s_waitcnt vmcnt(60)
	v_add_co_u32_e32 v60, vcc, s44, v4
	s_mov_b32 s45, 0x30000
	s_waitcnt vmcnt(59)
	v_addc_co_u32_e32 v61, vcc, 0, v5, vcc
	global_load_dword v53, v[36:37], off offset:-4096 nt
	global_load_dword v54, v[36:37], off nt
	global_load_dword v55, v[38:39], off offset:-4096 nt
	global_load_dword v56, v[38:39], off nt
	global_load_dword v57, v[46:47], off offset:-4096 nt
	global_load_dword v58, v[46:47], off nt
	global_load_dword v59, v[60:61], off offset:-4096 nt
	s_nop 0
	global_load_dword v60, v[60:61], off nt
	v_add_co_u32_e32 v36, vcc, s45, v4
	s_mov_b32 s46, 0x32000
	s_nop 0
	v_addc_co_u32_e32 v37, vcc, 0, v5, vcc
	v_add_co_u32_e32 v38, vcc, s46, v4
	s_mov_b32 s47, 0x34000
	s_nop 0
	v_addc_co_u32_e32 v39, vcc, 0, v5, vcc
	v_add_co_u32_e32 v46, vcc, s47, v4
	s_mov_b32 s48, 0x36000
	s_nop 0
	v_addc_co_u32_e32 v47, vcc, 0, v5, vcc
	s_waitcnt vmcnt(60)
	v_add_co_u32_e32 v68, vcc, s48, v4
	s_mov_b32 s49, 0x38000
	s_waitcnt vmcnt(59)
	v_addc_co_u32_e32 v69, vcc, 0, v5, vcc
	global_load_dword v61, v[36:37], off offset:-4096 nt
	global_load_dword v62, v[36:37], off nt
	global_load_dword v63, v[38:39], off offset:-4096 nt
	global_load_dword v64, v[38:39], off nt
	global_load_dword v65, v[46:47], off offset:-4096 nt
	global_load_dword v66, v[46:47], off nt
	global_load_dword v67, v[68:69], off offset:-4096 nt
	s_nop 0
	global_load_dword v68, v[68:69], off nt
	v_add_co_u32_e32 v36, vcc, s49, v4
	s_mov_b32 s50, 0x3a000
	s_nop 0
	v_addc_co_u32_e32 v37, vcc, 0, v5, vcc
	v_add_co_u32_e32 v38, vcc, s50, v4
	s_mov_b32 s4, 0x3c000
	s_nop 0
	v_addc_co_u32_e32 v39, vcc, 0, v5, vcc
	v_add_co_u32_e32 v46, vcc, s4, v4
	s_mov_b32 s4, 0x3e000
	s_nop 0
	v_addc_co_u32_e32 v47, vcc, 0, v5, vcc
	s_waitcnt vmcnt(60)
	v_add_co_u32_e32 v76, vcc, s4, v4
	s_mov_b32 s4, 0x3f000
	s_waitcnt vmcnt(59)
	v_addc_co_u32_e32 v77, vcc, 0, v5, vcc
	v_add_co_u32_e32 v4, vcc, s4, v4
	global_load_dword v69, v[36:37], off offset:-4096 nt
	global_load_dword v70, v[36:37], off nt
	global_load_dword v71, v[38:39], off offset:-4096 nt
	global_load_dword v72, v[38:39], off nt
	global_load_dword v73, v[46:47], off offset:-4096 nt
	global_load_dword v74, v[46:47], off nt
	global_load_dword v75, v[76:77], off offset:-4096 nt
	s_nop 0
	global_load_dword v77, v[76:77], off nt
	v_addc_co_u32_e32 v5, vcc, 0, v5, vcc
	global_load_dword v76, v2, s[2:3] nt
	global_load_dword v78, v[6:7], off offset:-4096 nt
	global_load_dword v79, v[6:7], off nt
	global_load_dword v45, v[8:9], off offset:-4096 nt
	global_load_dword v46, v[8:9], off nt
	global_load_dword v47, v[10:11], off offset:-4096 nt
	global_load_dword v49, v[10:11], off nt
	global_load_dword v80, v[4:5], off nt
	v_add_u32_e32 v8, s6, v2
	v_lshlrev_b32_e32 v2, 3, v0
	v_and_b32_e32 v2, 56, v2
	v_mul_u32_u24_e32 v6, 0x104, v2
	v_lshlrev_b32_e32 v2, 1, v2
	v_lshl_add_u64 v[4:5], s[82:83], 0, v[2:3]
	s_mov_b64 s[2:3], 0x2500000
	v_lshlrev_b32_e32 v2, 2, v1
	s_mov_b32 s51, 0x3b000
	v_lshl_add_u64 v[4:5], v[4:5], 0, s[2:3]
	v_add3_u32 v9, s6, v6, v2
	v_or_b32_e32 v10, 8, v1
	v_or_b32_e32 v11, 16, v1
	v_or_b32_e32 v36, 24, v1
	v_or_b32_e32 v37, 32, v1
	v_or_b32_e32 v38, 40, v1
	v_or_b32_e32 v39, 48, v1
	v_or_b32_e32 v40, 56, v1
	v_lshlrev_b32_e32 v2, 2, v198
	s_movk_i32 s52, 0x7fff
	s_mov_b32 s53, 0xffff0000
	s_branch .LBB0_192

.LBB0_192:
	v_add_u32_e32 v6, 0x400, v8
	s_waitcnt vmcnt(6)
	ds_write2_b32 v8, v76, v78 offset1:65
	s_waitcnt vmcnt(4)
	ds_write2_b32 v8, v79, v45 offset0:130 offset1:195
	s_waitcnt vmcnt(2)
	ds_write2_b32 v6, v46, v47 offset0:4 offset1:69
	s_waitcnt vmcnt(1)
	ds_write2_b32 v6, v49, v12 offset0:134 offset1:199
	v_add_u32_e32 v6, 0x800, v8
	ds_write2_b32 v6, v13, v14 offset0:8 offset1:73
	ds_write2_b32 v6, v15, v16 offset0:138 offset1:203
	v_add_u32_e32 v6, 0xc00, v8
	ds_write2_b32 v6, v17, v18 offset0:12 offset1:77
	ds_write2_b32 v6, v19, v20 offset0:142 offset1:207
	v_add_u32_e32 v6, 0x1000, v8
	ds_write2_b32 v6, v21, v22 offset0:16 offset1:81
	ds_write2_b32 v6, v23, v24 offset0:146 offset1:211
	v_add_u32_e32 v6, 0x1400, v8
	ds_write2_b32 v6, v25, v26 offset0:20 offset1:85
	ds_write2_b32 v6, v27, v28 offset0:150 offset1:215
	v_add_u32_e32 v6, 0x1800, v8
	ds_write2_b32 v6, v29, v30 offset0:24 offset1:89
	ds_write2_b32 v6, v31, v32 offset0:154 offset1:219
	v_add_u32_e32 v6, 0x1c00, v8
	ds_write2_b32 v6, v33, v34 offset0:28 offset1:93
	ds_write2_b32 v6, v35, v41 offset0:158 offset1:223
	v_add_u32_e32 v6, 0x2000, v8
	ds_write2_b32 v6, v42, v43 offset0:32 offset1:97
	ds_write2_b32 v6, v44, v48 offset0:162 offset1:227
	v_add_u32_e32 v6, 0x2400, v8
	ds_write2_b32 v6, v50, v51 offset0:36 offset1:101
	ds_write2_b32 v6, v52, v53 offset0:166 offset1:231
	v_add_u32_e32 v6, 0x2800, v8
	ds_write2_b32 v6, v54, v55 offset0:40 offset1:105
	ds_write2_b32 v6, v56, v57 offset0:170 offset1:235
	v_add_u32_e32 v6, 0x2c00, v8
	ds_write2_b32 v6, v58, v59 offset0:44 offset1:109
	ds_write2_b32 v6, v60, v61 offset0:174 offset1:239
	v_add_u32_e32 v6, 0x3000, v8
	ds_write2_b32 v6, v62, v63 offset0:48 offset1:113
	ds_write2_b32 v6, v64, v65 offset0:178 offset1:243
	v_add_u32_e32 v6, 0x3400, v8
	ds_write2_b32 v6, v66, v67 offset0:52 offset1:117
	ds_write2_b32 v6, v68, v69 offset0:182 offset1:247
	v_add_u32_e32 v6, 0x3800, v8
	ds_write2_b32 v6, v70, v71 offset0:56 offset1:121
	ds_write2_b32 v6, v72, v73 offset0:186 offset1:251
	v_add_u32_e32 v6, 0x3c00, v8
	ds_write2_b32 v6, v74, v75 offset0:60 offset1:125
	s_waitcnt vmcnt(0)
	ds_write2_b32 v6, v77, v80 offset0:190 offset1:255
	s_waitcnt lgkmcnt(0)
	s_add_i32 s54, s55, s85
	s_cmpk_gt_i32 s54, 0xff
	s_cselect_b64 s[2:3], -1, 0
	s_and_b64 vcc, exec, s[2:3]
	s_cbranch_vccnz .LBB0_191
	s_ashr_i32 s4, s54, 31
	s_lshr_b32 s4, s4, 24
	s_add_i32 s4, s54, s4
	s_and_b32 s4, s4, 0xff00
	s_sub_i32 s56, s54, s4
	s_sext_i32_i16 s4, s56
	s_bfe_u32 s4, s4, 0x4001b
	s_add_i32 s57, s56, s4
	s_sext_i32_i16 s4, s57
	s_lshl_b32 s4, s4, 2
	s_andn2_b32 s4, s4, 63
	s_ashr_i32 s5, s4, 31
	s_lshl_b64 s[4:5], s[4:5], 12
	s_add_u32 s58, s0, s4
	s_addc_u32 s59, s1, s5
	s_and_b32 s4, s57, 0xfff0
	s_sub_i32 s4, s56, s4
	s_sext_i32_i16 s4, s4
	s_lshl_b32 s4, s4, 6
	s_ashr_i32 s5, s4, 31
	s_lshl_b64 s[4:5], s[4:5], 2
	s_add_u32 s4, s58, s4
	s_addc_u32 s5, s59, s5
	v_lshl_add_u64 v[6:7], s[4:5], 0, v[2:3]
	v_add_co_u32_e32 v74, vcc, s7, v6
	s_nop 1
	v_addc_co_u32_e32 v75, vcc, 0, v7, vcc
	v_add_co_u32_e32 v12, vcc, s22, v6
	s_nop 1
	v_addc_co_u32_e32 v13, vcc, 0, v7, vcc
	v_add_co_u32_e32 v14, vcc, s23, v6
	s_nop 1
	v_addc_co_u32_e32 v15, vcc, 0, v7, vcc
	v_add_co_u32_e32 v16, vcc, s24, v6
	s_nop 1
	v_addc_co_u32_e32 v17, vcc, 0, v7, vcc
	v_add_co_u32_e32 v18, vcc, s25, v6
	s_nop 1
	v_addc_co_u32_e32 v19, vcc, 0, v7, vcc
	global_load_dword v45, v[12:13], off offset:-4096 nt
	global_load_dword v46, v[12:13], off nt
	global_load_dword v47, v[14:15], off offset:-4096 nt
	global_load_dword v49, v[14:15], off nt
	s_nop 0
	global_load_dword v12, v[16:17], off offset:-4096 nt
	global_load_dword v13, v[16:17], off nt
	global_load_dword v14, v[18:19], off offset:-4096 nt
	global_load_dword v15, v[18:19], off nt
	v_add_co_u32_e32 v18, vcc, s26, v6
	s_nop 1
	v_addc_co_u32_e32 v19, vcc, 0, v7, vcc
	v_add_co_u32_e32 v20, vcc, s27, v6
	s_nop 1
	v_addc_co_u32_e32 v21, vcc, 0, v7, vcc
	v_add_co_u32_e32 v22, vcc, s28, v6
	s_nop 1
	v_addc_co_u32_e32 v23, vcc, 0, v7, vcc
	v_add_co_u32_e32 v24, vcc, s29, v6
	s_nop 1
	v_addc_co_u32_e32 v25, vcc, 0, v7, vcc
	v_add_co_u32_e32 v26, vcc, s30, v6
	global_load_dword v16, v[18:19], off offset:-4096 nt
	global_load_dword v17, v[18:19], off nt
	s_nop 0
	global_load_dword v18, v[20:21], off offset:-4096 nt
	global_load_dword v19, v[20:21], off nt
	s_nop 0
	global_load_dword v20, v[22:23], off offset:-4096 nt
	global_load_dword v21, v[22:23], off nt
	s_nop 0
	global_load_dword v22, v[24:25], off offset:-4096 nt
	global_load_dword v23, v[24:25], off nt
	v_addc_co_u32_e32 v27, vcc, 0, v7, vcc
	v_add_co_u32_e32 v28, vcc, s31, v6
	s_nop 1
	v_addc_co_u32_e32 v29, vcc, 0, v7, vcc
	v_add_co_u32_e32 v30, vcc, s33, v6
	s_nop 1
	v_addc_co_u32_e32 v31, vcc, 0, v7, vcc
	v_add_co_u32_e32 v32, vcc, s34, v6
	s_nop 1
	v_addc_co_u32_e32 v33, vcc, 0, v7, vcc
	v_add_co_u32_e32 v34, vcc, s35, v6
	global_load_dword v24, v[26:27], off offset:-4096 nt
	global_load_dword v25, v[26:27], off nt
	s_nop 0
	global_load_dword v26, v[28:29], off offset:-4096 nt
	global_load_dword v27, v[28:29], off nt
	s_nop 0
	global_load_dword v28, v[30:31], off offset:-4096 nt
	global_load_dword v29, v[30:31], off nt
	s_nop 0
	global_load_dword v30, v[32:33], off offset:-4096 nt
	global_load_dword v31, v[32:33], off nt
	v_addc_co_u32_e32 v35, vcc, 0, v7, vcc
	v_add_co_u32_e32 v42, vcc, s36, v6
	s_nop 1
	v_addc_co_u32_e32 v43, vcc, 0, v7, vcc
	v_add_co_u32_e32 v50, vcc, s37, v6
	s_nop 1
	v_addc_co_u32_e32 v51, vcc, 0, v7, vcc
	v_add_co_u32_e32 v52, vcc, s38, v6
	s_nop 1
	v_addc_co_u32_e32 v53, vcc, 0, v7, vcc
	global_load_dword v32, v[34:35], off offset:-4096 nt
	global_load_dword v33, v[34:35], off nt
	s_nop 0
	global_load_dword v34, v[42:43], off offset:-4096 nt
	global_load_dword v35, v[42:43], off nt
	global_load_dword v41, v[50:51], off offset:-4096 nt
	s_nop 0
	global_load_dword v42, v[50:51], off nt
	global_load_dword v43, v[52:53], off offset:-4096 nt
	global_load_dword v44, v[52:53], off nt
	v_add_co_u32_e32 v50, vcc, s39, v6
	s_nop 1
	v_addc_co_u32_e32 v51, vcc, 0, v7, vcc
	v_add_co_u32_e32 v52, vcc, s40, v6
	s_nop 1
	v_addc_co_u32_e32 v53, vcc, 0, v7, vcc
	v_add_co_u32_e32 v54, vcc, s41, v6
	s_nop 1
	v_addc_co_u32_e32 v55, vcc, 0, v7, vcc
	v_add_co_u32_e32 v56, vcc, s42, v6
	s_nop 1
	v_addc_co_u32_e32 v57, vcc, 0, v7, vcc
	v_add_co_u32_e32 v58, vcc, s43, v6
	global_load_dword v48, v[50:51], off offset:-4096 nt
	s_nop 0
	global_load_dword v50, v[50:51], off nt
	s_nop 0
	global_load_dword v51, v[52:53], off offset:-4096 nt
	s_nop 0
	global_load_dword v52, v[52:53], off nt
	s_nop 0
	global_load_dword v53, v[54:55], off offset:-4096 nt
	s_nop 0
	global_load_dword v54, v[54:55], off nt
	s_nop 0
	global_load_dword v55, v[56:57], off offset:-4096 nt
	s_nop 0
	global_load_dword v56, v[56:57], off nt
	v_addc_co_u32_e32 v59, vcc, 0, v7, vcc
	v_add_co_u32_e32 v60, vcc, s44, v6
	s_nop 1
	v_addc_co_u32_e32 v61, vcc, 0, v7, vcc
	v_add_co_u32_e32 v62, vcc, s45, v6
	s_nop 1
	v_addc_co_u32_e32 v63, vcc, 0, v7, vcc
	v_add_co_u32_e32 v64, vcc, s46, v6
	s_nop 1
	v_addc_co_u32_e32 v65, vcc, 0, v7, vcc
	v_add_co_u32_e32 v66, vcc, s47, v6
	global_load_dword v57, v[58:59], off offset:-4096 nt
	s_nop 0
	global_load_dword v58, v[58:59], off nt
	s_nop 0
	global_load_dword v59, v[60:61], off offset:-4096 nt
	s_nop 0
	global_load_dword v60, v[60:61], off nt
	s_nop 0
	global_load_dword v61, v[62:63], off offset:-4096 nt
	s_nop 0
	global_load_dword v62, v[62:63], off nt
	s_nop 0
	global_load_dword v63, v[64:65], off offset:-4096 nt
	s_nop 0
	global_load_dword v64, v[64:65], off nt
	v_addc_co_u32_e32 v67, vcc, 0, v7, vcc
	v_add_co_u32_e32 v68, vcc, s48, v6
	s_nop 1
	v_addc_co_u32_e32 v69, vcc, 0, v7, vcc
	v_add_co_u32_e32 v70, vcc, s49, v6
	s_nop 1
	v_addc_co_u32_e32 v71, vcc, 0, v7, vcc
	v_add_co_u32_e32 v72, vcc, s50, v6
	s_nop 1
	v_addc_co_u32_e32 v73, vcc, 0, v7, vcc
	v_add_co_u32_e32 v80, vcc, s51, v6
	global_load_dword v65, v[66:67], off offset:-4096 nt
	s_nop 0
	global_load_dword v66, v[66:67], off nt
	s_nop 0
	global_load_dword v67, v[68:69], off offset:-4096 nt
	s_nop 0
	global_load_dword v68, v[68:69], off nt
	s_nop 0
	global_load_dword v69, v[70:71], off offset:-4096 nt
	s_nop 0
	global_load_dword v70, v[70:71], off nt
	s_nop 0
	global_load_dword v71, v[72:73], off offset:-4096 nt
	s_nop 0
	global_load_dword v72, v[72:73], off nt
	v_addc_co_u32_e32 v81, vcc, 0, v7, vcc
	v_add_co_u32_e32 v82, vcc, 0x3c000, v6
	s_nop 1
	v_addc_co_u32_e32 v83, vcc, 0, v7, vcc
	v_add_co_u32_e32 v84, vcc, 0x3d000, v6
	s_nop 1
	v_addc_co_u32_e32 v85, vcc, 0, v7, vcc
	v_add_co_u32_e32 v86, vcc, 0x3e000, v6
	s_nop 1
	v_addc_co_u32_e32 v87, vcc, 0, v7, vcc
	v_add_co_u32_e32 v6, vcc, 0x3f000, v6
	s_nop 1
	v_addc_co_u32_e32 v7, vcc, 0, v7, vcc
	global_load_dword v76, v2, s[4:5] nt
	global_load_dword v78, v[74:75], off offset:-4096 nt
	global_load_dword v79, v[74:75], off nt
	global_load_dword v73, v[80:81], off nt
	s_nop 0
	global_load_dword v74, v[82:83], off nt
	global_load_dword v75, v[84:85], off nt
	global_load_dword v77, v[86:87], off nt
	global_load_dword v80, v[6:7], off nt
	s_branch .LBB0_191
.LBB0_194:
	v_readlane_b32 s88, v252, 14
	s_cmpk_gt_i32 s88, 0x1ff
	s_mov_b32 s96, s80
	s_cbranch_scc1 .LBB0_199
	s_ashr_i32 s0, s88, 31
	s_lshr_b32 s0, s0, 23
	s_add_i32 s0, s88, s0
	s_and_b32 s0, s0, 0xfe00
	s_sub_i32 s2, s88, s0
	s_sext_i32_i16 s0, s2
	s_bfe_u32 s0, s0, 0x5001a
	s_add_i32 s3, s2, s0
	s_sext_i32_i16 s0, s3
	s_lshl_b32 s0, s0, 1
	s_andn2_b32 s0, s0, 63
	s_ashr_i32 s1, s0, 31
	s_lshl_b64 s[0:1], s[0:1], 13
	s_waitcnt lgkmcnt(0)
	s_add_u32 s4, s8, s0
	s_addc_u32 s5, s9, s1
	s_and_b32 s3, s3, 0xffe0
	s_sub_i32 s2, s2, s3
	s_sext_i32_i16 s2, s2
	s_lshl_b32 s2, s2, 6
	s_ashr_i32 s3, s2, 31
	s_lshl_b64 s[2:3], s[2:3], 2
	s_add_u32 s4, s4, s2
	s_addc_u32 s5, s5, s3
	v_mov_b32_e32 v3, 0
	v_lshlrev_b32_e32 v2, 2, v198
	v_lshl_add_u64 v[4:5], s[4:5], 0, v[2:3]
	s_movk_i32 s7, 0x2000
	v_add_co_u32_e32 v6, vcc, s7, v4
	s_movk_i32 s22, 0x4000
	s_nop 0
	v_addc_co_u32_e32 v7, vcc, 0, v5, vcc
	global_load_dword v19, v2, s[4:5] nt
	global_load_dword v20, v[6:7], off nt
	v_add_co_u32_e32 v6, vcc, s22, v4
	s_movk_i32 s23, 0x6000
	s_nop 0
	v_addc_co_u32_e32 v7, vcc, 0, v5, vcc
	global_load_dword v21, v[6:7], off nt
	v_add_co_u32_e32 v6, vcc, s23, v4
	s_mov_b32 s24, 0x8000
	s_nop 0
	v_addc_co_u32_e32 v7, vcc, 0, v5, vcc
	global_load_dword v22, v[6:7], off nt
	v_add_co_u32_e32 v6, vcc, s24, v4
	s_mov_b32 s25, 0xa000
	s_nop 0
	v_addc_co_u32_e32 v7, vcc, 0, v5, vcc
	global_load_dword v23, v[6:7], off nt
	v_add_co_u32_e32 v6, vcc, s25, v4
	s_mov_b32 s26, 0xc000
	s_nop 0
	v_addc_co_u32_e32 v7, vcc, 0, v5, vcc
	global_load_dword v24, v[6:7], off nt
	v_add_co_u32_e32 v6, vcc, s26, v4
	s_mov_b32 s27, 0xe000
	s_nop 0
	v_addc_co_u32_e32 v7, vcc, 0, v5, vcc
	global_load_dword v25, v[6:7], off nt
	v_add_co_u32_e32 v6, vcc, s27, v4
	s_mov_b32 s28, 0x10000
	s_nop 0
	v_addc_co_u32_e32 v7, vcc, 0, v5, vcc
	global_load_dword v26, v[6:7], off nt
	v_add_co_u32_e32 v6, vcc, s28, v4
	s_mov_b32 s29, 0x12000
	s_nop 0
	v_addc_co_u32_e32 v7, vcc, 0, v5, vcc
	global_load_dword v27, v[6:7], off nt
	v_add_co_u32_e32 v6, vcc, s29, v4
	s_mov_b32 s30, 0x14000
	s_nop 0
	v_addc_co_u32_e32 v7, vcc, 0, v5, vcc
	global_load_dword v28, v[6:7], off nt
	v_add_co_u32_e32 v6, vcc, s30, v4
	s_mov_b32 s31, 0x16000
	s_nop 0
	v_addc_co_u32_e32 v7, vcc, 0, v5, vcc
	global_load_dword v29, v[6:7], off nt
	v_add_co_u32_e32 v6, vcc, s31, v4
	s_mov_b32 s33, 0x18000
	s_nop 0
	v_addc_co_u32_e32 v7, vcc, 0, v5, vcc
	global_load_dword v30, v[6:7], off nt
	v_add_co_u32_e32 v6, vcc, s33, v4
	s_mov_b32 s34, 0x1a000
	s_nop 0
	v_addc_co_u32_e32 v7, vcc, 0, v5, vcc
	global_load_dword v31, v[6:7], off nt
	v_add_co_u32_e32 v6, vcc, s34, v4
	s_mov_b32 s35, 0x1c000
	s_nop 0
	v_addc_co_u32_e32 v7, vcc, 0, v5, vcc
	global_load_dword v32, v[6:7], off nt
	v_add_co_u32_e32 v6, vcc, s35, v4
	s_mov_b32 s36, 0x1e000
	s_nop 0
	v_addc_co_u32_e32 v7, vcc, 0, v5, vcc
	global_load_dword v33, v[6:7], off nt
	v_add_co_u32_e32 v6, vcc, s36, v4
	s_mov_b32 s37, 0x20000
	s_nop 0
	v_addc_co_u32_e32 v7, vcc, 0, v5, vcc
	global_load_dword v34, v[6:7], off nt
	v_add_co_u32_e32 v6, vcc, s37, v4
	s_mov_b32 s38, 0x22000
	s_nop 0
	v_addc_co_u32_e32 v7, vcc, 0, v5, vcc
	global_load_dword v35, v[6:7], off nt
	v_add_co_u32_e32 v6, vcc, s38, v4
	s_mov_b32 s39, 0x24000
	s_nop 0
	v_addc_co_u32_e32 v7, vcc, 0, v5, vcc
	global_load_dword v36, v[6:7], off nt
	v_add_co_u32_e32 v6, vcc, s39, v4
	s_mov_b32 s40, 0x26000
	s_nop 0
	v_addc_co_u32_e32 v7, vcc, 0, v5, vcc
	global_load_dword v37, v[6:7], off nt
	v_add_co_u32_e32 v6, vcc, s40, v4
	s_mov_b32 s41, 0x28000
	s_nop 0
	v_addc_co_u32_e32 v7, vcc, 0, v5, vcc
	global_load_dword v38, v[6:7], off nt
	v_add_co_u32_e32 v6, vcc, s41, v4
	s_mov_b32 s42, 0x2a000
	s_nop 0
	v_addc_co_u32_e32 v7, vcc, 0, v5, vcc
	global_load_dword v39, v[6:7], off nt
	v_add_co_u32_e32 v6, vcc, s42, v4
	s_mov_b32 s43, 0x2c000
	s_nop 0
	v_addc_co_u32_e32 v7, vcc, 0, v5, vcc
	global_load_dword v40, v[6:7], off nt
	v_add_co_u32_e32 v6, vcc, s43, v4
	s_mov_b32 s44, 0x2e000
	s_nop 0
	v_addc_co_u32_e32 v7, vcc, 0, v5, vcc
	global_load_dword v41, v[6:7], off nt
	v_add_co_u32_e32 v6, vcc, s44, v4
	s_mov_b32 s45, 0x30000
	s_nop 0
	v_addc_co_u32_e32 v7, vcc, 0, v5, vcc
	global_load_dword v42, v[6:7], off nt
	v_add_co_u32_e32 v6, vcc, s45, v4
	s_mov_b32 s46, 0x32000
	s_nop 0
	v_addc_co_u32_e32 v7, vcc, 0, v5, vcc
	global_load_dword v43, v[6:7], off nt
	v_add_co_u32_e32 v6, vcc, s46, v4
	s_mov_b32 s47, 0x34000
	s_nop 0
	v_addc_co_u32_e32 v7, vcc, 0, v5, vcc
	global_load_dword v44, v[6:7], off nt
	v_add_co_u32_e32 v6, vcc, s47, v4
	s_mov_b32 s48, 0x36000
	s_nop 0
	v_addc_co_u32_e32 v7, vcc, 0, v5, vcc
	global_load_dword v45, v[6:7], off nt
	v_add_co_u32_e32 v6, vcc, s48, v4
	s_mov_b32 s49, 0x38000
	s_nop 0
	v_addc_co_u32_e32 v7, vcc, 0, v5, vcc
	global_load_dword v46, v[6:7], off nt
	v_add_co_u32_e32 v6, vcc, s49, v4
	s_mov_b32 s50, 0x3a000
	s_nop 0
	v_addc_co_u32_e32 v7, vcc, 0, v5, vcc
	global_load_dword v47, v[6:7], off nt
	v_add_co_u32_e32 v6, vcc, s50, v4
	s_mov_b32 s51, 0x3c000
	s_nop 0
	v_addc_co_u32_e32 v7, vcc, 0, v5, vcc
	global_load_dword v48, v[6:7], off nt
	v_add_co_u32_e32 v6, vcc, s51, v4
	s_mov_b32 s52, 0x3e000
	s_nop 0
	v_addc_co_u32_e32 v7, vcc, 0, v5, vcc
	global_load_dword v49, v[6:7], off nt
	v_add_co_u32_e32 v6, vcc, s52, v4
	s_mov_b32 s53, 0x40000
	s_nop 0
	v_addc_co_u32_e32 v7, vcc, 0, v5, vcc
	global_load_dword v50, v[6:7], off nt
	v_add_co_u32_e32 v6, vcc, s53, v4
	s_mov_b32 s54, 0x42000
	s_nop 0
	v_addc_co_u32_e32 v7, vcc, 0, v5, vcc
	global_load_dword v51, v[6:7], off nt
	v_add_co_u32_e32 v6, vcc, s54, v4
	s_mov_b32 s55, 0x44000
	s_nop 0
	v_addc_co_u32_e32 v7, vcc, 0, v5, vcc
	global_load_dword v52, v[6:7], off nt
	v_add_co_u32_e32 v6, vcc, s55, v4
	s_mov_b32 s56, 0x46000
	s_nop 0
	v_addc_co_u32_e32 v7, vcc, 0, v5, vcc
	global_load_dword v53, v[6:7], off nt
	v_add_co_u32_e32 v6, vcc, s56, v4
	s_mov_b32 s57, 0x48000
	s_nop 0
	v_addc_co_u32_e32 v7, vcc, 0, v5, vcc
	global_load_dword v54, v[6:7], off nt
	v_add_co_u32_e32 v6, vcc, s57, v4
	s_mov_b32 s58, 0x4a000
	s_nop 0
	v_addc_co_u32_e32 v7, vcc, 0, v5, vcc
	global_load_dword v55, v[6:7], off nt
	v_add_co_u32_e32 v6, vcc, s58, v4
	s_mov_b32 s59, 0x4c000
	s_nop 0
	v_addc_co_u32_e32 v7, vcc, 0, v5, vcc
	global_load_dword v56, v[6:7], off nt
	v_add_co_u32_e32 v6, vcc, s59, v4
	s_mov_b32 s60, 0x4e000
	s_nop 0
	v_addc_co_u32_e32 v7, vcc, 0, v5, vcc
	global_load_dword v57, v[6:7], off nt
	v_add_co_u32_e32 v6, vcc, s60, v4
	s_mov_b32 s61, 0x50000
	s_nop 0
	v_addc_co_u32_e32 v7, vcc, 0, v5, vcc
	global_load_dword v58, v[6:7], off nt
	v_add_co_u32_e32 v6, vcc, s61, v4
	s_mov_b32 s62, 0x52000
	s_nop 0
	v_addc_co_u32_e32 v7, vcc, 0, v5, vcc
	global_load_dword v59, v[6:7], off nt
	v_add_co_u32_e32 v6, vcc, s62, v4
	s_mov_b32 s63, 0x54000
	s_nop 0
	v_addc_co_u32_e32 v7, vcc, 0, v5, vcc
	global_load_dword v60, v[6:7], off nt
	v_add_co_u32_e32 v6, vcc, s63, v4
	s_mov_b32 s64, 0x56000
	s_nop 0
	v_addc_co_u32_e32 v7, vcc, 0, v5, vcc
	global_load_dword v61, v[6:7], off nt
	v_add_co_u32_e32 v6, vcc, s64, v4
	s_mov_b32 s65, 0x58000
	s_nop 0
	v_addc_co_u32_e32 v7, vcc, 0, v5, vcc
	global_load_dword v62, v[6:7], off nt
	v_add_co_u32_e32 v6, vcc, s65, v4
	s_mov_b32 s66, 0x5a000
	s_nop 0
	v_addc_co_u32_e32 v7, vcc, 0, v5, vcc
	global_load_dword v63, v[6:7], off nt
	v_add_co_u32_e32 v6, vcc, s66, v4
	s_mov_b32 s67, 0x5c000
	s_nop 0
	v_addc_co_u32_e32 v7, vcc, 0, v5, vcc
	global_load_dword v64, v[6:7], off nt
	v_add_co_u32_e32 v6, vcc, s67, v4
	s_mov_b32 s68, 0x5e000
	s_nop 0
	v_addc_co_u32_e32 v7, vcc, 0, v5, vcc
	global_load_dword v65, v[6:7], off nt
	v_add_co_u32_e32 v6, vcc, s68, v4
	s_mov_b32 s69, 0x60000
	s_nop 0
	v_addc_co_u32_e32 v7, vcc, 0, v5, vcc
	global_load_dword v66, v[6:7], off nt
	v_add_co_u32_e32 v6, vcc, s69, v4
	s_mov_b32 s70, 0x62000
	s_nop 0
	v_addc_co_u32_e32 v7, vcc, 0, v5, vcc
	global_load_dword v67, v[6:7], off nt
	v_add_co_u32_e32 v6, vcc, s70, v4
	s_mov_b32 s71, 0x64000
	s_nop 0
	v_addc_co_u32_e32 v7, vcc, 0, v5, vcc
	global_load_dword v68, v[6:7], off nt
	v_add_co_u32_e32 v6, vcc, s71, v4
	s_mov_b32 s72, 0x66000
	s_nop 0
	v_addc_co_u32_e32 v7, vcc, 0, v5, vcc
	global_load_dword v69, v[6:7], off nt
	v_add_co_u32_e32 v6, vcc, s72, v4
	s_mov_b32 s73, 0x68000
	s_nop 0
	v_addc_co_u32_e32 v7, vcc, 0, v5, vcc
	global_load_dword v70, v[6:7], off nt
	v_add_co_u32_e32 v6, vcc, s73, v4
	s_mov_b32 s74, 0x6a000
	s_nop 0
	v_addc_co_u32_e32 v7, vcc, 0, v5, vcc
	global_load_dword v71, v[6:7], off nt
	v_add_co_u32_e32 v6, vcc, s74, v4
	s_mov_b32 s75, 0x6c000
	s_nop 0
	v_addc_co_u32_e32 v7, vcc, 0, v5, vcc
	global_load_dword v72, v[6:7], off nt
	v_add_co_u32_e32 v6, vcc, s75, v4
	s_mov_b32 s76, 0x6e000
	s_nop 0
	v_addc_co_u32_e32 v7, vcc, 0, v5, vcc
	global_load_dword v73, v[6:7], off nt
	v_add_co_u32_e32 v6, vcc, s76, v4
	s_mov_b32 s77, 0x70000
	s_nop 0
	v_addc_co_u32_e32 v7, vcc, 0, v5, vcc
	global_load_dword v74, v[6:7], off nt
	v_add_co_u32_e32 v6, vcc, s77, v4
	s_mov_b32 s78, 0x72000
	s_nop 0
	v_addc_co_u32_e32 v7, vcc, 0, v5, vcc
	global_load_dword v75, v[6:7], off nt
	v_add_co_u32_e32 v6, vcc, s78, v4
	s_mov_b32 s79, 0x74000
	s_nop 0
	v_addc_co_u32_e32 v7, vcc, 0, v5, vcc
	global_load_dword v76, v[6:7], off nt
	v_add_co_u32_e32 v6, vcc, s79, v4
	s_mov_b32 s80, 0x76000
	s_nop 0
	v_addc_co_u32_e32 v7, vcc, 0, v5, vcc
	global_load_dword v77, v[6:7], off nt
	v_add_co_u32_e32 v6, vcc, s80, v4
	s_mov_b32 s4, 0x78000
	s_nop 0
	v_addc_co_u32_e32 v7, vcc, 0, v5, vcc
	global_load_dword v78, v[6:7], off nt
	v_add_co_u32_e32 v6, vcc, s4, v4
	s_mov_b32 s4, 0x7a000
	s_nop 0
	v_addc_co_u32_e32 v7, vcc, 0, v5, vcc
	global_load_dword v79, v[6:7], off nt
	v_add_co_u32_e32 v6, vcc, s4, v4
	s_mov_b32 s4, 0x7c000
	s_nop 0
	v_addc_co_u32_e32 v7, vcc, 0, v5, vcc
	global_load_dword v80, v[6:7], off nt
	v_add_co_u32_e32 v6, vcc, s4, v4
	s_mov_b32 s4, 0x7e000
	s_nop 0
	v_addc_co_u32_e32 v7, vcc, 0, v5, vcc
	v_add_co_u32_e32 v4, vcc, s4, v4
	global_load_dword v81, v[6:7], off nt
	s_nop 0
	v_addc_co_u32_e32 v5, vcc, 0, v5, vcc
	global_load_dword v5, v[4:5], off nt
	v_add_u32_e32 v10, s6, v2
	v_lshlrev_b32_e32 v2, 3, v0
	v_and_b32_e32 v4, 56, v2
	v_lshlrev_b32_e32 v2, 1, v4
	v_mul_u32_u24_e32 v8, 0x104, v4
	v_lshl_add_u64 v[6:7], s[82:83], 0, v[2:3]
	s_mov_b64 s[4:5], 0x2700000
	v_lshlrev_b32_e32 v2, 2, v1
	s_mov_b32 s12, s90
	v_lshl_add_u64 v[6:7], v[6:7], 0, s[4:5]
	v_add3_u32 v11, s6, v8, v2
	s_waitcnt vmcnt(62)
	v_or_b32_e32 v12, 8, v1
	v_or_b32_e32 v13, 16, v1
	v_or_b32_e32 v14, 24, v1
	v_or_b32_e32 v15, 32, v1
	v_or_b32_e32 v16, 40, v1
	v_or_b32_e32 v17, 48, v1
	v_or_b32_e32 v18, 56, v1
	s_movk_i32 s81, 0x7fff
	s_mov_b32 s84, 0xffff0000
	s_branch .LBB0_197

.LBB0_197:
	v_add_u32_e32 v2, 0x400, v10
	s_waitcnt vmcnt(62)
	ds_write2_b32 v10, v19, v20 offset1:65
	s_waitcnt vmcnt(60)
	ds_write2_b32 v10, v21, v22 offset0:130 offset1:195
	s_waitcnt vmcnt(58)
	ds_write2_b32 v2, v23, v24 offset0:4 offset1:69
	s_waitcnt vmcnt(56)
	ds_write2_b32 v2, v25, v26 offset0:134 offset1:199
	v_add_u32_e32 v2, 0x800, v10
	s_waitcnt vmcnt(54)
	ds_write2_b32 v2, v27, v28 offset0:8 offset1:73
	s_waitcnt vmcnt(52)
	ds_write2_b32 v2, v29, v30 offset0:138 offset1:203
	v_add_u32_e32 v2, 0xc00, v10
	s_waitcnt vmcnt(50)
	ds_write2_b32 v2, v31, v32 offset0:12 offset1:77
	s_waitcnt vmcnt(48)
	ds_write2_b32 v2, v33, v34 offset0:142 offset1:207
	v_add_u32_e32 v2, 0x1000, v10
	s_waitcnt vmcnt(46)
	ds_write2_b32 v2, v35, v36 offset0:16 offset1:81
	s_waitcnt vmcnt(44)
	ds_write2_b32 v2, v37, v38 offset0:146 offset1:211
	v_add_u32_e32 v2, 0x1400, v10
	s_waitcnt vmcnt(42)
	ds_write2_b32 v2, v39, v40 offset0:20 offset1:85
	s_waitcnt vmcnt(40)
	ds_write2_b32 v2, v41, v42 offset0:150 offset1:215
	v_add_u32_e32 v2, 0x1800, v10
	s_waitcnt vmcnt(38)
	ds_write2_b32 v2, v43, v44 offset0:24 offset1:89
	s_waitcnt vmcnt(36)
	ds_write2_b32 v2, v45, v46 offset0:154 offset1:219
	v_add_u32_e32 v2, 0x1c00, v10
	s_waitcnt vmcnt(34)
	ds_write2_b32 v2, v47, v48 offset0:28 offset1:93
	s_waitcnt vmcnt(32)
	ds_write2_b32 v2, v49, v50 offset0:158 offset1:223
	v_add_u32_e32 v2, 0x2000, v10
	s_waitcnt vmcnt(30)
	ds_write2_b32 v2, v51, v52 offset0:32 offset1:97
	s_waitcnt vmcnt(28)
	ds_write2_b32 v2, v53, v54 offset0:162 offset1:227
	v_add_u32_e32 v2, 0x2400, v10
	s_waitcnt vmcnt(26)
	ds_write2_b32 v2, v55, v56 offset0:36 offset1:101
	s_waitcnt vmcnt(24)
	ds_write2_b32 v2, v57, v58 offset0:166 offset1:231
	v_add_u32_e32 v2, 0x2800, v10
	s_waitcnt vmcnt(22)
	ds_write2_b32 v2, v59, v60 offset0:40 offset1:105
	s_waitcnt vmcnt(20)
	ds_write2_b32 v2, v61, v62 offset0:170 offset1:235
	v_add_u32_e32 v2, 0x2c00, v10
	s_waitcnt vmcnt(18)
	ds_write2_b32 v2, v63, v64 offset0:44 offset1:109
	s_waitcnt vmcnt(16)
	ds_write2_b32 v2, v65, v66 offset0:174 offset1:239
	v_add_u32_e32 v2, 0x3000, v10
	s_waitcnt vmcnt(14)
	ds_write2_b32 v2, v67, v68 offset0:48 offset1:113
	s_waitcnt vmcnt(12)
	ds_write2_b32 v2, v69, v70 offset0:178 offset1:243
	v_add_u32_e32 v2, 0x3400, v10
	s_waitcnt vmcnt(10)
	ds_write2_b32 v2, v71, v72 offset0:52 offset1:117
	s_waitcnt vmcnt(8)
	ds_write2_b32 v2, v73, v74 offset0:182 offset1:247
	v_add_u32_e32 v2, 0x3800, v10
	s_waitcnt vmcnt(6)
	ds_write2_b32 v2, v75, v76 offset0:56 offset1:121
	s_waitcnt vmcnt(4)
	ds_write2_b32 v2, v77, v78 offset0:186 offset1:251
	v_add_u32_e32 v2, 0x3c00, v10
	s_waitcnt vmcnt(2)
	ds_write2_b32 v2, v79, v80 offset0:60 offset1:125
	s_waitcnt vmcnt(0)
	ds_write2_b32 v2, v81, v5 offset0:190 offset1:255
	s_waitcnt lgkmcnt(0)
	s_mov_b32 s13, s85
	s_add_i32 s85, s88, s85
	s_cmpk_gt_i32 s85, 0x1ff
	s_cselect_b64 s[4:5], -1, 0
	s_and_b64 vcc, exec, s[4:5]
	s_cbranch_vccnz .LBB0_196
	s_ashr_i32 s89, s85, 31
	s_lshr_b32 s89, s89, 23
	s_add_i32 s89, s85, s89
	s_and_b32 s89, s89, 0xfe00
	s_sub_i32 s89, s85, s89
	s_sext_i32_i16 s90, s89
	s_bfe_u32 s90, s90, 0x5001a
	s_add_i32 s92, s89, s90
	s_sext_i32_i16 s90, s92
	s_lshl_b32 s90, s90, 1
	s_andn2_b32 s90, s90, 63
	s_ashr_i32 s91, s90, 31
	s_lshl_b64 s[90:91], s[90:91], 13
	s_add_u32 s93, s8, s90
	s_addc_u32 s94, s9, s91
	s_and_b32 s90, s92, 0xffe0
	s_sub_i32 s89, s89, s90
	s_sext_i32_i16 s89, s89
	s_lshl_b32 s90, s89, 6
	s_ashr_i32 s91, s90, 31
	s_lshl_b64 s[90:91], s[90:91], 2
	s_add_u32 s90, s93, s90
	s_addc_u32 s91, s94, s91
	v_lshlrev_b32_e32 v2, 2, v198
	v_lshl_add_u64 v[8:9], s[90:91], 0, v[2:3]
	v_add_co_u32_e32 v20, vcc, s7, v8
	global_load_dword v19, v2, s[90:91] nt
	s_nop 0
	v_addc_co_u32_e32 v21, vcc, 0, v9, vcc
	v_add_co_u32_e32 v22, vcc, s22, v8
	global_load_dword v20, v[20:21], off nt
	s_nop 0
	v_addc_co_u32_e32 v23, vcc, 0, v9, vcc
	global_load_dword v21, v[22:23], off nt
	v_add_co_u32_e32 v22, vcc, s23, v8
	s_nop 1
	v_addc_co_u32_e32 v23, vcc, 0, v9, vcc
	v_add_co_u32_e32 v24, vcc, s24, v8
	global_load_dword v22, v[22:23], off nt
	s_nop 0
	v_addc_co_u32_e32 v25, vcc, 0, v9, vcc
	global_load_dword v23, v[24:25], off nt
	v_add_co_u32_e32 v24, vcc, s25, v8
	s_nop 1
	v_addc_co_u32_e32 v25, vcc, 0, v9, vcc
	v_add_co_u32_e32 v26, vcc, s26, v8
	global_load_dword v24, v[24:25], off nt
	s_nop 0
	v_addc_co_u32_e32 v27, vcc, 0, v9, vcc
	global_load_dword v25, v[26:27], off nt
	v_add_co_u32_e32 v26, vcc, s27, v8
	s_nop 1
	v_addc_co_u32_e32 v27, vcc, 0, v9, vcc
	v_add_co_u32_e32 v28, vcc, s28, v8
	global_load_dword v26, v[26:27], off nt
	s_nop 0
	v_addc_co_u32_e32 v29, vcc, 0, v9, vcc
	global_load_dword v27, v[28:29], off nt
	v_add_co_u32_e32 v28, vcc, s29, v8
	s_nop 1
	v_addc_co_u32_e32 v29, vcc, 0, v9, vcc
	v_add_co_u32_e32 v30, vcc, s30, v8
	global_load_dword v28, v[28:29], off nt
	s_nop 0
	v_addc_co_u32_e32 v31, vcc, 0, v9, vcc
	global_load_dword v29, v[30:31], off nt
	v_add_co_u32_e32 v30, vcc, s31, v8
	s_nop 1
	v_addc_co_u32_e32 v31, vcc, 0, v9, vcc
	v_add_co_u32_e32 v32, vcc, s33, v8
	global_load_dword v30, v[30:31], off nt
	s_nop 0
	v_addc_co_u32_e32 v33, vcc, 0, v9, vcc
	global_load_dword v31, v[32:33], off nt
	v_add_co_u32_e32 v32, vcc, s34, v8
	s_nop 1
	v_addc_co_u32_e32 v33, vcc, 0, v9, vcc
	v_add_co_u32_e32 v34, vcc, s35, v8
	global_load_dword v32, v[32:33], off nt
	s_nop 0
	v_addc_co_u32_e32 v35, vcc, 0, v9, vcc
	global_load_dword v33, v[34:35], off nt
	v_add_co_u32_e32 v34, vcc, s36, v8
	s_nop 1
	v_addc_co_u32_e32 v35, vcc, 0, v9, vcc
	v_add_co_u32_e32 v36, vcc, s37, v8
	global_load_dword v34, v[34:35], off nt
	s_nop 0
	v_addc_co_u32_e32 v37, vcc, 0, v9, vcc
	global_load_dword v35, v[36:37], off nt
	v_add_co_u32_e32 v36, vcc, s38, v8
	s_nop 1
	v_addc_co_u32_e32 v37, vcc, 0, v9, vcc
	v_add_co_u32_e32 v38, vcc, s39, v8
	global_load_dword v36, v[36:37], off nt
	s_nop 0
	v_addc_co_u32_e32 v39, vcc, 0, v9, vcc
	global_load_dword v37, v[38:39], off nt
	v_add_co_u32_e32 v38, vcc, s40, v8
	s_nop 1
	v_addc_co_u32_e32 v39, vcc, 0, v9, vcc
	v_add_co_u32_e32 v40, vcc, s41, v8
	global_load_dword v38, v[38:39], off nt
	s_nop 0
	v_addc_co_u32_e32 v41, vcc, 0, v9, vcc
	global_load_dword v39, v[40:41], off nt
	v_add_co_u32_e32 v40, vcc, s42, v8
	s_nop 1
	v_addc_co_u32_e32 v41, vcc, 0, v9, vcc
	v_add_co_u32_e32 v42, vcc, s43, v8
	global_load_dword v40, v[40:41], off nt
	s_nop 0
	v_addc_co_u32_e32 v43, vcc, 0, v9, vcc
	global_load_dword v41, v[42:43], off nt
	v_add_co_u32_e32 v42, vcc, s44, v8
	s_nop 1
	v_addc_co_u32_e32 v43, vcc, 0, v9, vcc
	v_add_co_u32_e32 v44, vcc, s45, v8
	global_load_dword v42, v[42:43], off nt
	s_nop 0
	v_addc_co_u32_e32 v45, vcc, 0, v9, vcc
	global_load_dword v43, v[44:45], off nt
	v_add_co_u32_e32 v44, vcc, s46, v8
	s_nop 1
	v_addc_co_u32_e32 v45, vcc, 0, v9, vcc
	v_add_co_u32_e32 v46, vcc, s47, v8
	global_load_dword v44, v[44:45], off nt
	s_nop 0
	v_addc_co_u32_e32 v47, vcc, 0, v9, vcc
	global_load_dword v45, v[46:47], off nt
	v_add_co_u32_e32 v46, vcc, s48, v8
	s_nop 1
	v_addc_co_u32_e32 v47, vcc, 0, v9, vcc
	v_add_co_u32_e32 v48, vcc, s49, v8
	global_load_dword v46, v[46:47], off nt
	s_nop 0
	v_addc_co_u32_e32 v49, vcc, 0, v9, vcc
	global_load_dword v47, v[48:49], off nt
	v_add_co_u32_e32 v48, vcc, s50, v8
	s_nop 1
	v_addc_co_u32_e32 v49, vcc, 0, v9, vcc
	v_add_co_u32_e32 v50, vcc, s51, v8
	global_load_dword v48, v[48:49], off nt
	s_nop 0
	v_addc_co_u32_e32 v51, vcc, 0, v9, vcc
	global_load_dword v49, v[50:51], off nt
	v_add_co_u32_e32 v50, vcc, s52, v8
	s_nop 1
	v_addc_co_u32_e32 v51, vcc, 0, v9, vcc
	v_add_co_u32_e32 v52, vcc, s53, v8
	global_load_dword v50, v[50:51], off nt
	s_nop 0
	v_addc_co_u32_e32 v53, vcc, 0, v9, vcc
	global_load_dword v51, v[52:53], off nt
	v_add_co_u32_e32 v52, vcc, s54, v8
	s_nop 1
	v_addc_co_u32_e32 v53, vcc, 0, v9, vcc
	v_add_co_u32_e32 v54, vcc, s55, v8
	global_load_dword v52, v[52:53], off nt
	s_nop 0
	v_addc_co_u32_e32 v55, vcc, 0, v9, vcc
	global_load_dword v53, v[54:55], off nt
	v_add_co_u32_e32 v54, vcc, s56, v8
	s_nop 1
	v_addc_co_u32_e32 v55, vcc, 0, v9, vcc
	v_add_co_u32_e32 v56, vcc, s57, v8
	global_load_dword v54, v[54:55], off nt
	s_nop 0
	v_addc_co_u32_e32 v57, vcc, 0, v9, vcc
	global_load_dword v55, v[56:57], off nt
	v_add_co_u32_e32 v56, vcc, s58, v8
	s_nop 1
	v_addc_co_u32_e32 v57, vcc, 0, v9, vcc
	v_add_co_u32_e32 v58, vcc, s59, v8
	global_load_dword v56, v[56:57], off nt
	s_nop 0
	v_addc_co_u32_e32 v59, vcc, 0, v9, vcc
	global_load_dword v57, v[58:59], off nt
	v_add_co_u32_e32 v58, vcc, s60, v8
	s_nop 1
	v_addc_co_u32_e32 v59, vcc, 0, v9, vcc
	v_add_co_u32_e32 v60, vcc, s61, v8
	global_load_dword v58, v[58:59], off nt
	s_nop 0
	v_addc_co_u32_e32 v61, vcc, 0, v9, vcc
	global_load_dword v59, v[60:61], off nt
	v_add_co_u32_e32 v60, vcc, s62, v8
	s_nop 1
	v_addc_co_u32_e32 v61, vcc, 0, v9, vcc
	v_add_co_u32_e32 v62, vcc, s63, v8
	global_load_dword v60, v[60:61], off nt
	s_nop 0
	v_addc_co_u32_e32 v63, vcc, 0, v9, vcc
	global_load_dword v61, v[62:63], off nt
	v_add_co_u32_e32 v62, vcc, s64, v8
	s_nop 1
	v_addc_co_u32_e32 v63, vcc, 0, v9, vcc
	v_add_co_u32_e32 v64, vcc, s65, v8
	global_load_dword v62, v[62:63], off nt
	s_nop 0
	v_addc_co_u32_e32 v65, vcc, 0, v9, vcc
	global_load_dword v63, v[64:65], off nt
	v_add_co_u32_e32 v64, vcc, s66, v8
	s_nop 1
	v_addc_co_u32_e32 v65, vcc, 0, v9, vcc
	v_add_co_u32_e32 v66, vcc, s67, v8
	global_load_dword v64, v[64:65], off nt
	s_nop 0
	v_addc_co_u32_e32 v67, vcc, 0, v9, vcc
	global_load_dword v65, v[66:67], off nt
	v_add_co_u32_e32 v66, vcc, s68, v8
	s_nop 1
	v_addc_co_u32_e32 v67, vcc, 0, v9, vcc
	v_add_co_u32_e32 v68, vcc, s69, v8
	global_load_dword v66, v[66:67], off nt
	s_nop 0
	v_addc_co_u32_e32 v69, vcc, 0, v9, vcc
	global_load_dword v67, v[68:69], off nt
	v_add_co_u32_e32 v68, vcc, s70, v8
	s_nop 1
	v_addc_co_u32_e32 v69, vcc, 0, v9, vcc
	v_add_co_u32_e32 v70, vcc, s71, v8
	global_load_dword v68, v[68:69], off nt
	s_nop 0
	v_addc_co_u32_e32 v71, vcc, 0, v9, vcc
	global_load_dword v69, v[70:71], off nt
	v_add_co_u32_e32 v70, vcc, s72, v8
	s_nop 1
	v_addc_co_u32_e32 v71, vcc, 0, v9, vcc
	v_add_co_u32_e32 v72, vcc, s73, v8
	global_load_dword v70, v[70:71], off nt
	s_nop 0
	v_addc_co_u32_e32 v73, vcc, 0, v9, vcc
	global_load_dword v71, v[72:73], off nt
	v_add_co_u32_e32 v72, vcc, s74, v8
	s_nop 1
	v_addc_co_u32_e32 v73, vcc, 0, v9, vcc
	v_add_co_u32_e32 v74, vcc, s75, v8
	global_load_dword v72, v[72:73], off nt
	s_nop 0
	v_addc_co_u32_e32 v75, vcc, 0, v9, vcc
	global_load_dword v73, v[74:75], off nt
	v_add_co_u32_e32 v74, vcc, s76, v8
	s_nop 1
	v_addc_co_u32_e32 v75, vcc, 0, v9, vcc
	v_add_co_u32_e32 v76, vcc, s77, v8
	global_load_dword v74, v[74:75], off nt
	s_nop 0
	v_addc_co_u32_e32 v77, vcc, 0, v9, vcc
	global_load_dword v75, v[76:77], off nt
	v_add_co_u32_e32 v76, vcc, s78, v8
	s_nop 1
	v_addc_co_u32_e32 v77, vcc, 0, v9, vcc
	v_add_co_u32_e32 v78, vcc, s79, v8
	global_load_dword v76, v[76:77], off nt
	s_nop 0
	v_addc_co_u32_e32 v79, vcc, 0, v9, vcc
	global_load_dword v77, v[78:79], off nt
	v_add_co_u32_e32 v78, vcc, s80, v8
	s_nop 1
	v_addc_co_u32_e32 v79, vcc, 0, v9, vcc
	v_add_co_u32_e32 v80, vcc, 0x78000, v8
	global_load_dword v78, v[78:79], off nt
	s_nop 0
	v_addc_co_u32_e32 v81, vcc, 0, v9, vcc
	global_load_dword v79, v[80:81], off nt
	v_add_co_u32_e32 v80, vcc, 0x7a000, v8
	s_nop 1
	v_addc_co_u32_e32 v81, vcc, 0, v9, vcc
	v_add_co_u32_e32 v82, vcc, 0x7c000, v8
	global_load_dword v80, v[80:81], off nt
	s_nop 0
	v_addc_co_u32_e32 v83, vcc, 0, v9, vcc
	v_add_co_u32_e32 v8, vcc, 0x7e000, v8
	s_nop 1
	v_addc_co_u32_e32 v9, vcc, 0, v9, vcc
	global_load_dword v5, v[8:9], off nt
	global_load_dword v81, v[82:83], off nt
	s_branch .LBB0_196

.LBB0_200:
	s_ashr_i32 s0, s88, 31
	s_lshr_b32 s0, s0, 22
	s_add_i32 s0, s88, s0
	s_and_b32 s0, s0, 0xfc00
	s_sub_i32 s2, s88, s0
	s_sext_i32_i16 s0, s2
	s_bfe_u32 s0, s0, 0x5001a
	s_add_i32 s3, s2, s0
	s_sext_i32_i16 s0, s3
	s_lshl_b32 s0, s0, 1
	s_andn2_b32 s0, s0, 63
	s_ashr_i32 s1, s0, 31
	s_lshl_b64 s[0:1], s[0:1], 13
	s_waitcnt lgkmcnt(0)
	s_add_u32 s4, s20, s0
	s_addc_u32 s5, s21, s1
	s_and_b32 s0, s3, 0xffe0
	s_sub_i32 s0, s2, s0
	s_sext_i32_i16 s0, s0
	s_lshl_b32 s0, s0, 6
	s_ashr_i32 s1, s0, 31
	s_lshl_b64 s[0:1], s[0:1], 2
	s_add_u32 s0, s4, s0
	s_addc_u32 s1, s5, s1
	v_mov_b32_e32 v3, 0
	v_lshlrev_b32_e32 v2, 2, v198
	v_lshl_add_u64 v[4:5], s[0:1], 0, v[2:3]
	s_movk_i32 s2, 0x2000
	v_add_co_u32_e32 v6, vcc, s2, v4
	s_movk_i32 s3, 0x4000
	s_nop 0
	v_addc_co_u32_e32 v7, vcc, 0, v5, vcc
	s_waitcnt vmcnt(62)
	v_add_co_u32_e32 v16, vcc, s3, v4
	s_movk_i32 s4, 0x6000
	s_waitcnt vmcnt(61)
	v_addc_co_u32_e32 v17, vcc, 0, v5, vcc
	s_waitcnt vmcnt(60)
	v_add_co_u32_e32 v18, vcc, s4, v4
	s_mov_b32 s5, 0x8000
	s_waitcnt vmcnt(59)
	v_addc_co_u32_e32 v19, vcc, 0, v5, vcc
	s_waitcnt vmcnt(58)
	v_add_co_u32_e32 v20, vcc, s5, v4
	s_mov_b32 s7, 0xa000
	s_waitcnt vmcnt(57)
	v_addc_co_u32_e32 v21, vcc, 0, v5, vcc
	s_waitcnt vmcnt(56)
	v_add_co_u32_e32 v22, vcc, s7, v4
	s_mov_b32 s8, 0xc000
	s_waitcnt vmcnt(55)
	v_addc_co_u32_e32 v23, vcc, 0, v5, vcc
	s_waitcnt vmcnt(54)
	v_add_co_u32_e32 v24, vcc, s8, v4
	s_mov_b32 s9, 0xe000
	s_waitcnt vmcnt(53)
	v_addc_co_u32_e32 v25, vcc, 0, v5, vcc
	s_waitcnt vmcnt(52)
	v_add_co_u32_e32 v26, vcc, s9, v4
	s_mov_b32 s10, 0x10000
	s_waitcnt vmcnt(51)
	v_addc_co_u32_e32 v27, vcc, 0, v5, vcc
	s_waitcnt vmcnt(50)
	v_add_co_u32_e32 v28, vcc, s10, v4
	s_mov_b32 s11, 0x12000
	s_waitcnt vmcnt(49)
	v_addc_co_u32_e32 v29, vcc, 0, v5, vcc
	global_load_dword v8, v[6:7], off nt
	global_load_dword v9, v[16:17], off nt
	global_load_dword v10, v[18:19], off nt
	global_load_dword v11, v[20:21], off nt
	global_load_dword v12, v[22:23], off nt
	global_load_dword v13, v[24:25], off nt
	global_load_dword v14, v[26:27], off nt
	global_load_dword v15, v[28:29], off nt
	v_add_co_u32_e32 v6, vcc, s11, v4
	s_mov_b32 s22, 0x14000
	s_nop 0
	v_addc_co_u32_e32 v7, vcc, 0, v5, vcc
	v_add_co_u32_e32 v18, vcc, s22, v4
	s_mov_b32 s23, 0x16000
	s_nop 0
	v_addc_co_u32_e32 v19, vcc, 0, v5, vcc
	v_add_co_u32_e32 v20, vcc, s23, v4
	s_mov_b32 s24, 0x18000
	s_nop 0
	v_addc_co_u32_e32 v21, vcc, 0, v5, vcc
	v_add_co_u32_e32 v22, vcc, s24, v4
	s_mov_b32 s25, 0x1a000
	s_nop 0
	v_addc_co_u32_e32 v23, vcc, 0, v5, vcc
	v_add_co_u32_e32 v24, vcc, s25, v4
	s_mov_b32 s26, 0x1c000
	s_nop 0
	v_addc_co_u32_e32 v25, vcc, 0, v5, vcc
	v_add_co_u32_e32 v26, vcc, s26, v4
	s_mov_b32 s27, 0x1e000
	s_nop 0
	v_addc_co_u32_e32 v27, vcc, 0, v5, vcc
	v_add_co_u32_e32 v28, vcc, s27, v4
	s_mov_b32 s28, 0x20000
	s_nop 0
	v_addc_co_u32_e32 v29, vcc, 0, v5, vcc
	s_waitcnt vmcnt(56)
	v_add_co_u32_e32 v30, vcc, s28, v4
	s_mov_b32 s29, 0x22000
	s_waitcnt vmcnt(55)
	v_addc_co_u32_e32 v31, vcc, 0, v5, vcc
	global_load_dword v16, v[6:7], off nt
	global_load_dword v17, v[18:19], off nt
	s_nop 0
	global_load_dword v18, v[20:21], off nt
	global_load_dword v19, v[22:23], off nt
	s_nop 0
	global_load_dword v20, v[24:25], off nt
	global_load_dword v21, v[26:27], off nt
	global_load_dword v22, v[28:29], off nt
	global_load_dword v23, v[30:31], off nt
	v_add_co_u32_e32 v6, vcc, s29, v4
	s_mov_b32 s30, 0x24000
	s_nop 0
	v_addc_co_u32_e32 v7, vcc, 0, v5, vcc
	v_add_co_u32_e32 v26, vcc, s30, v4
	s_mov_b32 s31, 0x26000
	s_nop 0
	v_addc_co_u32_e32 v27, vcc, 0, v5, vcc
	v_add_co_u32_e32 v28, vcc, s31, v4
	s_mov_b32 s33, 0x28000
	s_nop 0
	v_addc_co_u32_e32 v29, vcc, 0, v5, vcc
	v_add_co_u32_e32 v30, vcc, s33, v4
	s_mov_b32 s34, 0x2a000
	s_nop 0
	v_addc_co_u32_e32 v31, vcc, 0, v5, vcc
	s_waitcnt vmcnt(62)
	v_add_co_u32_e32 v32, vcc, s34, v4
	s_mov_b32 s35, 0x2c000
	s_waitcnt vmcnt(61)
	v_addc_co_u32_e32 v33, vcc, 0, v5, vcc
	s_waitcnt vmcnt(60)
	v_add_co_u32_e32 v34, vcc, s35, v4
	s_mov_b32 s36, 0x2e000
	s_waitcnt vmcnt(59)
	v_addc_co_u32_e32 v35, vcc, 0, v5, vcc
	s_waitcnt vmcnt(58)
	v_add_co_u32_e32 v36, vcc, s36, v4
	s_mov_b32 s37, 0x30000
	s_waitcnt vmcnt(57)
	v_addc_co_u32_e32 v37, vcc, 0, v5, vcc
	s_waitcnt vmcnt(56)
	v_add_co_u32_e32 v38, vcc, s37, v4
	s_mov_b32 s38, 0x32000
	s_nop 0
	v_addc_co_u32_e32 v39, vcc, 0, v5, vcc
	global_load_dword v24, v[6:7], off nt
	global_load_dword v25, v[26:27], off nt
	s_nop 0
	global_load_dword v26, v[28:29], off nt
	global_load_dword v27, v[30:31], off nt
	s_nop 0
	global_load_dword v28, v[32:33], off nt
	global_load_dword v29, v[34:35], off nt
	global_load_dword v30, v[36:37], off nt
	global_load_dword v31, v[38:39], off nt
	v_add_co_u32_e32 v6, vcc, s38, v4
	s_mov_b32 s39, 0x34000
	s_nop 0
	v_addc_co_u32_e32 v7, vcc, 0, v5, vcc
	v_add_co_u32_e32 v32, vcc, s39, v4
	s_mov_b32 s40, 0x36000
	s_nop 0
	v_addc_co_u32_e32 v33, vcc, 0, v5, vcc
	v_add_co_u32_e32 v34, vcc, s40, v4
	s_mov_b32 s41, 0x38000
	s_nop 0
	v_addc_co_u32_e32 v35, vcc, 0, v5, vcc
	v_add_co_u32_e32 v36, vcc, s41, v4
	s_mov_b32 s42, 0x3a000
	s_nop 0
	v_addc_co_u32_e32 v37, vcc, 0, v5, vcc
	v_add_co_u32_e32 v38, vcc, s42, v4
	s_mov_b32 s43, 0x3c000
	s_nop 0
	v_addc_co_u32_e32 v39, vcc, 0, v5, vcc
	s_waitcnt vmcnt(62)
	v_add_co_u32_e32 v48, vcc, s43, v4
	s_mov_b32 s44, 0x3e000
	s_nop 0
	v_addc_co_u32_e32 v49, vcc, 0, v5, vcc
	v_add_co_u32_e32 v50, vcc, s44, v4
	s_mov_b32 s45, 0x40000
	s_waitcnt vmcnt(61)
	v_addc_co_u32_e32 v51, vcc, 0, v5, vcc
	s_waitcnt vmcnt(60)
	v_add_co_u32_e32 v52, vcc, s45, v4
	s_mov_b32 s46, 0x42000
	s_waitcnt vmcnt(59)
	v_addc_co_u32_e32 v53, vcc, 0, v5, vcc
	global_load_dword v41, v[6:7], off nt
	global_load_dword v43, v[32:33], off nt
	global_load_dword v44, v[34:35], off nt
	global_load_dword v45, v[36:37], off nt
	global_load_dword v46, v[38:39], off nt
	global_load_dword v47, v[48:49], off nt
	s_nop 0
	global_load_dword v48, v[50:51], off nt
	global_load_dword v49, v[52:53], off nt
	v_add_co_u32_e32 v6, vcc, s46, v4
	s_mov_b32 s47, 0x44000
	s_nop 0
	v_addc_co_u32_e32 v7, vcc, 0, v5, vcc
	v_add_co_u32_e32 v32, vcc, s47, v4
	s_mov_b32 s48, 0x46000
	s_nop 0
	v_addc_co_u32_e32 v33, vcc, 0, v5, vcc
	v_add_co_u32_e32 v34, vcc, s48, v4
	s_mov_b32 s49, 0x48000
	s_nop 0
	v_addc_co_u32_e32 v35, vcc, 0, v5, vcc
	v_add_co_u32_e32 v36, vcc, s49, v4
	s_mov_b32 s50, 0x4a000
	s_nop 0
	v_addc_co_u32_e32 v37, vcc, 0, v5, vcc
	v_add_co_u32_e32 v38, vcc, s50, v4
	s_mov_b32 s51, 0x4c000
	s_nop 0
	v_addc_co_u32_e32 v39, vcc, 0, v5, vcc
	s_waitcnt vmcnt(62)
	v_add_co_u32_e32 v56, vcc, s51, v4
	s_mov_b32 s52, 0x4e000
	s_nop 0
	v_addc_co_u32_e32 v57, vcc, 0, v5, vcc
	v_add_co_u32_e32 v58, vcc, s52, v4
	s_mov_b32 s53, 0x50000
	s_waitcnt vmcnt(61)
	v_addc_co_u32_e32 v59, vcc, 0, v5, vcc
	s_waitcnt vmcnt(60)
	v_add_co_u32_e32 v60, vcc, s53, v4
	s_mov_b32 s54, 0x52000
	s_waitcnt vmcnt(59)
	v_addc_co_u32_e32 v61, vcc, 0, v5, vcc
	global_load_dword v50, v[6:7], off nt
	global_load_dword v51, v[32:33], off nt
	global_load_dword v52, v[34:35], off nt
	global_load_dword v53, v[36:37], off nt
	global_load_dword v54, v[38:39], off nt
	global_load_dword v55, v[56:57], off nt
	s_nop 0
	global_load_dword v56, v[58:59], off nt
	global_load_dword v57, v[60:61], off nt
	v_add_co_u32_e32 v6, vcc, s54, v4
	s_mov_b32 s55, 0x54000
	s_nop 0
	v_addc_co_u32_e32 v7, vcc, 0, v5, vcc
	v_add_co_u32_e32 v32, vcc, s55, v4
	s_mov_b32 s56, 0x56000
	s_nop 0
	v_addc_co_u32_e32 v33, vcc, 0, v5, vcc
	v_add_co_u32_e32 v34, vcc, s56, v4
	s_mov_b32 s57, 0x58000
	s_nop 0
	v_addc_co_u32_e32 v35, vcc, 0, v5, vcc
	v_add_co_u32_e32 v36, vcc, s57, v4
	s_mov_b32 s58, 0x5a000
	s_nop 0
	v_addc_co_u32_e32 v37, vcc, 0, v5, vcc
	v_add_co_u32_e32 v38, vcc, s58, v4
	s_mov_b32 s59, 0x5c000
	s_nop 0
	v_addc_co_u32_e32 v39, vcc, 0, v5, vcc
	s_waitcnt vmcnt(62)
	v_add_co_u32_e32 v64, vcc, s59, v4
	s_mov_b32 s60, 0x5e000
	s_nop 0
	v_addc_co_u32_e32 v65, vcc, 0, v5, vcc
	v_add_co_u32_e32 v66, vcc, s60, v4
	s_mov_b32 s61, 0x60000
	s_waitcnt vmcnt(61)
	v_addc_co_u32_e32 v67, vcc, 0, v5, vcc
	s_waitcnt vmcnt(60)
	v_add_co_u32_e32 v68, vcc, s61, v4
	s_mov_b32 s62, 0x62000
	s_waitcnt vmcnt(59)
	v_addc_co_u32_e32 v69, vcc, 0, v5, vcc
	global_load_dword v58, v[6:7], off nt
	global_load_dword v59, v[32:33], off nt
	global_load_dword v60, v[34:35], off nt
	global_load_dword v61, v[36:37], off nt
	global_load_dword v62, v[38:39], off nt
	global_load_dword v63, v[64:65], off nt
	s_nop 0
	global_load_dword v64, v[66:67], off nt
	global_load_dword v65, v[68:69], off nt
	v_add_co_u32_e32 v6, vcc, s62, v4
	s_mov_b32 s63, 0x64000
	s_nop 0
	v_addc_co_u32_e32 v7, vcc, 0, v5, vcc
	v_add_co_u32_e32 v32, vcc, s63, v4
	s_mov_b32 s64, 0x66000
	s_nop 0
	v_addc_co_u32_e32 v33, vcc, 0, v5, vcc
	v_add_co_u32_e32 v34, vcc, s64, v4
	s_mov_b32 s65, 0x68000
	s_nop 0
	v_addc_co_u32_e32 v35, vcc, 0, v5, vcc
	v_add_co_u32_e32 v36, vcc, s65, v4
	s_mov_b32 s66, 0x6a000
	s_nop 0
	v_addc_co_u32_e32 v37, vcc, 0, v5, vcc
	v_add_co_u32_e32 v38, vcc, s66, v4
	s_mov_b32 s67, 0x6c000
	s_nop 0
	v_addc_co_u32_e32 v39, vcc, 0, v5, vcc
	s_waitcnt vmcnt(62)
	v_add_co_u32_e32 v72, vcc, s67, v4
	s_mov_b32 s68, 0x6e000
	s_waitcnt vmcnt(60)
	v_addc_co_u32_e32 v73, vcc, 0, v5, vcc
	s_waitcnt vmcnt(59)
	v_add_co_u32_e32 v74, vcc, s68, v4
	s_mov_b32 s69, 0x70000
	s_waitcnt vmcnt(58)
	v_addc_co_u32_e32 v75, vcc, 0, v5, vcc
	v_add_co_u32_e32 v76, vcc, s69, v4
	s_mov_b32 s70, 0x72000
	s_waitcnt vmcnt(57)
	v_addc_co_u32_e32 v77, vcc, 0, v5, vcc
	global_load_dword v66, v[6:7], off nt
	global_load_dword v67, v[32:33], off nt
	global_load_dword v68, v[34:35], off nt
	global_load_dword v69, v[36:37], off nt
	global_load_dword v70, v[38:39], off nt
	global_load_dword v71, v[72:73], off nt
	s_nop 0
	global_load_dword v72, v[74:75], off nt
	global_load_dword v73, v[76:77], off nt
	v_add_co_u32_e32 v6, vcc, s70, v4
	s_mov_b32 s71, 0x74000
	s_nop 0
	v_addc_co_u32_e32 v7, vcc, 0, v5, vcc
	v_add_co_u32_e32 v32, vcc, s71, v4
	s_mov_b32 s72, 0x76000
	s_nop 0
	v_addc_co_u32_e32 v33, vcc, 0, v5, vcc
	v_add_co_u32_e32 v34, vcc, s72, v4
	s_mov_b32 s73, 0x78000
	s_nop 0
	v_addc_co_u32_e32 v35, vcc, 0, v5, vcc
	v_add_co_u32_e32 v36, vcc, s73, v4
	s_mov_b32 s73, 0x7a000
	s_nop 0
	v_addc_co_u32_e32 v37, vcc, 0, v5, vcc
	v_add_co_u32_e32 v38, vcc, s73, v4
	s_mov_b32 s73, 0x7c000
	s_nop 0
	v_addc_co_u32_e32 v39, vcc, 0, v5, vcc
	s_waitcnt vmcnt(62)
	v_add_co_u32_e32 v80, vcc, s73, v4
	s_mov_b32 s73, 0x7e000
	s_nop 0
	v_addc_co_u32_e32 v81, vcc, 0, v5, vcc
	v_add_co_u32_e32 v4, vcc, s73, v4
	s_mov_b32 s76, s88
	s_nop 0
	v_addc_co_u32_e32 v5, vcc, 0, v5, vcc
	global_load_dword v42, v2, s[0:1] nt
	global_load_dword v74, v[6:7], off nt
	global_load_dword v75, v[32:33], off nt
	global_load_dword v76, v[34:35], off nt
	global_load_dword v77, v[36:37], off nt
	global_load_dword v78, v[38:39], off nt
	global_load_dword v79, v[80:81], off nt
	s_nop 0
	global_load_dword v80, v[4:5], off nt
	v_add_u32_e32 v32, s6, v2
	v_lshlrev_b32_e32 v2, 3, v0
	v_and_b32_e32 v2, 56, v2
	v_mul_u32_u24_e32 v6, 0x104, v2
	v_lshlrev_b32_e32 v2, 1, v2
	v_lshl_add_u64 v[4:5], s[82:83], 0, v[2:3]
	s_mov_b64 s[0:1], 0x2f00000
	v_lshlrev_b32_e32 v2, 2, v1
	v_lshl_add_u64 v[4:5], v[4:5], 0, s[0:1]
	v_add3_u32 v33, s6, v6, v2
	v_or_b32_e32 v34, 8, v1
	v_or_b32_e32 v35, 16, v1
	v_or_b32_e32 v36, 24, v1
	v_or_b32_e32 v37, 32, v1
	v_or_b32_e32 v38, 40, v1
	v_or_b32_e32 v39, 48, v1
	v_or_b32_e32 v40, 56, v1
	v_lshlrev_b32_e32 v2, 2, v198
	s_movk_i32 s73, 0x7fff
	s_mov_b32 s74, 0xffff0000
	s_branch .LBB0_202

.LBB0_202:
	v_add_u32_e32 v6, 0x400, v32
	s_waitcnt vmcnt(7)
	ds_write2_b32 v32, v42, v8 offset1:65
	ds_write2_b32 v32, v9, v10 offset0:130 offset1:195
	ds_write2_b32 v6, v11, v12 offset0:4 offset1:69
	ds_write2_b32 v6, v13, v14 offset0:134 offset1:199
	v_add_u32_e32 v6, 0x800, v32
	ds_write2_b32 v6, v15, v16 offset0:8 offset1:73
	ds_write2_b32 v6, v17, v18 offset0:138 offset1:203
	v_add_u32_e32 v6, 0xc00, v32
	ds_write2_b32 v6, v19, v20 offset0:12 offset1:77
	ds_write2_b32 v6, v21, v22 offset0:142 offset1:207
	v_add_u32_e32 v6, 0x1000, v32
	ds_write2_b32 v6, v23, v24 offset0:16 offset1:81
	ds_write2_b32 v6, v25, v26 offset0:146 offset1:211
	v_add_u32_e32 v6, 0x1400, v32
	ds_write2_b32 v6, v27, v28 offset0:20 offset1:85
	ds_write2_b32 v6, v29, v30 offset0:150 offset1:215
	v_add_u32_e32 v6, 0x1800, v32
	ds_write2_b32 v6, v31, v41 offset0:24 offset1:89
	ds_write2_b32 v6, v43, v44 offset0:154 offset1:219
	v_add_u32_e32 v6, 0x1c00, v32
	ds_write2_b32 v6, v45, v46 offset0:28 offset1:93
	ds_write2_b32 v6, v47, v48 offset0:158 offset1:223
	v_add_u32_e32 v6, 0x2000, v32
	ds_write2_b32 v6, v49, v50 offset0:32 offset1:97
	ds_write2_b32 v6, v51, v52 offset0:162 offset1:227
	v_add_u32_e32 v6, 0x2400, v32
	ds_write2_b32 v6, v53, v54 offset0:36 offset1:101
	ds_write2_b32 v6, v55, v56 offset0:166 offset1:231
	v_add_u32_e32 v6, 0x2800, v32
	ds_write2_b32 v6, v57, v58 offset0:40 offset1:105
	ds_write2_b32 v6, v59, v60 offset0:170 offset1:235
	v_add_u32_e32 v6, 0x2c00, v32
	ds_write2_b32 v6, v61, v62 offset0:44 offset1:109
	ds_write2_b32 v6, v63, v64 offset0:174 offset1:239
	v_add_u32_e32 v6, 0x3000, v32
	ds_write2_b32 v6, v65, v66 offset0:48 offset1:113
	ds_write2_b32 v6, v67, v68 offset0:178 offset1:243
	v_add_u32_e32 v6, 0x3400, v32
	ds_write2_b32 v6, v69, v70 offset0:52 offset1:117
	ds_write2_b32 v6, v71, v72 offset0:182 offset1:247
	v_add_u32_e32 v6, 0x3800, v32
	s_waitcnt vmcnt(6)
	ds_write2_b32 v6, v73, v74 offset0:56 offset1:121
	s_waitcnt vmcnt(4)
	ds_write2_b32 v6, v75, v76 offset0:186 offset1:251
	v_add_u32_e32 v6, 0x3c00, v32
	s_waitcnt vmcnt(2)
	ds_write2_b32 v6, v77, v78 offset0:60 offset1:125
	s_waitcnt vmcnt(0)
	ds_write2_b32 v6, v79, v80 offset0:190 offset1:255
	s_waitcnt lgkmcnt(0)
	s_add_i32 s75, s76, s85
	s_cmpk_gt_i32 s75, 0x3ff
	s_cselect_b64 s[0:1], -1, 0
	s_and_b64 vcc, exec, s[0:1]
	s_cbranch_vccnz .LBB0_201
	s_ashr_i32 s77, s75, 31
	s_lshr_b32 s77, s77, 22
	s_add_i32 s77, s75, s77
	s_and_b32 s77, s77, 0xfc00
	s_sub_i32 s77, s75, s77
	s_sext_i32_i16 s78, s77
	s_bfe_u32 s78, s78, 0x5001a
	s_add_i32 s80, s77, s78
	s_sext_i32_i16 s78, s80
	s_lshl_b32 s78, s78, 1
	s_andn2_b32 s78, s78, 63
	s_ashr_i32 s79, s78, 31
	s_lshl_b64 s[78:79], s[78:79], 13
	s_add_u32 s81, s20, s78
	s_addc_u32 s84, s21, s79
	s_and_b32 s78, s80, 0xffe0
	s_sub_i32 s77, s77, s78
	s_sext_i32_i16 s77, s77
	s_lshl_b32 s78, s77, 6
	s_ashr_i32 s79, s78, 31
	s_lshl_b64 s[78:79], s[78:79], 2
	s_add_u32 s78, s81, s78
	s_addc_u32 s79, s84, s79
	v_lshl_add_u64 v[6:7], s[78:79], 0, v[2:3]
	v_add_co_u32_e32 v8, vcc, s2, v6
	global_load_dword v42, v2, s[78:79] nt
	s_nop 0
	v_addc_co_u32_e32 v9, vcc, 0, v7, vcc
	v_add_co_u32_e32 v10, vcc, s3, v6
	global_load_dword v8, v[8:9], off nt
	s_nop 0
	v_addc_co_u32_e32 v11, vcc, 0, v7, vcc
	global_load_dword v9, v[10:11], off nt
	v_add_co_u32_e32 v10, vcc, s4, v6
	s_mov_b32 s80, s96
	s_nop 0
	v_addc_co_u32_e32 v11, vcc, 0, v7, vcc
	v_add_co_u32_e32 v12, vcc, s5, v6
	global_load_dword v10, v[10:11], off nt
	s_nop 0
	v_addc_co_u32_e32 v13, vcc, 0, v7, vcc
	global_load_dword v11, v[12:13], off nt
	v_add_co_u32_e32 v12, vcc, s7, v6
	s_nop 1
	v_addc_co_u32_e32 v13, vcc, 0, v7, vcc
	v_add_co_u32_e32 v14, vcc, s8, v6
	global_load_dword v12, v[12:13], off nt
	s_nop 0
	v_addc_co_u32_e32 v15, vcc, 0, v7, vcc
	global_load_dword v13, v[14:15], off nt
	v_add_co_u32_e32 v14, vcc, s9, v6
	s_nop 1
	v_addc_co_u32_e32 v15, vcc, 0, v7, vcc
	v_add_co_u32_e32 v16, vcc, s10, v6
	global_load_dword v14, v[14:15], off nt
	s_nop 0
	v_addc_co_u32_e32 v17, vcc, 0, v7, vcc
	global_load_dword v15, v[16:17], off nt
	v_add_co_u32_e32 v16, vcc, s11, v6
	s_nop 1
	v_addc_co_u32_e32 v17, vcc, 0, v7, vcc
	v_add_co_u32_e32 v18, vcc, s22, v6
	global_load_dword v16, v[16:17], off nt
	s_nop 0
	v_addc_co_u32_e32 v19, vcc, 0, v7, vcc
	global_load_dword v17, v[18:19], off nt
	v_add_co_u32_e32 v18, vcc, s23, v6
	s_nop 1
	v_addc_co_u32_e32 v19, vcc, 0, v7, vcc
	v_add_co_u32_e32 v20, vcc, s24, v6
	global_load_dword v18, v[18:19], off nt
	s_nop 0
	v_addc_co_u32_e32 v21, vcc, 0, v7, vcc
	global_load_dword v19, v[20:21], off nt
	v_add_co_u32_e32 v20, vcc, s25, v6
	s_nop 1
	v_addc_co_u32_e32 v21, vcc, 0, v7, vcc
	v_add_co_u32_e32 v22, vcc, s26, v6
	global_load_dword v20, v[20:21], off nt
	s_nop 0
	v_addc_co_u32_e32 v23, vcc, 0, v7, vcc
	global_load_dword v21, v[22:23], off nt
	v_add_co_u32_e32 v22, vcc, s27, v6
	s_nop 1
	v_addc_co_u32_e32 v23, vcc, 0, v7, vcc
	v_add_co_u32_e32 v24, vcc, s28, v6
	global_load_dword v22, v[22:23], off nt
	s_nop 0
	v_addc_co_u32_e32 v25, vcc, 0, v7, vcc
	global_load_dword v23, v[24:25], off nt
	v_add_co_u32_e32 v24, vcc, s29, v6
	s_nop 1
	v_addc_co_u32_e32 v25, vcc, 0, v7, vcc
	v_add_co_u32_e32 v26, vcc, s30, v6
	global_load_dword v24, v[24:25], off nt
	s_nop 0
	v_addc_co_u32_e32 v27, vcc, 0, v7, vcc
	global_load_dword v25, v[26:27], off nt
	v_add_co_u32_e32 v26, vcc, s31, v6
	s_nop 1
	v_addc_co_u32_e32 v27, vcc, 0, v7, vcc
	v_add_co_u32_e32 v28, vcc, s33, v6
	global_load_dword v26, v[26:27], off nt
	s_nop 0
	v_addc_co_u32_e32 v29, vcc, 0, v7, vcc
	global_load_dword v27, v[28:29], off nt
	v_add_co_u32_e32 v28, vcc, s34, v6
	s_nop 1
	v_addc_co_u32_e32 v29, vcc, 0, v7, vcc
	v_add_co_u32_e32 v30, vcc, s35, v6
	global_load_dword v28, v[28:29], off nt
	s_nop 0
	v_addc_co_u32_e32 v31, vcc, 0, v7, vcc
	global_load_dword v29, v[30:31], off nt
	v_add_co_u32_e32 v30, vcc, s36, v6
	s_nop 1
	v_addc_co_u32_e32 v31, vcc, 0, v7, vcc
	v_add_co_u32_e32 v44, vcc, s37, v6
	global_load_dword v30, v[30:31], off nt
	s_nop 0
	v_addc_co_u32_e32 v45, vcc, 0, v7, vcc
	global_load_dword v31, v[44:45], off nt
	v_add_co_u32_e32 v44, vcc, s38, v6
	s_nop 1
	v_addc_co_u32_e32 v45, vcc, 0, v7, vcc
	global_load_dword v41, v[44:45], off nt
	v_add_co_u32_e32 v44, vcc, s39, v6
	s_nop 1
	v_addc_co_u32_e32 v45, vcc, 0, v7, vcc
	global_load_dword v43, v[44:45], off nt
	v_add_co_u32_e32 v44, vcc, s40, v6
	s_nop 1
	v_addc_co_u32_e32 v45, vcc, 0, v7, vcc
	v_add_co_u32_e32 v46, vcc, s41, v6
	global_load_dword v44, v[44:45], off nt
	s_nop 0
	v_addc_co_u32_e32 v47, vcc, 0, v7, vcc
	global_load_dword v45, v[46:47], off nt
	v_add_co_u32_e32 v46, vcc, s42, v6
	s_nop 1
	v_addc_co_u32_e32 v47, vcc, 0, v7, vcc
	v_add_co_u32_e32 v48, vcc, s43, v6
	global_load_dword v46, v[46:47], off nt
	s_nop 0
	v_addc_co_u32_e32 v49, vcc, 0, v7, vcc
	global_load_dword v47, v[48:49], off nt
	v_add_co_u32_e32 v48, vcc, s44, v6
	s_nop 1
	v_addc_co_u32_e32 v49, vcc, 0, v7, vcc
	v_add_co_u32_e32 v50, vcc, s45, v6
	global_load_dword v48, v[48:49], off nt
	s_nop 0
	v_addc_co_u32_e32 v51, vcc, 0, v7, vcc
	global_load_dword v49, v[50:51], off nt
	v_add_co_u32_e32 v50, vcc, s46, v6
	s_nop 1
	v_addc_co_u32_e32 v51, vcc, 0, v7, vcc
	v_add_co_u32_e32 v52, vcc, s47, v6
	global_load_dword v50, v[50:51], off nt
	s_nop 0
	v_addc_co_u32_e32 v53, vcc, 0, v7, vcc
	global_load_dword v51, v[52:53], off nt
	v_add_co_u32_e32 v52, vcc, s48, v6
	s_nop 1
	v_addc_co_u32_e32 v53, vcc, 0, v7, vcc
	v_add_co_u32_e32 v54, vcc, s49, v6
	global_load_dword v52, v[52:53], off nt
	s_nop 0
	v_addc_co_u32_e32 v55, vcc, 0, v7, vcc
	global_load_dword v53, v[54:55], off nt
	v_add_co_u32_e32 v54, vcc, s50, v6
	s_nop 1
	v_addc_co_u32_e32 v55, vcc, 0, v7, vcc
	v_add_co_u32_e32 v56, vcc, s51, v6
	global_load_dword v54, v[54:55], off nt
	s_nop 0
	v_addc_co_u32_e32 v57, vcc, 0, v7, vcc
	global_load_dword v55, v[56:57], off nt
	v_add_co_u32_e32 v56, vcc, s52, v6
	s_nop 1
	v_addc_co_u32_e32 v57, vcc, 0, v7, vcc
	v_add_co_u32_e32 v58, vcc, s53, v6
	global_load_dword v56, v[56:57], off nt
	s_nop 0
	v_addc_co_u32_e32 v59, vcc, 0, v7, vcc
	global_load_dword v57, v[58:59], off nt
	v_add_co_u32_e32 v58, vcc, s54, v6
	s_nop 1
	v_addc_co_u32_e32 v59, vcc, 0, v7, vcc
	v_add_co_u32_e32 v60, vcc, s55, v6
	global_load_dword v58, v[58:59], off nt
	s_nop 0
	v_addc_co_u32_e32 v61, vcc, 0, v7, vcc
	global_load_dword v59, v[60:61], off nt
	v_add_co_u32_e32 v60, vcc, s56, v6
	s_nop 1
	v_addc_co_u32_e32 v61, vcc, 0, v7, vcc
	v_add_co_u32_e32 v62, vcc, s57, v6
	global_load_dword v60, v[60:61], off nt
	s_nop 0
	v_addc_co_u32_e32 v63, vcc, 0, v7, vcc
	global_load_dword v61, v[62:63], off nt
	v_add_co_u32_e32 v62, vcc, s58, v6
	s_nop 1
	v_addc_co_u32_e32 v63, vcc, 0, v7, vcc
	v_add_co_u32_e32 v64, vcc, s59, v6
	global_load_dword v62, v[62:63], off nt
	s_nop 0
	v_addc_co_u32_e32 v65, vcc, 0, v7, vcc
	global_load_dword v63, v[64:65], off nt
	v_add_co_u32_e32 v64, vcc, s60, v6
	s_nop 1
	v_addc_co_u32_e32 v65, vcc, 0, v7, vcc
	v_add_co_u32_e32 v66, vcc, s61, v6
	global_load_dword v64, v[64:65], off nt
	s_nop 0
	v_addc_co_u32_e32 v67, vcc, 0, v7, vcc
	global_load_dword v65, v[66:67], off nt
	v_add_co_u32_e32 v66, vcc, s62, v6
	s_nop 1
	v_addc_co_u32_e32 v67, vcc, 0, v7, vcc
	v_add_co_u32_e32 v68, vcc, s63, v6
	global_load_dword v66, v[66:67], off nt
	s_nop 0
	v_addc_co_u32_e32 v69, vcc, 0, v7, vcc
	global_load_dword v67, v[68:69], off nt
	v_add_co_u32_e32 v68, vcc, s64, v6
	s_nop 1
	v_addc_co_u32_e32 v69, vcc, 0, v7, vcc
	v_add_co_u32_e32 v70, vcc, s65, v6
	global_load_dword v68, v[68:69], off nt
	s_nop 0
	v_addc_co_u32_e32 v71, vcc, 0, v7, vcc
	global_load_dword v69, v[70:71], off nt
	v_add_co_u32_e32 v70, vcc, s66, v6
	s_nop 1
	v_addc_co_u32_e32 v71, vcc, 0, v7, vcc
	v_add_co_u32_e32 v72, vcc, s67, v6
	global_load_dword v70, v[70:71], off nt
	s_nop 0
	v_addc_co_u32_e32 v73, vcc, 0, v7, vcc
	global_load_dword v71, v[72:73], off nt
	v_add_co_u32_e32 v72, vcc, s68, v6
	s_nop 1
	v_addc_co_u32_e32 v73, vcc, 0, v7, vcc
	v_add_co_u32_e32 v74, vcc, s69, v6
	global_load_dword v72, v[72:73], off nt
	s_nop 0
	v_addc_co_u32_e32 v75, vcc, 0, v7, vcc
	global_load_dword v73, v[74:75], off nt
	v_add_co_u32_e32 v74, vcc, s70, v6
	s_nop 1
	v_addc_co_u32_e32 v75, vcc, 0, v7, vcc
	v_add_co_u32_e32 v76, vcc, s71, v6
	global_load_dword v74, v[74:75], off nt
	s_nop 0
	v_addc_co_u32_e32 v77, vcc, 0, v7, vcc
	global_load_dword v75, v[76:77], off nt
	v_add_co_u32_e32 v76, vcc, s72, v6
	s_nop 1
	v_addc_co_u32_e32 v77, vcc, 0, v7, vcc
	v_add_co_u32_e32 v78, vcc, 0x78000, v6
	global_load_dword v76, v[76:77], off nt
	s_nop 0
	v_addc_co_u32_e32 v79, vcc, 0, v7, vcc
	global_load_dword v77, v[78:79], off nt
	v_add_co_u32_e32 v78, vcc, 0x7a000, v6
	s_nop 1
	v_addc_co_u32_e32 v79, vcc, 0, v7, vcc
	v_add_co_u32_e32 v80, vcc, 0x7c000, v6
	global_load_dword v78, v[78:79], off nt
	s_nop 0
	v_addc_co_u32_e32 v81, vcc, 0, v7, vcc
	v_add_co_u32_e32 v6, vcc, 0x7e000, v6
	global_load_dword v79, v[80:81], off nt
	s_nop 0
	v_addc_co_u32_e32 v7, vcc, 0, v7, vcc
	global_load_dword v80, v[6:7], off nt
	s_branch .LBB0_201
.LBB0_204:
	s_add_u32 s0, s10, s0
	s_addc_u32 s1, s11, s1
	s_add_u32 s0, s0, s2
	s_addc_u32 s1, s1, s3
	v_lshlrev_b32_e32 v2, 2, v198
	v_mov_b32_e32 v3, 0
	v_lshl_add_u64 v[6:7], s[0:1], 0, v[2:3]
	s_waitcnt vmcnt(62)
	v_add_co_u32_e32 v26, vcc, 0x2000, v6
	v_lshlrev_b32_e32 v4, 1, v4
	s_nop 0
	v_addc_co_u32_e32 v27, vcc, 0, v7, vcc
	v_add_co_u32_e32 v28, vcc, 0x4000, v6
	s_waitcnt vmcnt(9)
	v_mov_b32_e32 v5, v3
	v_addc_co_u32_e32 v29, vcc, 0, v7, vcc
	v_add_co_u32_e32 v30, vcc, 0x6000, v6
	v_lshl_add_u64 v[4:5], s[82:83], 0, v[4:5]
	s_nop 0
	v_addc_co_u32_e32 v31, vcc, 0, v7, vcc
	v_add_co_u32_e32 v32, vcc, 0x8000, v6
	s_mov_b32 s2, 0xc000
	s_nop 0
	v_addc_co_u32_e32 v33, vcc, 0, v7, vcc
	v_add_co_u32_e32 v34, vcc, 0xa000, v6
	s_mov_b32 s3, 0xe000
	s_nop 0
	v_addc_co_u32_e32 v35, vcc, 0, v7, vcc
	v_add_co_u32_e32 v36, vcc, 0xc000, v6
	s_mov_b32 s4, 0x10000
	s_nop 0
	v_addc_co_u32_e32 v37, vcc, 0, v7, vcc
	v_add_co_u32_e32 v38, vcc, 0xe000, v6
	s_mov_b32 s5, 0x12000
	s_nop 0
	v_addc_co_u32_e32 v39, vcc, 0, v7, vcc
	v_add_co_u32_e32 v40, vcc, 0x10000, v6
	s_mov_b32 s7, 0x14000
	s_nop 0
	v_addc_co_u32_e32 v41, vcc, 0, v7, vcc
	global_load_dword v8, v[26:27], off nt
	global_load_dword v9, v[28:29], off nt
	global_load_dword v19, v[30:31], off nt
	global_load_dword v20, v[32:33], off nt
	global_load_dword v21, v[34:35], off nt
	global_load_dword v22, v[36:37], off nt
	global_load_dword v23, v[38:39], off nt
	global_load_dword v24, v[40:41], off nt
	v_add_co_u32_e32 v34, vcc, 0x12000, v6
	s_mov_b32 s8, 0x16000
	s_nop 0
	v_addc_co_u32_e32 v35, vcc, 0, v7, vcc
	v_add_co_u32_e32 v36, vcc, 0x14000, v6
	s_mov_b32 s9, 0x18000
	s_nop 0
	v_addc_co_u32_e32 v37, vcc, 0, v7, vcc
	v_add_co_u32_e32 v38, vcc, 0x16000, v6
	s_mov_b32 s22, 0x1a000
	s_nop 0
	v_addc_co_u32_e32 v39, vcc, 0, v7, vcc
	v_add_co_u32_e32 v40, vcc, 0x18000, v6
	s_mov_b32 s23, 0x1c000
	s_nop 0
	v_addc_co_u32_e32 v41, vcc, 0, v7, vcc
	v_add_co_u32_e32 v42, vcc, 0x1a000, v6
	s_mov_b32 s24, 0x1e000
	s_nop 0
	v_addc_co_u32_e32 v43, vcc, 0, v7, vcc
	v_add_co_u32_e32 v44, vcc, 0x1c000, v6
	s_mov_b32 s25, 0x20000
	s_nop 0
	v_addc_co_u32_e32 v45, vcc, 0, v7, vcc
	v_add_co_u32_e32 v46, vcc, 0x1e000, v6
	s_mov_b32 s26, 0x22000
	s_nop 0
	v_addc_co_u32_e32 v47, vcc, 0, v7, vcc
	v_add_co_u32_e32 v48, vcc, 0x20000, v6
	s_mov_b32 s27, 0x24000
	s_nop 0
	v_addc_co_u32_e32 v49, vcc, 0, v7, vcc
	global_load_dword v25, v[34:35], off nt
	global_load_dword v26, v[36:37], off nt
	global_load_dword v27, v[38:39], off nt
	global_load_dword v28, v[40:41], off nt
	global_load_dword v29, v[42:43], off nt
	global_load_dword v30, v[44:45], off nt
	global_load_dword v31, v[46:47], off nt
	global_load_dword v32, v[48:49], off nt
	v_add_co_u32_e32 v42, vcc, 0x22000, v6
	s_mov_b32 s28, 0x26000
	s_nop 0
	v_addc_co_u32_e32 v43, vcc, 0, v7, vcc
	v_add_co_u32_e32 v44, vcc, 0x24000, v6
	s_mov_b32 s29, 0x28000
	s_nop 0
	v_addc_co_u32_e32 v45, vcc, 0, v7, vcc
	v_add_co_u32_e32 v46, vcc, 0x26000, v6
	s_mov_b32 s30, 0x2a000
	s_nop 0
	v_addc_co_u32_e32 v47, vcc, 0, v7, vcc
	v_add_co_u32_e32 v48, vcc, 0x28000, v6
	s_mov_b32 s31, 0x2c000
	s_nop 0
	v_addc_co_u32_e32 v49, vcc, 0, v7, vcc
	v_add_co_u32_e32 v50, vcc, 0x2a000, v6
	s_mov_b32 s33, 0x2e000
	s_nop 0
	v_addc_co_u32_e32 v51, vcc, 0, v7, vcc
	v_add_co_u32_e32 v52, vcc, 0x2c000, v6
	s_mov_b32 s34, 0x30000
	s_nop 0
	v_addc_co_u32_e32 v53, vcc, 0, v7, vcc
	v_add_co_u32_e32 v54, vcc, 0x2e000, v6
	s_mov_b32 s35, 0x32000
	s_nop 0
	v_addc_co_u32_e32 v55, vcc, 0, v7, vcc
	v_add_co_u32_e32 v56, vcc, 0x30000, v6
	s_mov_b32 s36, 0x34000
	s_nop 0
	v_addc_co_u32_e32 v57, vcc, 0, v7, vcc
	global_load_dword v33, v[42:43], off nt
	global_load_dword v34, v[44:45], off nt
	global_load_dword v35, v[46:47], off nt
	global_load_dword v36, v[48:49], off nt
	global_load_dword v37, v[50:51], off nt
	global_load_dword v38, v[52:53], off nt
	global_load_dword v39, v[54:55], off nt
	global_load_dword v40, v[56:57], off nt
	v_add_co_u32_e32 v50, vcc, 0x32000, v6
	s_mov_b32 s37, 0x36000
	s_nop 0
	v_addc_co_u32_e32 v51, vcc, 0, v7, vcc
	v_add_co_u32_e32 v52, vcc, 0x34000, v6
	s_mov_b32 s38, 0x38000
	s_nop 0
	v_addc_co_u32_e32 v53, vcc, 0, v7, vcc
	v_add_co_u32_e32 v54, vcc, 0x36000, v6
	s_mov_b32 s39, 0x3a000
	s_nop 0
	v_addc_co_u32_e32 v55, vcc, 0, v7, vcc
	v_add_co_u32_e32 v56, vcc, 0x38000, v6
	s_mov_b32 s40, 0x3c000
	s_nop 0
	v_addc_co_u32_e32 v57, vcc, 0, v7, vcc
	v_add_co_u32_e32 v58, vcc, 0x3a000, v6
	s_mov_b32 s41, 0x3e000
	s_nop 0
	v_addc_co_u32_e32 v59, vcc, 0, v7, vcc
	v_add_co_u32_e32 v60, vcc, 0x3c000, v6
	s_mov_b32 s42, 0x40000
	s_nop 0
	v_addc_co_u32_e32 v61, vcc, 0, v7, vcc
	v_add_co_u32_e32 v62, vcc, 0x3e000, v6
	s_mov_b32 s43, 0x42000
	s_nop 0
	v_addc_co_u32_e32 v63, vcc, 0, v7, vcc
	v_add_co_u32_e32 v64, vcc, 0x40000, v6
	s_mov_b32 s44, 0x44000
	s_nop 0
	v_addc_co_u32_e32 v65, vcc, 0, v7, vcc
	global_load_dword v41, v[50:51], off nt
	global_load_dword v42, v[52:53], off nt
	global_load_dword v44, v[54:55], off nt
	global_load_dword v45, v[56:57], off nt
	global_load_dword v46, v[58:59], off nt
	global_load_dword v47, v[60:61], off nt
	global_load_dword v48, v[62:63], off nt
	global_load_dword v49, v[64:65], off nt
	v_add_co_u32_e32 v58, vcc, 0x42000, v6
	s_mov_b32 s45, 0x46000
	s_nop 0
	v_addc_co_u32_e32 v59, vcc, 0, v7, vcc
	v_add_co_u32_e32 v60, vcc, 0x44000, v6
	s_mov_b32 s46, 0x48000
	s_nop 0
	v_addc_co_u32_e32 v61, vcc, 0, v7, vcc
	v_add_co_u32_e32 v62, vcc, 0x46000, v6
	s_mov_b32 s47, 0x4a000
	s_nop 0
	v_addc_co_u32_e32 v63, vcc, 0, v7, vcc
	v_add_co_u32_e32 v64, vcc, 0x48000, v6
	s_mov_b32 s48, 0x4c000
	s_nop 0
	v_addc_co_u32_e32 v65, vcc, 0, v7, vcc
	v_add_co_u32_e32 v66, vcc, 0x4a000, v6
	s_mov_b32 s49, 0x4e000
	s_nop 0
	v_addc_co_u32_e32 v67, vcc, 0, v7, vcc
	v_add_co_u32_e32 v68, vcc, 0x4c000, v6
	s_mov_b32 s50, 0x50000
	s_nop 0
	v_addc_co_u32_e32 v69, vcc, 0, v7, vcc
	v_add_co_u32_e32 v70, vcc, 0x4e000, v6
	s_mov_b32 s51, 0x52000
	s_nop 0
	v_addc_co_u32_e32 v71, vcc, 0, v7, vcc
	v_add_co_u32_e32 v72, vcc, 0x50000, v6
	s_mov_b32 s52, 0x54000
	s_nop 0
	v_addc_co_u32_e32 v73, vcc, 0, v7, vcc
	global_load_dword v50, v[58:59], off nt
	global_load_dword v51, v[60:61], off nt
	global_load_dword v52, v[62:63], off nt
	global_load_dword v53, v[64:65], off nt
	global_load_dword v54, v[66:67], off nt
	global_load_dword v55, v[68:69], off nt
	global_load_dword v56, v[70:71], off nt
	global_load_dword v57, v[72:73], off nt
	v_add_co_u32_e32 v66, vcc, 0x52000, v6
	s_mov_b32 s53, 0x56000
	s_nop 0
	v_addc_co_u32_e32 v67, vcc, 0, v7, vcc
	v_add_co_u32_e32 v68, vcc, 0x54000, v6
	s_mov_b32 s54, 0x58000
	s_nop 0
	v_addc_co_u32_e32 v69, vcc, 0, v7, vcc
	v_add_co_u32_e32 v70, vcc, 0x56000, v6
	s_mov_b32 s55, 0x5a000
	s_nop 0
	v_addc_co_u32_e32 v71, vcc, 0, v7, vcc
	v_add_co_u32_e32 v72, vcc, 0x58000, v6
	s_mov_b32 s56, 0x5c000
	s_nop 0
	v_addc_co_u32_e32 v73, vcc, 0, v7, vcc
	v_add_co_u32_e32 v74, vcc, 0x5a000, v6
	s_mov_b32 s57, 0x5e000
	s_nop 0
	v_addc_co_u32_e32 v75, vcc, 0, v7, vcc
	v_add_co_u32_e32 v76, vcc, 0x5c000, v6
	s_mov_b32 s58, 0x60000
	s_nop 0
	v_addc_co_u32_e32 v77, vcc, 0, v7, vcc
	v_add_co_u32_e32 v78, vcc, 0x5e000, v6
	s_mov_b32 s59, 0x62000
	s_nop 0
	v_addc_co_u32_e32 v79, vcc, 0, v7, vcc
	v_add_co_u32_e32 v80, vcc, 0x60000, v6
	s_mov_b32 s60, 0x64000
	s_waitcnt vmcnt(48)
	v_addc_co_u32_e32 v81, vcc, 0, v7, vcc
	global_load_dword v58, v[66:67], off nt
	global_load_dword v59, v[68:69], off nt
	global_load_dword v60, v[70:71], off nt
	global_load_dword v61, v[72:73], off nt
	global_load_dword v62, v[74:75], off nt
	global_load_dword v63, v[76:77], off nt
	global_load_dword v64, v[78:79], off nt
	global_load_dword v65, v[80:81], off nt
	v_add_co_u32_e32 v74, vcc, 0x62000, v6
	s_mov_b32 s61, 0x66000
	s_nop 0
	v_addc_co_u32_e32 v75, vcc, 0, v7, vcc
	v_add_co_u32_e32 v76, vcc, 0x64000, v6
	s_mov_b32 s62, 0x68000
	s_nop 0
	v_addc_co_u32_e32 v77, vcc, 0, v7, vcc
	v_add_co_u32_e32 v78, vcc, 0x66000, v6
	s_mov_b32 s63, 0x6a000
	s_nop 0
	v_addc_co_u32_e32 v79, vcc, 0, v7, vcc
	v_add_co_u32_e32 v80, vcc, 0x68000, v6
	s_mov_b32 s64, 0x6c000
	s_nop 0
	v_addc_co_u32_e32 v81, vcc, 0, v7, vcc
	v_add_co_u32_e32 v82, vcc, 0x6a000, v6
	s_mov_b32 s65, 0x6e000
	s_nop 0
	v_addc_co_u32_e32 v83, vcc, 0, v7, vcc
	v_add_co_u32_e32 v84, vcc, 0x6c000, v6
	s_mov_b32 s66, 0x70000
	s_nop 0
	v_addc_co_u32_e32 v85, vcc, 0, v7, vcc
	v_add_co_u32_e32 v86, vcc, 0x6e000, v6
	s_mov_b32 s67, 0x72000
	s_nop 0
	v_addc_co_u32_e32 v87, vcc, 0, v7, vcc
	v_add_co_u32_e32 v88, vcc, 0x70000, v6
	s_mov_b32 s68, 0x74000
	s_nop 0
	v_addc_co_u32_e32 v89, vcc, 0, v7, vcc
	global_load_dword v66, v[74:75], off nt
	global_load_dword v67, v[76:77], off nt
	global_load_dword v68, v[78:79], off nt
	global_load_dword v69, v[80:81], off nt
	global_load_dword v70, v[82:83], off nt
	global_load_dword v71, v[84:85], off nt
	global_load_dword v72, v[86:87], off nt
	global_load_dword v73, v[88:89], off nt
	v_add_co_u32_e32 v82, vcc, 0x72000, v6
	s_mov_b32 s69, 0x76000
	s_nop 0
	v_addc_co_u32_e32 v83, vcc, 0, v7, vcc
	v_add_co_u32_e32 v84, vcc, 0x74000, v6
	s_movk_i32 s70, 0x7fff
	s_nop 0
	v_addc_co_u32_e32 v85, vcc, 0, v7, vcc
	v_add_co_u32_e32 v86, vcc, 0x76000, v6
	s_mov_b32 s71, 0xffff0000
	s_nop 0
	v_addc_co_u32_e32 v87, vcc, 0, v7, vcc
	v_add_co_u32_e32 v88, vcc, 0x78000, v6
	v_readlane_b32 s73, v252, 14
	s_nop 0
	v_addc_co_u32_e32 v89, vcc, 0, v7, vcc
	v_add_co_u32_e32 v90, vcc, 0x7a000, v6
	s_mov_b32 s80, s96
	s_nop 0
	v_addc_co_u32_e32 v91, vcc, 0, v7, vcc
	v_add_co_u32_e32 v92, vcc, 0x7c000, v6
	s_mov_b32 s90, s12
	s_nop 0
	v_addc_co_u32_e32 v93, vcc, 0, v7, vcc
	v_add_co_u32_e32 v6, vcc, 0x7e000, v6
	s_nop 1
	v_addc_co_u32_e32 v7, vcc, 0, v7, vcc
	global_load_dword v43, v2, s[0:1] nt
	global_load_dword v74, v[82:83], off nt
	global_load_dword v75, v[84:85], off nt
	global_load_dword v76, v[86:87], off nt
	global_load_dword v77, v[88:89], off nt
	global_load_dword v78, v[90:91], off nt
	global_load_dword v79, v[92:93], off nt
	global_load_dword v80, v[6:7], off nt
	s_mov_b64 s[0:1], 0x2700800
	v_lshl_add_u64 v[4:5], v[4:5], 0, s[0:1]
	s_branch .LBB0_206

.LBB0_206:
	v_add_u32_e32 v6, 0x400, v10
	s_waitcnt vmcnt(7)
	ds_write2_b32 v10, v43, v8 offset1:65
	ds_write2_b32 v10, v9, v19 offset0:130 offset1:195
	ds_write2_b32 v6, v20, v21 offset0:4 offset1:69
	ds_write2_b32 v6, v22, v23 offset0:134 offset1:199
	v_add_u32_e32 v6, 0x800, v10
	ds_write2_b32 v6, v24, v25 offset0:8 offset1:73
	ds_write2_b32 v6, v26, v27 offset0:138 offset1:203
	v_add_u32_e32 v6, 0xc00, v10
	ds_write2_b32 v6, v28, v29 offset0:12 offset1:77
	ds_write2_b32 v6, v30, v31 offset0:142 offset1:207
	v_add_u32_e32 v6, 0x1000, v10
	ds_write2_b32 v6, v32, v33 offset0:16 offset1:81
	ds_write2_b32 v6, v34, v35 offset0:146 offset1:211
	v_add_u32_e32 v6, 0x1400, v10
	ds_write2_b32 v6, v36, v37 offset0:20 offset1:85
	ds_write2_b32 v6, v38, v39 offset0:150 offset1:215
	v_add_u32_e32 v6, 0x1800, v10
	ds_write2_b32 v6, v40, v41 offset0:24 offset1:89
	ds_write2_b32 v6, v42, v44 offset0:154 offset1:219
	v_add_u32_e32 v6, 0x1c00, v10
	ds_write2_b32 v6, v45, v46 offset0:28 offset1:93
	ds_write2_b32 v6, v47, v48 offset0:158 offset1:223
	v_add_u32_e32 v6, 0x2000, v10
	ds_write2_b32 v6, v49, v50 offset0:32 offset1:97
	ds_write2_b32 v6, v51, v52 offset0:162 offset1:227
	v_add_u32_e32 v6, 0x2400, v10
	ds_write2_b32 v6, v53, v54 offset0:36 offset1:101
	ds_write2_b32 v6, v55, v56 offset0:166 offset1:231
	v_add_u32_e32 v6, 0x2800, v10
	ds_write2_b32 v6, v57, v58 offset0:40 offset1:105
	ds_write2_b32 v6, v59, v60 offset0:170 offset1:235
	v_add_u32_e32 v6, 0x2c00, v10
	ds_write2_b32 v6, v61, v62 offset0:44 offset1:109
	ds_write2_b32 v6, v63, v64 offset0:174 offset1:239
	v_add_u32_e32 v6, 0x3000, v10
	ds_write2_b32 v6, v65, v66 offset0:48 offset1:113
	ds_write2_b32 v6, v67, v68 offset0:178 offset1:243
	v_add_u32_e32 v6, 0x3400, v10
	ds_write2_b32 v6, v69, v70 offset0:52 offset1:117
	ds_write2_b32 v6, v71, v72 offset0:182 offset1:247
	v_add_u32_e32 v6, 0x3800, v10
	s_waitcnt vmcnt(6)
	ds_write2_b32 v6, v73, v74 offset0:56 offset1:121
	s_waitcnt vmcnt(4)
	ds_write2_b32 v6, v75, v76 offset0:186 offset1:251
	v_add_u32_e32 v6, 0x3c00, v10
	s_waitcnt vmcnt(2)
	ds_write2_b32 v6, v77, v78 offset0:60 offset1:125
	s_waitcnt vmcnt(0)
	ds_write2_b32 v6, v79, v80 offset0:190 offset1:255
	s_waitcnt lgkmcnt(0)
	s_add_i32 s72, s73, s85
	s_cmpk_gt_i32 s72, 0x1ff
	s_cselect_b64 s[0:1], -1, 0
	s_and_b64 vcc, exec, s[0:1]
	s_cbranch_vccnz .LBB0_205
	s_ashr_i32 s74, s72, 31
	s_lshr_b32 s74, s74, 23
	s_add_i32 s74, s72, s74
	s_and_b32 s74, s74, 0xfe00
	s_sub_i32 s76, s72, s74
	s_sext_i32_i16 s74, s76
	s_bfe_u32 s74, s74, 0x5001a
	s_add_i32 s77, s76, s74
	s_sext_i32_i16 s74, s77
	s_lshl_b32 s74, s74, 1
	s_andn2_b32 s74, s74, 63
	s_ashr_i32 s75, s74, 31
	s_lshl_b64 s[74:75], s[74:75], 13
	s_add_u32 s78, s10, s74
	s_addc_u32 s79, s11, s75
	s_and_b32 s74, s77, 0xffe0
	s_sub_i32 s74, s76, s74
	s_sext_i32_i16 s74, s74
	s_lshl_b32 s74, s74, 6
	s_ashr_i32 s75, s74, 31
	s_lshl_b64 s[74:75], s[74:75], 2
	s_add_u32 s74, s78, s74
	s_addc_u32 s75, s79, s75
	v_lshl_add_u64 v[6:7], s[74:75], 0, v[2:3]
	global_load_dword v43, v2, s[74:75] nt
	s_movk_i32 s74, 0x2000
	v_add_co_u32_e32 v8, vcc, s74, v6
	s_movk_i32 s74, 0x4000
	s_nop 0
	v_addc_co_u32_e32 v9, vcc, 0, v7, vcc
	v_add_co_u32_e32 v20, vcc, s74, v6
	s_movk_i32 s74, 0x6000
	s_nop 0
	v_addc_co_u32_e32 v21, vcc, 0, v7, vcc
	global_load_dword v8, v[8:9], off nt
	s_nop 0
	global_load_dword v9, v[20:21], off nt
	v_add_co_u32_e32 v20, vcc, s74, v6
	s_mov_b32 s74, 0x8000
	s_nop 0
	v_addc_co_u32_e32 v21, vcc, 0, v7, vcc
	global_load_dword v19, v[20:21], off nt
	v_add_co_u32_e32 v20, vcc, s74, v6
	s_mov_b32 s74, 0xa000
	s_nop 0
	v_addc_co_u32_e32 v21, vcc, 0, v7, vcc
	v_add_co_u32_e32 v22, vcc, s74, v6
	global_load_dword v20, v[20:21], off nt
	s_nop 0
	v_addc_co_u32_e32 v23, vcc, 0, v7, vcc
	global_load_dword v21, v[22:23], off nt
	v_add_co_u32_e32 v22, vcc, s2, v6
	s_nop 1
	v_addc_co_u32_e32 v23, vcc, 0, v7, vcc
	v_add_co_u32_e32 v24, vcc, s3, v6
	global_load_dword v22, v[22:23], off nt
	s_nop 0
	v_addc_co_u32_e32 v25, vcc, 0, v7, vcc
	global_load_dword v23, v[24:25], off nt
	v_add_co_u32_e32 v24, vcc, s4, v6
	s_nop 1
	v_addc_co_u32_e32 v25, vcc, 0, v7, vcc
	v_add_co_u32_e32 v26, vcc, s5, v6
	global_load_dword v24, v[24:25], off nt
	s_nop 0
	v_addc_co_u32_e32 v27, vcc, 0, v7, vcc
	global_load_dword v25, v[26:27], off nt
	v_add_co_u32_e32 v26, vcc, s7, v6
	s_nop 1
	v_addc_co_u32_e32 v27, vcc, 0, v7, vcc
	v_add_co_u32_e32 v28, vcc, s8, v6
	global_load_dword v26, v[26:27], off nt
	s_nop 0
	v_addc_co_u32_e32 v29, vcc, 0, v7, vcc
	global_load_dword v27, v[28:29], off nt
	v_add_co_u32_e32 v28, vcc, s9, v6
	s_nop 1
	v_addc_co_u32_e32 v29, vcc, 0, v7, vcc
	v_add_co_u32_e32 v30, vcc, s22, v6
	global_load_dword v28, v[28:29], off nt
	s_nop 0
	v_addc_co_u32_e32 v31, vcc, 0, v7, vcc
	global_load_dword v29, v[30:31], off nt
	v_add_co_u32_e32 v30, vcc, s23, v6
	s_nop 1
	v_addc_co_u32_e32 v31, vcc, 0, v7, vcc
	v_add_co_u32_e32 v32, vcc, s24, v6
	global_load_dword v30, v[30:31], off nt
	s_nop 0
	v_addc_co_u32_e32 v33, vcc, 0, v7, vcc
	global_load_dword v31, v[32:33], off nt
	v_add_co_u32_e32 v32, vcc, s25, v6
	s_nop 1
	v_addc_co_u32_e32 v33, vcc, 0, v7, vcc
	v_add_co_u32_e32 v34, vcc, s26, v6
	global_load_dword v32, v[32:33], off nt
	s_nop 0
	v_addc_co_u32_e32 v35, vcc, 0, v7, vcc
	global_load_dword v33, v[34:35], off nt
	v_add_co_u32_e32 v34, vcc, s27, v6
	s_nop 1
	v_addc_co_u32_e32 v35, vcc, 0, v7, vcc
	v_add_co_u32_e32 v36, vcc, s28, v6
	global_load_dword v34, v[34:35], off nt
	s_nop 0
	v_addc_co_u32_e32 v37, vcc, 0, v7, vcc
	global_load_dword v35, v[36:37], off nt
	v_add_co_u32_e32 v36, vcc, s29, v6
	s_nop 1
	v_addc_co_u32_e32 v37, vcc, 0, v7, vcc
	v_add_co_u32_e32 v38, vcc, s30, v6
	global_load_dword v36, v[36:37], off nt
	s_nop 0
	v_addc_co_u32_e32 v39, vcc, 0, v7, vcc
	global_load_dword v37, v[38:39], off nt
	v_add_co_u32_e32 v38, vcc, s31, v6
	s_nop 1
	v_addc_co_u32_e32 v39, vcc, 0, v7, vcc
	v_add_co_u32_e32 v40, vcc, s33, v6
	global_load_dword v38, v[38:39], off nt
	s_nop 0
	v_addc_co_u32_e32 v41, vcc, 0, v7, vcc
	global_load_dword v39, v[40:41], off nt
	v_add_co_u32_e32 v40, vcc, s34, v6
	s_nop 1
	v_addc_co_u32_e32 v41, vcc, 0, v7, vcc
	v_add_co_u32_e32 v44, vcc, s35, v6
	global_load_dword v40, v[40:41], off nt
	s_nop 0
	v_addc_co_u32_e32 v45, vcc, 0, v7, vcc
	global_load_dword v41, v[44:45], off nt
	v_add_co_u32_e32 v44, vcc, s36, v6
	s_nop 1
	v_addc_co_u32_e32 v45, vcc, 0, v7, vcc
	global_load_dword v42, v[44:45], off nt
	v_add_co_u32_e32 v44, vcc, s37, v6
	s_nop 1
	v_addc_co_u32_e32 v45, vcc, 0, v7, vcc
	v_add_co_u32_e32 v46, vcc, s38, v6
	global_load_dword v44, v[44:45], off nt
	s_nop 0
	v_addc_co_u32_e32 v47, vcc, 0, v7, vcc
	global_load_dword v45, v[46:47], off nt
	v_add_co_u32_e32 v46, vcc, s39, v6
	s_nop 1
	v_addc_co_u32_e32 v47, vcc, 0, v7, vcc
	v_add_co_u32_e32 v48, vcc, s40, v6
	global_load_dword v46, v[46:47], off nt
	s_nop 0
	v_addc_co_u32_e32 v49, vcc, 0, v7, vcc
	global_load_dword v47, v[48:49], off nt
	v_add_co_u32_e32 v48, vcc, s41, v6
	s_nop 1
	v_addc_co_u32_e32 v49, vcc, 0, v7, vcc
	v_add_co_u32_e32 v50, vcc, s42, v6
	global_load_dword v48, v[48:49], off nt
	s_nop 0
	v_addc_co_u32_e32 v51, vcc, 0, v7, vcc
	global_load_dword v49, v[50:51], off nt
	v_add_co_u32_e32 v50, vcc, s43, v6
	s_nop 1
	v_addc_co_u32_e32 v51, vcc, 0, v7, vcc
	v_add_co_u32_e32 v52, vcc, s44, v6
	global_load_dword v50, v[50:51], off nt
	s_nop 0
	v_addc_co_u32_e32 v53, vcc, 0, v7, vcc
	global_load_dword v51, v[52:53], off nt
	v_add_co_u32_e32 v52, vcc, s45, v6
	s_nop 1
	v_addc_co_u32_e32 v53, vcc, 0, v7, vcc
	v_add_co_u32_e32 v54, vcc, s46, v6
	global_load_dword v52, v[52:53], off nt
	s_nop 0
	v_addc_co_u32_e32 v55, vcc, 0, v7, vcc
	global_load_dword v53, v[54:55], off nt
	v_add_co_u32_e32 v54, vcc, s47, v6
	s_nop 1
	v_addc_co_u32_e32 v55, vcc, 0, v7, vcc
	v_add_co_u32_e32 v56, vcc, s48, v6
	global_load_dword v54, v[54:55], off nt
	s_nop 0
	v_addc_co_u32_e32 v57, vcc, 0, v7, vcc
	global_load_dword v55, v[56:57], off nt
	v_add_co_u32_e32 v56, vcc, s49, v6
	s_nop 1
	v_addc_co_u32_e32 v57, vcc, 0, v7, vcc
	v_add_co_u32_e32 v58, vcc, s50, v6
	global_load_dword v56, v[56:57], off nt
	s_nop 0
	v_addc_co_u32_e32 v59, vcc, 0, v7, vcc
	global_load_dword v57, v[58:59], off nt
	v_add_co_u32_e32 v58, vcc, s51, v6
	s_nop 1
	v_addc_co_u32_e32 v59, vcc, 0, v7, vcc
	v_add_co_u32_e32 v60, vcc, s52, v6
	global_load_dword v58, v[58:59], off nt
	s_nop 0
	v_addc_co_u32_e32 v61, vcc, 0, v7, vcc
	global_load_dword v59, v[60:61], off nt
	v_add_co_u32_e32 v60, vcc, s53, v6
	s_nop 1
	v_addc_co_u32_e32 v61, vcc, 0, v7, vcc
	v_add_co_u32_e32 v62, vcc, s54, v6
	global_load_dword v60, v[60:61], off nt
	s_nop 0
	v_addc_co_u32_e32 v63, vcc, 0, v7, vcc
	global_load_dword v61, v[62:63], off nt
	v_add_co_u32_e32 v62, vcc, s55, v6
	s_nop 1
	v_addc_co_u32_e32 v63, vcc, 0, v7, vcc
	v_add_co_u32_e32 v64, vcc, s56, v6
	global_load_dword v62, v[62:63], off nt
	s_nop 0
	v_addc_co_u32_e32 v65, vcc, 0, v7, vcc
	global_load_dword v63, v[64:65], off nt
	v_add_co_u32_e32 v64, vcc, s57, v6
	s_nop 1
	v_addc_co_u32_e32 v65, vcc, 0, v7, vcc
	v_add_co_u32_e32 v66, vcc, s58, v6
	global_load_dword v64, v[64:65], off nt
	s_nop 0
	v_addc_co_u32_e32 v67, vcc, 0, v7, vcc
	global_load_dword v65, v[66:67], off nt
	v_add_co_u32_e32 v66, vcc, s59, v6
	s_nop 1
	v_addc_co_u32_e32 v67, vcc, 0, v7, vcc
	v_add_co_u32_e32 v68, vcc, s60, v6
	global_load_dword v66, v[66:67], off nt
	s_nop 0
	v_addc_co_u32_e32 v69, vcc, 0, v7, vcc
	global_load_dword v67, v[68:69], off nt
	v_add_co_u32_e32 v68, vcc, s61, v6
	s_nop 1
	v_addc_co_u32_e32 v69, vcc, 0, v7, vcc
	v_add_co_u32_e32 v70, vcc, s62, v6
	global_load_dword v68, v[68:69], off nt
	s_nop 0
	v_addc_co_u32_e32 v71, vcc, 0, v7, vcc
	global_load_dword v69, v[70:71], off nt
	v_add_co_u32_e32 v70, vcc, s63, v6
	s_nop 1
	v_addc_co_u32_e32 v71, vcc, 0, v7, vcc
	v_add_co_u32_e32 v72, vcc, s64, v6
	global_load_dword v70, v[70:71], off nt
	s_nop 0
	v_addc_co_u32_e32 v73, vcc, 0, v7, vcc
	global_load_dword v71, v[72:73], off nt
	v_add_co_u32_e32 v72, vcc, s65, v6
	s_nop 1
	v_addc_co_u32_e32 v73, vcc, 0, v7, vcc
	v_add_co_u32_e32 v74, vcc, s66, v6
	global_load_dword v72, v[72:73], off nt
	s_nop 0
	v_addc_co_u32_e32 v75, vcc, 0, v7, vcc
	global_load_dword v73, v[74:75], off nt
	v_add_co_u32_e32 v74, vcc, s67, v6
	s_nop 1
	v_addc_co_u32_e32 v75, vcc, 0, v7, vcc
	v_add_co_u32_e32 v76, vcc, s68, v6
	global_load_dword v74, v[74:75], off nt
	s_nop 0
	v_addc_co_u32_e32 v77, vcc, 0, v7, vcc
	global_load_dword v75, v[76:77], off nt
	v_add_co_u32_e32 v76, vcc, s69, v6
	s_nop 1
	v_addc_co_u32_e32 v77, vcc, 0, v7, vcc
	v_add_co_u32_e32 v78, vcc, 0x78000, v6
	global_load_dword v76, v[76:77], off nt
	s_nop 0
	v_addc_co_u32_e32 v79, vcc, 0, v7, vcc
	global_load_dword v77, v[78:79], off nt
	v_add_co_u32_e32 v78, vcc, 0x7a000, v6
	s_nop 1
	v_addc_co_u32_e32 v79, vcc, 0, v7, vcc
	v_add_co_u32_e32 v80, vcc, 0x7c000, v6
	global_load_dword v78, v[78:79], off nt
	s_nop 0
	v_addc_co_u32_e32 v81, vcc, 0, v7, vcc
	v_add_co_u32_e32 v6, vcc, 0x7e000, v6
	global_load_dword v79, v[80:81], off nt
	s_nop 0
	v_addc_co_u32_e32 v7, vcc, 0, v7, vcc
	global_load_dword v80, v[6:7], off nt
	s_branch .LBB0_205

.LBB0_213:
	s_ashr_i32 s0, s88, 31
	s_lshr_b32 s0, s0, 22
	s_add_i32 s0, s88, s0
	s_and_b32 s0, s0, 0xfc00
	s_sub_i32 s2, s88, s0
	s_sext_i32_i16 s0, s2
	s_bfe_u32 s0, s0, 0x5001a
	s_add_i32 s3, s2, s0
	s_sext_i32_i16 s0, s3
	s_lshl_b32 s0, s0, 1
	s_andn2_b32 s0, s0, 63
	s_ashr_i32 s1, s0, 31
	s_lshl_b64 s[0:1], s[0:1], 13
	s_waitcnt lgkmcnt(0)
	s_add_u32 s4, s18, s0
	s_addc_u32 s5, s19, s1
	s_and_b32 s0, s3, 0xffe0
	s_sub_i32 s0, s2, s0
	s_sext_i32_i16 s0, s0
	s_lshl_b32 s0, s0, 6
	s_ashr_i32 s1, s0, 31
	s_lshl_b64 s[0:1], s[0:1], 2
	s_add_u32 s0, s4, s0
	s_addc_u32 s1, s5, s1
	v_mov_b32_e32 v3, 0
	v_lshlrev_b32_e32 v2, 2, v198
	v_lshl_add_u64 v[4:5], s[0:1], 0, v[2:3]
	s_movk_i32 s4, 0x2000
	v_add_co_u32_e32 v6, vcc, s4, v4
	s_movk_i32 s5, 0x4000
	s_nop 0
	v_addc_co_u32_e32 v7, vcc, 0, v5, vcc
	s_waitcnt vmcnt(62)
	v_add_co_u32_e32 v16, vcc, s5, v4
	s_movk_i32 s7, 0x6000
	s_waitcnt vmcnt(61)
	v_addc_co_u32_e32 v17, vcc, 0, v5, vcc
	s_waitcnt vmcnt(60)
	v_add_co_u32_e32 v18, vcc, s7, v4
	s_mov_b32 s8, 0x8000
	s_waitcnt vmcnt(59)
	v_addc_co_u32_e32 v19, vcc, 0, v5, vcc
	s_waitcnt vmcnt(58)
	v_add_co_u32_e32 v20, vcc, s8, v4
	s_mov_b32 s9, 0xa000
	s_waitcnt vmcnt(57)
	v_addc_co_u32_e32 v21, vcc, 0, v5, vcc
	s_waitcnt vmcnt(56)
	v_add_co_u32_e32 v22, vcc, s9, v4
	s_mov_b32 s10, 0xc000
	s_waitcnt vmcnt(55)
	v_addc_co_u32_e32 v23, vcc, 0, v5, vcc
	s_waitcnt vmcnt(54)
	v_add_co_u32_e32 v24, vcc, s10, v4
	s_mov_b32 s11, 0xe000
	s_waitcnt vmcnt(53)
	v_addc_co_u32_e32 v25, vcc, 0, v5, vcc
	s_waitcnt vmcnt(52)
	v_add_co_u32_e32 v26, vcc, s11, v4
	s_mov_b32 s20, 0x10000
	s_waitcnt vmcnt(51)
	v_addc_co_u32_e32 v27, vcc, 0, v5, vcc
	s_waitcnt vmcnt(50)
	v_add_co_u32_e32 v28, vcc, s20, v4
	s_mov_b32 s21, 0x12000
	s_waitcnt vmcnt(49)
	v_addc_co_u32_e32 v29, vcc, 0, v5, vcc
	global_load_dword v1, v[6:7], off nt
	global_load_dword v8, v[16:17], off nt
	global_load_dword v9, v[18:19], off nt
	global_load_dword v10, v[20:21], off nt
	global_load_dword v11, v[22:23], off nt
	global_load_dword v12, v[24:25], off nt
	global_load_dword v13, v[26:27], off nt
	global_load_dword v14, v[28:29], off nt
	v_add_co_u32_e32 v6, vcc, s21, v4
	s_mov_b32 s22, 0x14000
	s_nop 0
	v_addc_co_u32_e32 v7, vcc, 0, v5, vcc
	v_add_co_u32_e32 v16, vcc, s22, v4
	s_mov_b32 s23, 0x16000
	s_nop 0
	v_addc_co_u32_e32 v17, vcc, 0, v5, vcc
	v_add_co_u32_e32 v18, vcc, s23, v4
	s_mov_b32 s24, 0x18000
	s_nop 0
	v_addc_co_u32_e32 v19, vcc, 0, v5, vcc
	v_add_co_u32_e32 v20, vcc, s24, v4
	s_mov_b32 s25, 0x1a000
	s_nop 0
	v_addc_co_u32_e32 v21, vcc, 0, v5, vcc
	v_add_co_u32_e32 v22, vcc, s25, v4
	s_mov_b32 s26, 0x1c000
	s_nop 0
	v_addc_co_u32_e32 v23, vcc, 0, v5, vcc
	v_add_co_u32_e32 v24, vcc, s26, v4
	s_mov_b32 s27, 0x1e000
	s_nop 0
	v_addc_co_u32_e32 v25, vcc, 0, v5, vcc
	v_add_co_u32_e32 v26, vcc, s27, v4
	s_mov_b32 s28, 0x20000
	s_nop 0
	v_addc_co_u32_e32 v27, vcc, 0, v5, vcc
	v_add_co_u32_e32 v28, vcc, s28, v4
	s_mov_b32 s29, 0x22000
	s_nop 0
	v_addc_co_u32_e32 v29, vcc, 0, v5, vcc
	global_load_dword v15, v[6:7], off nt
	s_nop 0
	global_load_dword v16, v[16:17], off nt
	s_nop 0
	global_load_dword v17, v[18:19], off nt
	s_nop 0
	global_load_dword v18, v[20:21], off nt
	global_load_dword v19, v[22:23], off nt
	s_nop 0
	global_load_dword v20, v[24:25], off nt
	global_load_dword v21, v[26:27], off nt
	global_load_dword v22, v[28:29], off nt
	v_add_co_u32_e32 v6, vcc, s29, v4
	s_mov_b32 s30, 0x24000
	s_nop 0
	v_addc_co_u32_e32 v7, vcc, 0, v5, vcc
	v_add_co_u32_e32 v24, vcc, s30, v4
	s_mov_b32 s31, 0x26000
	s_nop 0
	v_addc_co_u32_e32 v25, vcc, 0, v5, vcc
	v_add_co_u32_e32 v26, vcc, s31, v4
	s_mov_b32 s33, 0x28000
	s_nop 0
	v_addc_co_u32_e32 v27, vcc, 0, v5, vcc
	v_add_co_u32_e32 v28, vcc, s33, v4
	s_mov_b32 s34, 0x2a000
	s_nop 0
	v_addc_co_u32_e32 v29, vcc, 0, v5, vcc
	s_waitcnt vmcnt(62)
	v_add_co_u32_e32 v30, vcc, s34, v4
	s_mov_b32 s35, 0x2c000
	s_nop 0
	v_addc_co_u32_e32 v31, vcc, 0, v5, vcc
	v_add_co_u32_e32 v32, vcc, s35, v4
	s_mov_b32 s36, 0x2e000
	s_waitcnt vmcnt(61)
	v_addc_co_u32_e32 v33, vcc, 0, v5, vcc
	s_waitcnt vmcnt(60)
	v_add_co_u32_e32 v34, vcc, s36, v4
	s_mov_b32 s37, 0x30000
	s_waitcnt vmcnt(59)
	v_addc_co_u32_e32 v35, vcc, 0, v5, vcc
	s_waitcnt vmcnt(58)
	v_add_co_u32_e32 v36, vcc, s37, v4
	s_mov_b32 s38, 0x32000
	s_waitcnt vmcnt(57)
	v_addc_co_u32_e32 v37, vcc, 0, v5, vcc
	global_load_dword v23, v[6:7], off nt
	s_nop 0
	global_load_dword v24, v[24:25], off nt
	s_nop 0
	global_load_dword v25, v[26:27], off nt
	s_nop 0
	global_load_dword v26, v[28:29], off nt
	global_load_dword v27, v[30:31], off nt
	s_nop 0
	global_load_dword v28, v[32:33], off nt
	global_load_dword v29, v[34:35], off nt
	global_load_dword v30, v[36:37], off nt
	v_add_co_u32_e32 v6, vcc, s38, v4
	s_mov_b32 s39, 0x34000
	s_nop 0
	v_addc_co_u32_e32 v7, vcc, 0, v5, vcc
	v_add_co_u32_e32 v32, vcc, s39, v4
	s_mov_b32 s40, 0x36000
	s_nop 0
	v_addc_co_u32_e32 v33, vcc, 0, v5, vcc
	v_add_co_u32_e32 v34, vcc, s40, v4
	s_mov_b32 s41, 0x38000
	s_nop 0
	v_addc_co_u32_e32 v35, vcc, 0, v5, vcc
	v_add_co_u32_e32 v36, vcc, s41, v4
	s_mov_b32 s42, 0x3a000
	s_nop 0
	v_addc_co_u32_e32 v37, vcc, 0, v5, vcc
	s_waitcnt vmcnt(62)
	v_add_co_u32_e32 v38, vcc, s42, v4
	s_mov_b32 s43, 0x3c000
	s_nop 0
	v_addc_co_u32_e32 v39, vcc, 0, v5, vcc
	v_add_co_u32_e32 v40, vcc, s43, v4
	s_mov_b32 s44, 0x3e000
	s_nop 0
	v_addc_co_u32_e32 v41, vcc, 0, v5, vcc
	v_add_co_u32_e32 v42, vcc, s44, v4
	s_mov_b32 s45, 0x40000
	s_nop 0
	v_addc_co_u32_e32 v43, vcc, 0, v5, vcc
	v_add_co_u32_e32 v44, vcc, s45, v4
	s_mov_b32 s46, 0x42000
	s_nop 0
	v_addc_co_u32_e32 v45, vcc, 0, v5, vcc
	global_load_dword v31, v[6:7], off nt
	s_nop 0
	global_load_dword v32, v[32:33], off nt
	s_nop 0
	global_load_dword v33, v[34:35], off nt
	s_nop 0
	global_load_dword v34, v[36:37], off nt
	global_load_dword v35, v[38:39], off nt
	s_nop 0
	global_load_dword v36, v[40:41], off nt
	global_load_dword v38, v[42:43], off nt
	s_nop 0
	global_load_dword v40, v[44:45], off nt
	v_add_co_u32_e32 v6, vcc, s46, v4
	s_mov_b32 s47, 0x44000
	s_nop 0
	v_addc_co_u32_e32 v7, vcc, 0, v5, vcc
	v_add_co_u32_e32 v42, vcc, s47, v4
	s_mov_b32 s48, 0x46000
	s_nop 0
	v_addc_co_u32_e32 v43, vcc, 0, v5, vcc
	v_add_co_u32_e32 v48, vcc, s48, v4
	s_mov_b32 s49, 0x48000
	s_nop 0
	v_addc_co_u32_e32 v49, vcc, 0, v5, vcc
	v_add_co_u32_e32 v50, vcc, s49, v4
	s_mov_b32 s50, 0x4a000
	s_waitcnt vmcnt(62)
	v_addc_co_u32_e32 v51, vcc, 0, v5, vcc
	v_add_co_u32_e32 v52, vcc, s50, v4
	s_mov_b32 s51, 0x4c000
	s_nop 0
	v_addc_co_u32_e32 v53, vcc, 0, v5, vcc
	v_add_co_u32_e32 v54, vcc, s51, v4
	s_mov_b32 s52, 0x4e000
	s_nop 0
	v_addc_co_u32_e32 v55, vcc, 0, v5, vcc
	v_add_co_u32_e32 v56, vcc, s52, v4
	s_mov_b32 s53, 0x50000
	s_nop 0
	v_addc_co_u32_e32 v57, vcc, 0, v5, vcc
	v_add_co_u32_e32 v58, vcc, s53, v4
	s_mov_b32 s54, 0x52000
	s_waitcnt vmcnt(61)
	v_addc_co_u32_e32 v59, vcc, 0, v5, vcc
	global_load_dword v45, v[6:7], off nt
	global_load_dword v46, v[42:43], off nt
	global_load_dword v47, v[48:49], off nt
	s_nop 0
	global_load_dword v48, v[50:51], off nt
	global_load_dword v49, v[52:53], off nt
	s_nop 0
	global_load_dword v50, v[54:55], off nt
	global_load_dword v51, v[56:57], off nt
	global_load_dword v52, v[58:59], off nt
	v_add_co_u32_e32 v6, vcc, s54, v4
	s_mov_b32 s55, 0x54000
	s_nop 0
	v_addc_co_u32_e32 v7, vcc, 0, v5, vcc
	v_add_co_u32_e32 v42, vcc, s55, v4
	s_mov_b32 s56, 0x56000
	s_nop 0
	v_addc_co_u32_e32 v43, vcc, 0, v5, vcc
	v_add_co_u32_e32 v56, vcc, s56, v4
	s_mov_b32 s57, 0x58000
	s_nop 0
	v_addc_co_u32_e32 v57, vcc, 0, v5, vcc
	v_add_co_u32_e32 v58, vcc, s57, v4
	s_mov_b32 s58, 0x5a000
	s_nop 0
	v_addc_co_u32_e32 v59, vcc, 0, v5, vcc
	s_waitcnt vmcnt(62)
	v_add_co_u32_e32 v60, vcc, s58, v4
	s_mov_b32 s59, 0x5c000
	s_nop 0
	v_addc_co_u32_e32 v61, vcc, 0, v5, vcc
	v_add_co_u32_e32 v62, vcc, s59, v4
	s_mov_b32 s60, 0x5e000
	s_nop 0
	v_addc_co_u32_e32 v63, vcc, 0, v5, vcc
	v_add_co_u32_e32 v64, vcc, s60, v4
	s_mov_b32 s61, 0x60000
	s_nop 0
	v_addc_co_u32_e32 v65, vcc, 0, v5, vcc
	v_add_co_u32_e32 v66, vcc, s61, v4
	s_mov_b32 s62, 0x62000
	s_waitcnt vmcnt(61)
	v_addc_co_u32_e32 v67, vcc, 0, v5, vcc
	global_load_dword v53, v[6:7], off nt
	global_load_dword v54, v[42:43], off nt
	global_load_dword v55, v[56:57], off nt
	s_nop 0
	global_load_dword v56, v[58:59], off nt
	global_load_dword v57, v[60:61], off nt
	s_nop 0
	global_load_dword v58, v[62:63], off nt
	global_load_dword v59, v[64:65], off nt
	global_load_dword v60, v[66:67], off nt
	v_add_co_u32_e32 v6, vcc, s62, v4
	s_mov_b32 s63, 0x64000
	s_nop 0
	v_addc_co_u32_e32 v7, vcc, 0, v5, vcc
	v_add_co_u32_e32 v42, vcc, s63, v4
	s_mov_b32 s64, 0x66000
	s_nop 0
	v_addc_co_u32_e32 v43, vcc, 0, v5, vcc
	v_add_co_u32_e32 v64, vcc, s64, v4
	s_mov_b32 s65, 0x68000
	s_nop 0
	v_addc_co_u32_e32 v65, vcc, 0, v5, vcc
	v_add_co_u32_e32 v66, vcc, s65, v4
	s_mov_b32 s66, 0x6a000
	s_nop 0
	v_addc_co_u32_e32 v67, vcc, 0, v5, vcc
	s_waitcnt vmcnt(62)
	v_add_co_u32_e32 v68, vcc, s66, v4
	s_mov_b32 s67, 0x6c000
	s_nop 0
	v_addc_co_u32_e32 v69, vcc, 0, v5, vcc
	v_add_co_u32_e32 v70, vcc, s67, v4
	s_mov_b32 s68, 0x6e000
	s_nop 0
	v_addc_co_u32_e32 v71, vcc, 0, v5, vcc
	v_add_co_u32_e32 v72, vcc, s68, v4
	s_mov_b32 s69, 0x70000
	s_waitcnt vmcnt(60)
	v_addc_co_u32_e32 v73, vcc, 0, v5, vcc
	s_waitcnt vmcnt(59)
	v_add_co_u32_e32 v74, vcc, s69, v4
	s_mov_b32 s70, 0x72000
	s_waitcnt vmcnt(58)
	v_addc_co_u32_e32 v75, vcc, 0, v5, vcc
	global_load_dword v61, v[6:7], off nt
	global_load_dword v62, v[42:43], off nt
	global_load_dword v63, v[64:65], off nt
	s_nop 0
	global_load_dword v64, v[66:67], off nt
	global_load_dword v65, v[68:69], off nt
	s_nop 0
	global_load_dword v66, v[70:71], off nt
	global_load_dword v67, v[72:73], off nt
	global_load_dword v68, v[74:75], off nt
	v_add_co_u32_e32 v42, vcc, s70, v4
	s_mov_b32 s71, 0x74000
	s_nop 0
	v_addc_co_u32_e32 v43, vcc, 0, v5, vcc
	v_add_co_u32_e32 v70, vcc, s71, v4
	s_mov_b32 s72, 0x76000
	s_nop 0
	v_addc_co_u32_e32 v71, vcc, 0, v5, vcc
	v_add_co_u32_e32 v72, vcc, s72, v4
	s_mov_b32 s2, 0x78000
	s_nop 0
	v_addc_co_u32_e32 v73, vcc, 0, v5, vcc
	v_add_co_u32_e32 v74, vcc, s2, v4
	s_mov_b32 s2, 0x7a000
	s_nop 0
	v_addc_co_u32_e32 v75, vcc, 0, v5, vcc
	v_add_co_u32_e32 v76, vcc, s2, v4
	s_mov_b32 s2, 0x7c000
	s_waitcnt vmcnt(62)
	v_addc_co_u32_e32 v77, vcc, 0, v5, vcc
	v_add_co_u32_e32 v78, vcc, s2, v4
	s_mov_b32 s2, 0x7e000
	s_nop 0
	v_addc_co_u32_e32 v79, vcc, 0, v5, vcc
	v_add_co_u32_e32 v4, vcc, s2, v4
	v_add_u32_e32 v37, s6, v2
	s_nop 0
	v_addc_co_u32_e32 v5, vcc, 0, v5, vcc
	global_load_dword v6, v2, s[0:1] nt
	global_load_dword v7, v[42:43], off nt
	global_load_dword v69, v[70:71], off nt
	s_nop 0
	global_load_dword v70, v[72:73], off nt
	global_load_dword v71, v[74:75], off nt
	s_nop 0
	global_load_dword v72, v[76:77], off nt
	global_load_dword v73, v[78:79], off nt
	global_load_dword v74, v[4:5], off nt
	v_lshlrev_b32_e32 v2, 4, v0
	v_and_b32_e32 v2, 48, v2
	v_lshrrev_b32_e32 v39, 2, v198
	v_mul_u32_u24_e32 v41, 0x104, v2
	v_lshl_add_u64 v[4:5], s[82:83], 0, v[2:3]
	s_mov_b64 s[0:1], 0x3700000
	v_and_b32_e32 v2, 60, v198
	s_mov_b32 s74, s88
	v_lshl_add_u64 v[4:5], v[4:5], 0, s[0:1]
	v_add3_u32 v41, s6, v41, v2
	v_or_b32_e32 v42, 16, v39
	v_or_b32_e32 v43, 32, v39
	v_or_b32_e32 v44, 48, v39
	v_lshlrev_b32_e32 v2, 2, v198
	s_branch .LBB0_215

.LBB0_215:
	s_waitcnt vmcnt(7)
	v_mul_f32_e32 v75, 0x42800000, v6
	v_mul_f32_e32 v76, 0x42800000, v1
	ds_write2_b32 v37, v75, v76 offset1:65
	v_mul_f32_e32 v75, 0x42800000, v8
	v_mul_f32_e32 v76, 0x42800000, v9
	ds_write2_b32 v37, v75, v76 offset0:130 offset1:195
	v_mul_f32_e32 v75, 0x42800000, v10
	v_mul_f32_e32 v76, 0x42800000, v11
	v_add_u32_e32 v77, 0x400, v37
	ds_write2_b32 v77, v75, v76 offset0:4 offset1:69
	v_mul_f32_e32 v75, 0x42800000, v12
	v_mul_f32_e32 v76, 0x42800000, v13
	ds_write2_b32 v77, v75, v76 offset0:134 offset1:199
	v_mul_f32_e32 v75, 0x42800000, v14
	v_mul_f32_e32 v76, 0x42800000, v15
	v_add_u32_e32 v77, 0x800, v37
	ds_write2_b32 v77, v75, v76 offset0:8 offset1:73
	v_mul_f32_e32 v75, 0x42800000, v16
	v_mul_f32_e32 v76, 0x42800000, v17
	ds_write2_b32 v77, v75, v76 offset0:138 offset1:203
	v_mul_f32_e32 v75, 0x42800000, v18
	v_mul_f32_e32 v76, 0x42800000, v19
	v_add_u32_e32 v77, 0xc00, v37
	ds_write2_b32 v77, v75, v76 offset0:12 offset1:77
	v_mul_f32_e32 v75, 0x42800000, v20
	v_mul_f32_e32 v76, 0x42800000, v21
	ds_write2_b32 v77, v75, v76 offset0:142 offset1:207
	v_mul_f32_e32 v75, 0x42800000, v22
	v_mul_f32_e32 v76, 0x42800000, v23
	v_add_u32_e32 v77, 0x1000, v37
	ds_write2_b32 v77, v75, v76 offset0:16 offset1:81
	v_mul_f32_e32 v75, 0x42800000, v24
	v_mul_f32_e32 v76, 0x42800000, v25
	ds_write2_b32 v77, v75, v76 offset0:146 offset1:211
	v_mul_f32_e32 v75, 0x42800000, v26
	v_mul_f32_e32 v76, 0x42800000, v27
	v_add_u32_e32 v77, 0x1400, v37
	ds_write2_b32 v77, v75, v76 offset0:20 offset1:85
	v_mul_f32_e32 v75, 0x42800000, v28
	v_mul_f32_e32 v76, 0x42800000, v29
	ds_write2_b32 v77, v75, v76 offset0:150 offset1:215
	v_mul_f32_e32 v75, 0x42800000, v30
	v_mul_f32_e32 v76, 0x42800000, v31
	v_add_u32_e32 v77, 0x1800, v37
	ds_write2_b32 v77, v75, v76 offset0:24 offset1:89
	v_mul_f32_e32 v75, 0x42800000, v32
	v_mul_f32_e32 v76, 0x42800000, v33
	ds_write2_b32 v77, v75, v76 offset0:154 offset1:219
	v_mul_f32_e32 v75, 0x42800000, v34
	v_mul_f32_e32 v76, 0x42800000, v35
	v_add_u32_e32 v77, 0x1c00, v37
	ds_write2_b32 v77, v75, v76 offset0:28 offset1:93
	v_mul_f32_e32 v75, 0x42800000, v36
	v_mul_f32_e32 v76, 0x42800000, v38
	ds_write2_b32 v77, v75, v76 offset0:158 offset1:223
	v_mul_f32_e32 v75, 0x42800000, v40
	v_mul_f32_e32 v76, 0x42800000, v45
	v_add_u32_e32 v77, 0x2000, v37
	ds_write2_b32 v77, v75, v76 offset0:32 offset1:97
	v_mul_f32_e32 v75, 0x42800000, v46
	v_mul_f32_e32 v76, 0x42800000, v47
	ds_write2_b32 v77, v75, v76 offset0:162 offset1:227
	v_mul_f32_e32 v75, 0x42800000, v48
	v_mul_f32_e32 v76, 0x42800000, v49
	v_add_u32_e32 v77, 0x2400, v37
	ds_write2_b32 v77, v75, v76 offset0:36 offset1:101
	v_mul_f32_e32 v75, 0x42800000, v50
	v_mul_f32_e32 v76, 0x42800000, v51
	ds_write2_b32 v77, v75, v76 offset0:166 offset1:231
	v_mul_f32_e32 v75, 0x42800000, v52
	v_mul_f32_e32 v76, 0x42800000, v53
	v_add_u32_e32 v77, 0x2800, v37
	ds_write2_b32 v77, v75, v76 offset0:40 offset1:105
	v_mul_f32_e32 v75, 0x42800000, v54
	v_mul_f32_e32 v76, 0x42800000, v55
	ds_write2_b32 v77, v75, v76 offset0:170 offset1:235
	v_mul_f32_e32 v75, 0x42800000, v56
	v_mul_f32_e32 v76, 0x42800000, v57
	v_add_u32_e32 v77, 0x2c00, v37
	ds_write2_b32 v77, v75, v76 offset0:44 offset1:109
	v_mul_f32_e32 v75, 0x42800000, v58
	v_mul_f32_e32 v76, 0x42800000, v59
	ds_write2_b32 v77, v75, v76 offset0:174 offset1:239
	v_mul_f32_e32 v75, 0x42800000, v60
	v_mul_f32_e32 v76, 0x42800000, v61
	v_add_u32_e32 v77, 0x3000, v37
	ds_write2_b32 v77, v75, v76 offset0:48 offset1:113
	v_mul_f32_e32 v75, 0x42800000, v62
	v_mul_f32_e32 v76, 0x42800000, v63
	ds_write2_b32 v77, v75, v76 offset0:178 offset1:243
	v_mul_f32_e32 v75, 0x42800000, v64
	v_mul_f32_e32 v76, 0x42800000, v65
	v_add_u32_e32 v77, 0x3400, v37
	ds_write2_b32 v77, v75, v76 offset0:52 offset1:117
	v_mul_f32_e32 v75, 0x42800000, v66
	v_mul_f32_e32 v76, 0x42800000, v67
	ds_write2_b32 v77, v75, v76 offset0:182 offset1:247
	v_mul_f32_e32 v75, 0x42800000, v68
	s_waitcnt vmcnt(6)
	v_mul_f32_e32 v76, 0x42800000, v7
	v_add_u32_e32 v77, 0x3800, v37
	ds_write2_b32 v77, v75, v76 offset0:56 offset1:121
	s_waitcnt vmcnt(5)
	v_mul_f32_e32 v75, 0x42800000, v69
	s_waitcnt vmcnt(4)
	v_mul_f32_e32 v76, 0x42800000, v70
	ds_write2_b32 v77, v75, v76 offset0:186 offset1:251
	s_waitcnt vmcnt(3)
	v_mul_f32_e32 v75, 0x42800000, v71
	s_waitcnt vmcnt(2)
	v_mul_f32_e32 v76, 0x42800000, v72
	v_add_u32_e32 v77, 0x3c00, v37
	ds_write2_b32 v77, v75, v76 offset0:60 offset1:125
	s_waitcnt vmcnt(1)
	v_mul_f32_e32 v75, 0x42800000, v73
	s_waitcnt vmcnt(0)
	v_mul_f32_e32 v76, 0x42800000, v74
	ds_write2_b32 v77, v75, v76 offset0:190 offset1:255
	s_waitcnt lgkmcnt(0)
	s_add_i32 s73, s74, s85
	s_cmpk_gt_i32 s73, 0x3ff
	s_cselect_b64 s[0:1], -1, 0
	s_and_b64 vcc, exec, s[0:1]
	s_cbranch_vccnz .LBB0_214
	s_ashr_i32 s2, s73, 31
	s_lshr_b32 s2, s2, 22
	s_add_i32 s2, s73, s2
	s_and_b32 s2, s2, 0xfc00
	s_sub_i32 s75, s73, s2
	s_sext_i32_i16 s2, s75
	s_bfe_u32 s2, s2, 0x5001a
	s_add_i32 s76, s75, s2
	s_sext_i32_i16 s2, s76
	s_lshl_b32 s2, s2, 1
	s_andn2_b32 s2, s2, 63
	s_ashr_i32 s3, s2, 31
	s_lshl_b64 s[2:3], s[2:3], 13
	s_add_u32 s77, s18, s2
	s_addc_u32 s78, s19, s3
	s_and_b32 s2, s76, 0xffe0
	s_sub_i32 s2, s75, s2
	s_sext_i32_i16 s2, s2
	s_lshl_b32 s2, s2, 6
	s_ashr_i32 s3, s2, 31
	s_lshl_b64 s[2:3], s[2:3], 2
	s_add_u32 s2, s77, s2
	s_addc_u32 s3, s78, s3
	v_lshl_add_u64 v[6:7], s[2:3], 0, v[2:3]
	v_add_co_u32_e32 v8, vcc, s4, v6
	s_nop 1
	v_addc_co_u32_e32 v9, vcc, 0, v7, vcc
	v_add_co_u32_e32 v10, vcc, s5, v6
	s_nop 1
	v_addc_co_u32_e32 v11, vcc, 0, v7, vcc
	v_add_co_u32_e32 v12, vcc, s7, v6
	s_nop 1
	v_addc_co_u32_e32 v13, vcc, 0, v7, vcc
	v_add_co_u32_e32 v14, vcc, s8, v6
	s_nop 1
	v_addc_co_u32_e32 v15, vcc, 0, v7, vcc
	v_add_co_u32_e32 v16, vcc, s9, v6
	s_nop 1
	v_addc_co_u32_e32 v17, vcc, 0, v7, vcc
	v_add_co_u32_e32 v18, vcc, s10, v6
	s_nop 1
	v_addc_co_u32_e32 v19, vcc, 0, v7, vcc
	v_add_co_u32_e32 v20, vcc, s11, v6
	s_nop 1
	v_addc_co_u32_e32 v21, vcc, 0, v7, vcc
	v_add_co_u32_e32 v22, vcc, s20, v6
	s_nop 1
	v_addc_co_u32_e32 v23, vcc, 0, v7, vcc
	global_load_dword v1, v[8:9], off nt
	s_nop 0
	global_load_dword v8, v[10:11], off nt
	global_load_dword v9, v[12:13], off nt
	s_nop 0
	global_load_dword v10, v[14:15], off nt
	global_load_dword v11, v[16:17], off nt
	global_load_dword v12, v[18:19], off nt
	global_load_dword v13, v[20:21], off nt
	s_nop 0
	global_load_dword v14, v[22:23], off nt
	v_add_co_u32_e32 v16, vcc, s21, v6
	s_nop 1
	v_addc_co_u32_e32 v17, vcc, 0, v7, vcc
	v_add_co_u32_e32 v18, vcc, s22, v6
	s_nop 1
	v_addc_co_u32_e32 v19, vcc, 0, v7, vcc
	v_add_co_u32_e32 v20, vcc, s23, v6
	s_nop 1
	v_addc_co_u32_e32 v21, vcc, 0, v7, vcc
	v_add_co_u32_e32 v22, vcc, s24, v6
	s_nop 1
	v_addc_co_u32_e32 v23, vcc, 0, v7, vcc
	v_add_co_u32_e32 v24, vcc, s25, v6
	s_nop 1
	v_addc_co_u32_e32 v25, vcc, 0, v7, vcc
	v_add_co_u32_e32 v26, vcc, s26, v6
	s_nop 1
	v_addc_co_u32_e32 v27, vcc, 0, v7, vcc
	v_add_co_u32_e32 v28, vcc, s27, v6
	s_nop 1
	v_addc_co_u32_e32 v29, vcc, 0, v7, vcc
	v_add_co_u32_e32 v30, vcc, s28, v6
	s_nop 1
	v_addc_co_u32_e32 v31, vcc, 0, v7, vcc
	global_load_dword v15, v[16:17], off nt
	s_nop 0
	global_load_dword v16, v[18:19], off nt
	global_load_dword v17, v[20:21], off nt
	s_nop 0
	global_load_dword v18, v[22:23], off nt
	global_load_dword v19, v[24:25], off nt
	global_load_dword v20, v[26:27], off nt
	global_load_dword v21, v[28:29], off nt
	s_nop 0
	global_load_dword v22, v[30:31], off nt
	v_add_co_u32_e32 v24, vcc, s29, v6
	s_nop 1
	v_addc_co_u32_e32 v25, vcc, 0, v7, vcc
	v_add_co_u32_e32 v26, vcc, s30, v6
	s_nop 1
	v_addc_co_u32_e32 v27, vcc, 0, v7, vcc
	v_add_co_u32_e32 v28, vcc, s31, v6
	s_nop 1
	v_addc_co_u32_e32 v29, vcc, 0, v7, vcc
	v_add_co_u32_e32 v30, vcc, s33, v6
	s_nop 1
	v_addc_co_u32_e32 v31, vcc, 0, v7, vcc
	v_add_co_u32_e32 v32, vcc, s34, v6
	s_nop 1
	v_addc_co_u32_e32 v33, vcc, 0, v7, vcc
	v_add_co_u32_e32 v34, vcc, s35, v6
	s_nop 1
	v_addc_co_u32_e32 v35, vcc, 0, v7, vcc
	v_add_co_u32_e32 v46, vcc, s36, v6
	s_nop 1
	v_addc_co_u32_e32 v47, vcc, 0, v7, vcc
	v_add_co_u32_e32 v48, vcc, s37, v6
	s_nop 1
	v_addc_co_u32_e32 v49, vcc, 0, v7, vcc
	global_load_dword v23, v[24:25], off nt
	s_nop 0
	global_load_dword v24, v[26:27], off nt
	global_load_dword v25, v[28:29], off nt
	s_nop 0
	global_load_dword v26, v[30:31], off nt
	global_load_dword v27, v[32:33], off nt
	global_load_dword v28, v[34:35], off nt
	global_load_dword v29, v[46:47], off nt
	s_nop 0
	global_load_dword v30, v[48:49], off nt
	v_add_co_u32_e32 v32, vcc, s38, v6
	s_nop 1
	v_addc_co_u32_e32 v33, vcc, 0, v7, vcc
	v_add_co_u32_e32 v34, vcc, s39, v6
	s_nop 1
	v_addc_co_u32_e32 v35, vcc, 0, v7, vcc
	v_add_co_u32_e32 v46, vcc, s40, v6
	s_nop 1
	v_addc_co_u32_e32 v47, vcc, 0, v7, vcc
	v_add_co_u32_e32 v48, vcc, s41, v6
	s_nop 1
	v_addc_co_u32_e32 v49, vcc, 0, v7, vcc
	v_add_co_u32_e32 v50, vcc, s42, v6
	s_nop 1
	v_addc_co_u32_e32 v51, vcc, 0, v7, vcc
	v_add_co_u32_e32 v52, vcc, s43, v6
	s_nop 1
	v_addc_co_u32_e32 v53, vcc, 0, v7, vcc
	v_add_co_u32_e32 v54, vcc, s44, v6
	s_nop 1
	v_addc_co_u32_e32 v55, vcc, 0, v7, vcc
	v_add_co_u32_e32 v56, vcc, s45, v6
	s_nop 1
	v_addc_co_u32_e32 v57, vcc, 0, v7, vcc
	global_load_dword v31, v[32:33], off nt
	s_nop 0
	global_load_dword v32, v[34:35], off nt
	global_load_dword v33, v[46:47], off nt
	s_nop 0
	global_load_dword v34, v[48:49], off nt
	global_load_dword v35, v[50:51], off nt
	global_load_dword v36, v[52:53], off nt
	global_load_dword v38, v[54:55], off nt
	global_load_dword v40, v[56:57], off nt
	v_add_co_u32_e32 v46, vcc, s46, v6
	s_nop 1
	v_addc_co_u32_e32 v47, vcc, 0, v7, vcc
	v_add_co_u32_e32 v48, vcc, s47, v6
	s_nop 1
	v_addc_co_u32_e32 v49, vcc, 0, v7, vcc
	v_add_co_u32_e32 v50, vcc, s48, v6
	s_nop 1
	v_addc_co_u32_e32 v51, vcc, 0, v7, vcc
	v_add_co_u32_e32 v52, vcc, s49, v6
	s_nop 1
	v_addc_co_u32_e32 v53, vcc, 0, v7, vcc
	v_add_co_u32_e32 v54, vcc, s50, v6
	s_nop 1
	v_addc_co_u32_e32 v55, vcc, 0, v7, vcc
	v_add_co_u32_e32 v56, vcc, s51, v6
	s_nop 1
	v_addc_co_u32_e32 v57, vcc, 0, v7, vcc
	v_add_co_u32_e32 v58, vcc, s52, v6
	s_nop 1
	v_addc_co_u32_e32 v59, vcc, 0, v7, vcc
	v_add_co_u32_e32 v60, vcc, s53, v6
	s_nop 1
	v_addc_co_u32_e32 v61, vcc, 0, v7, vcc
	global_load_dword v45, v[46:47], off nt
	s_nop 0
	global_load_dword v46, v[48:49], off nt
	global_load_dword v47, v[50:51], off nt
	s_nop 0
	global_load_dword v48, v[52:53], off nt
	global_load_dword v49, v[54:55], off nt
	global_load_dword v50, v[56:57], off nt
	global_load_dword v51, v[58:59], off nt
	s_nop 0
	global_load_dword v52, v[60:61], off nt
	v_add_co_u32_e32 v54, vcc, s54, v6
	s_nop 1
	v_addc_co_u32_e32 v55, vcc, 0, v7, vcc
	v_add_co_u32_e32 v56, vcc, s55, v6
	s_nop 1
	v_addc_co_u32_e32 v57, vcc, 0, v7, vcc
	v_add_co_u32_e32 v58, vcc, s56, v6
	s_nop 1
	v_addc_co_u32_e32 v59, vcc, 0, v7, vcc
	v_add_co_u32_e32 v60, vcc, s57, v6
	s_nop 1
	v_addc_co_u32_e32 v61, vcc, 0, v7, vcc
	v_add_co_u32_e32 v62, vcc, s58, v6
	s_nop 1
	v_addc_co_u32_e32 v63, vcc, 0, v7, vcc
	v_add_co_u32_e32 v64, vcc, s59, v6
	s_nop 1
	v_addc_co_u32_e32 v65, vcc, 0, v7, vcc
	v_add_co_u32_e32 v66, vcc, s60, v6
	s_nop 1
	v_addc_co_u32_e32 v67, vcc, 0, v7, vcc
	v_add_co_u32_e32 v68, vcc, s61, v6
	s_nop 1
	v_addc_co_u32_e32 v69, vcc, 0, v7, vcc
	global_load_dword v53, v[54:55], off nt
	s_nop 0
	global_load_dword v54, v[56:57], off nt
	global_load_dword v55, v[58:59], off nt
	s_nop 0
	global_load_dword v56, v[60:61], off nt
	global_load_dword v57, v[62:63], off nt
	global_load_dword v58, v[64:65], off nt
	global_load_dword v59, v[66:67], off nt
	s_nop 0
	global_load_dword v60, v[68:69], off nt
	v_add_co_u32_e32 v62, vcc, s62, v6
	s_nop 1
	v_addc_co_u32_e32 v63, vcc, 0, v7, vcc
	v_add_co_u32_e32 v64, vcc, s63, v6
	s_nop 1
	v_addc_co_u32_e32 v65, vcc, 0, v7, vcc
	v_add_co_u32_e32 v66, vcc, s64, v6
	s_nop 1
	v_addc_co_u32_e32 v67, vcc, 0, v7, vcc
	v_add_co_u32_e32 v68, vcc, s65, v6
	s_nop 1
	v_addc_co_u32_e32 v69, vcc, 0, v7, vcc
	v_add_co_u32_e32 v70, vcc, s66, v6
	s_nop 1
	v_addc_co_u32_e32 v71, vcc, 0, v7, vcc
	v_add_co_u32_e32 v72, vcc, s67, v6
	s_nop 1
	v_addc_co_u32_e32 v73, vcc, 0, v7, vcc
	v_add_co_u32_e32 v74, vcc, s68, v6
	s_nop 1
	v_addc_co_u32_e32 v75, vcc, 0, v7, vcc
	v_add_co_u32_e32 v76, vcc, s69, v6
	s_nop 1
	v_addc_co_u32_e32 v77, vcc, 0, v7, vcc
	global_load_dword v61, v[62:63], off nt
	s_nop 0
	global_load_dword v62, v[64:65], off nt
	global_load_dword v63, v[66:67], off nt
	s_nop 0
	global_load_dword v64, v[68:69], off nt
	global_load_dword v65, v[70:71], off nt
	global_load_dword v66, v[72:73], off nt
	global_load_dword v67, v[74:75], off nt
	s_nop 0
	global_load_dword v68, v[76:77], off nt
	v_add_co_u32_e32 v70, vcc, s70, v6
	s_nop 1
	v_addc_co_u32_e32 v71, vcc, 0, v7, vcc
	v_add_co_u32_e32 v72, vcc, s71, v6
	s_nop 1
	v_addc_co_u32_e32 v73, vcc, 0, v7, vcc
	v_add_co_u32_e32 v74, vcc, s72, v6
	s_nop 1
	v_addc_co_u32_e32 v75, vcc, 0, v7, vcc
	v_add_co_u32_e32 v76, vcc, 0x78000, v6
	s_nop 1
	v_addc_co_u32_e32 v77, vcc, 0, v7, vcc
	v_add_co_u32_e32 v78, vcc, 0x7a000, v6
	s_nop 1
	v_addc_co_u32_e32 v79, vcc, 0, v7, vcc
	v_add_co_u32_e32 v80, vcc, 0x7c000, v6
	s_nop 1
	v_addc_co_u32_e32 v81, vcc, 0, v7, vcc
	v_add_co_u32_e32 v82, vcc, 0x7e000, v6
	s_nop 1
	v_addc_co_u32_e32 v83, vcc, 0, v7, vcc
	global_load_dword v6, v2, s[2:3] nt
	global_load_dword v7, v[70:71], off nt
	global_load_dword v69, v[72:73], off nt
	s_nop 0
	global_load_dword v70, v[74:75], off nt
	global_load_dword v71, v[76:77], off nt
	global_load_dword v72, v[78:79], off nt
	global_load_dword v73, v[80:81], off nt
	s_nop 0
	global_load_dword v74, v[82:83], off nt
	s_branch .LBB0_214
